# GEMM K-loops: removed the per-phase s_setprio 1/0 toggles (304) and 113 s_waitcnt lgkmcnt(0) that directly repeat an executed one; on top of v39
# speedup vs baseline: 1.0042x; 1.0042x over previous
.LBB0_451:
	ds_read_b128 v[146:149], v141
	ds_read_b128 v[150:153], v141 offset:1024
	ds_read_b128 v[154:157], v141 offset:2048
	ds_read_b128 v[158:161], v141 offset:3072
	s_add_i32 s48, s45, 0x80
	s_cmp_eq_u32 s28, s47
	s_cselect_b32 s50, s14, s48
	s_cselect_b32 s48, s15, s46
	s_or_b32 s49, s50, 0x80
	s_mov_b32 m0, s29
	v_add_u32_e32 v194, s45, v137
	ds_read_b128 v[162:165], v142
	ds_read_b128 v[166:169], v142 offset:1024
	ds_read_b128 v[170:173], v142 offset:2048
	ds_read_b128 v[174:177], v142 offset:3072
	ds_read_b128 v[178:181], v142 offset:4096
	ds_read_b128 v[182:185], v142 offset:5120
	ds_read_b128 v[186:189], v142 offset:6144
	ds_read_b128 v[190:193], v142 offset:7168
	global_load_lds_dwordx4 v194, s[4:5]
	v_add_u32_e32 v194, s45, v138
	s_mov_b32 m0, s30
	s_nop 0
	global_load_lds_dwordx4 v194, s[4:5]
	s_waitcnt lgkmcnt(8)
	s_barrier
	s_waitcnt lgkmcnt(0)


	v_mfma_f32_16x16x32_bf16 v[122:125], v[146:149], v[162:165], v[122:125]
	v_mfma_f32_16x16x32_bf16 v[126:129], v[154:157], v[162:165], v[126:129]
	v_mfma_f32_16x16x32_bf16 v[110:113], v[146:149], v[170:173], v[110:113]
	v_mfma_f32_16x16x32_bf16 v[106:109], v[154:157], v[170:173], v[106:109]
	v_mfma_f32_16x16x32_bf16 v[94:97], v[146:149], v[178:181], v[94:97]
	v_mfma_f32_16x16x32_bf16 v[90:93], v[154:157], v[178:181], v[90:93]
	v_mfma_f32_16x16x32_bf16 v[78:81], v[146:149], v[186:189], v[78:81]
	v_mfma_f32_16x16x32_bf16 v[74:77], v[154:157], v[186:189], v[74:77]
	v_mfma_f32_16x16x32_bf16 v[122:125], v[150:153], v[166:169], v[122:125]
	v_mfma_f32_16x16x32_bf16 v[126:129], v[158:161], v[166:169], v[126:129]
	v_mfma_f32_16x16x32_bf16 v[110:113], v[150:153], v[174:177], v[110:113]
	v_mfma_f32_16x16x32_bf16 v[106:109], v[158:161], v[174:177], v[106:109]
	v_mfma_f32_16x16x32_bf16 v[94:97], v[150:153], v[182:185], v[94:97]
	v_mfma_f32_16x16x32_bf16 v[90:93], v[158:161], v[182:185], v[90:93]
	v_mfma_f32_16x16x32_bf16 v[78:81], v[150:153], v[190:193], v[78:81]
	v_mfma_f32_16x16x32_bf16 v[74:77], v[158:161], v[190:193], v[74:77]

	s_barrier
	s_mov_b32 m0, s33
	v_add_u32_e32 v210, s48, v1
	ds_read_b128 v[194:197], v143
	ds_read_b128 v[198:201], v143 offset:1024
	ds_read_b128 v[202:205], v143 offset:2048
	ds_read_b128 v[206:209], v143 offset:3072
	global_load_lds_dwordx4 v210, s[6:7]
	v_add_u32_e32 v210, s48, v134
	s_mov_b32 m0, s34
	s_nop 0
	global_load_lds_dwordx4 v210, s[6:7]
	s_barrier
	s_waitcnt lgkmcnt(0)


	v_mfma_f32_16x16x32_bf16 v[118:121], v[194:197], v[162:165], v[118:121]
	v_mfma_f32_16x16x32_bf16 v[114:117], v[202:205], v[162:165], v[114:117]
	v_mfma_f32_16x16x32_bf16 v[102:105], v[194:197], v[170:173], v[102:105]
	v_mfma_f32_16x16x32_bf16 v[98:101], v[202:205], v[170:173], v[98:101]
	v_mfma_f32_16x16x32_bf16 v[86:89], v[194:197], v[178:181], v[86:89]
	v_mfma_f32_16x16x32_bf16 v[82:85], v[202:205], v[178:181], v[82:85]
	v_mfma_f32_16x16x32_bf16 v[70:73], v[194:197], v[186:189], v[70:73]
	v_mfma_f32_16x16x32_bf16 v[66:69], v[202:205], v[186:189], v[66:69]
	v_mfma_f32_16x16x32_bf16 v[118:121], v[198:201], v[166:169], v[118:121]
	v_mfma_f32_16x16x32_bf16 v[114:117], v[206:209], v[166:169], v[114:117]
	v_mfma_f32_16x16x32_bf16 v[102:105], v[198:201], v[174:177], v[102:105]
	v_mfma_f32_16x16x32_bf16 v[98:101], v[206:209], v[174:177], v[98:101]
	v_mfma_f32_16x16x32_bf16 v[86:89], v[198:201], v[182:185], v[86:89]
	v_mfma_f32_16x16x32_bf16 v[82:85], v[206:209], v[182:185], v[82:85]
	v_mfma_f32_16x16x32_bf16 v[70:73], v[198:201], v[190:193], v[70:73]
	v_mfma_f32_16x16x32_bf16 v[66:69], v[206:209], v[190:193], v[66:69]

	s_mov_b32 m0, s19
	v_add_u32_e32 v210, s50, v135
	s_barrier
	ds_read_b128 v[162:165], v142 offset:16384
	ds_read_b128 v[166:169], v142 offset:17408
	ds_read_b128 v[170:173], v142 offset:18432
	ds_read_b128 v[174:177], v142 offset:19456
	ds_read_b128 v[178:181], v142 offset:20480
	ds_read_b128 v[182:185], v142 offset:21504
	ds_read_b128 v[186:189], v142 offset:22528
	ds_read_b128 v[190:193], v142 offset:23552
	global_load_lds_dwordx4 v210, s[4:5]
	v_add_u32_e32 v210, s50, v136
	s_mov_b32 m0, s20
	s_nop 0
	global_load_lds_dwordx4 v210, s[4:5]
	s_barrier
	s_waitcnt lgkmcnt(0)


	v_mfma_f32_16x16x32_bf16 v[62:65], v[146:149], v[162:165], v[62:65]
	v_mfma_f32_16x16x32_bf16 v[58:61], v[154:157], v[162:165], v[58:61]
	v_mfma_f32_16x16x32_bf16 v[46:49], v[146:149], v[170:173], v[46:49]
	v_mfma_f32_16x16x32_bf16 v[42:45], v[154:157], v[170:173], v[42:45]
	v_mfma_f32_16x16x32_bf16 v[30:33], v[146:149], v[178:181], v[30:33]
	v_mfma_f32_16x16x32_bf16 v[26:29], v[154:157], v[178:181], v[26:29]
	v_mfma_f32_16x16x32_bf16 v[14:17], v[146:149], v[186:189], v[14:17]
	v_mfma_f32_16x16x32_bf16 v[10:13], v[154:157], v[186:189], v[10:13]
	v_mfma_f32_16x16x32_bf16 v[62:65], v[150:153], v[166:169], v[62:65]
	v_mfma_f32_16x16x32_bf16 v[58:61], v[158:161], v[166:169], v[58:61]
	v_mfma_f32_16x16x32_bf16 v[46:49], v[150:153], v[174:177], v[46:49]
	v_mfma_f32_16x16x32_bf16 v[42:45], v[158:161], v[174:177], v[42:45]
	v_mfma_f32_16x16x32_bf16 v[30:33], v[150:153], v[182:185], v[30:33]
	v_mfma_f32_16x16x32_bf16 v[26:29], v[158:161], v[182:185], v[26:29]
	v_mfma_f32_16x16x32_bf16 v[14:17], v[150:153], v[190:193], v[14:17]
	v_mfma_f32_16x16x32_bf16 v[10:13], v[158:161], v[190:193], v[10:13]

	s_barrier
	s_add_i32 s51, s48, 0x80000
	s_mov_b32 m0, s35
	v_add_u32_e32 v146, s51, v1
	global_load_lds_dwordx4 v146, s[6:7]
	v_add_u32_e32 v146, s51, v134
	s_mov_b32 m0, s36
	s_nop 0
	global_load_lds_dwordx4 v146, s[6:7]
	s_waitcnt vmcnt(6)
	s_barrier

	v_mfma_f32_16x16x32_bf16 v[54:57], v[194:197], v[162:165], v[54:57]
	v_mfma_f32_16x16x32_bf16 v[50:53], v[202:205], v[162:165], v[50:53]
	v_mfma_f32_16x16x32_bf16 v[38:41], v[194:197], v[170:173], v[38:41]
	v_mfma_f32_16x16x32_bf16 v[34:37], v[202:205], v[170:173], v[34:37]
	v_mfma_f32_16x16x32_bf16 v[22:25], v[194:197], v[178:181], v[22:25]
	v_mfma_f32_16x16x32_bf16 v[18:21], v[202:205], v[178:181], v[18:21]
	v_mfma_f32_16x16x32_bf16 v[6:9], v[194:197], v[186:189], v[6:9]
	v_mfma_f32_16x16x32_bf16 v[2:5], v[202:205], v[186:189], v[2:5]
	v_mfma_f32_16x16x32_bf16 v[54:57], v[198:201], v[166:169], v[54:57]
	v_mfma_f32_16x16x32_bf16 v[50:53], v[206:209], v[166:169], v[50:53]
	v_mfma_f32_16x16x32_bf16 v[38:41], v[198:201], v[174:177], v[38:41]
	v_mfma_f32_16x16x32_bf16 v[34:37], v[206:209], v[174:177], v[34:37]
	v_mfma_f32_16x16x32_bf16 v[22:25], v[198:201], v[182:185], v[22:25]
	v_mfma_f32_16x16x32_bf16 v[18:21], v[206:209], v[182:185], v[18:21]
	v_mfma_f32_16x16x32_bf16 v[6:9], v[198:201], v[190:193], v[6:9]
	v_mfma_f32_16x16x32_bf16 v[2:5], v[206:209], v[190:193], v[2:5]

	s_barrier
	ds_read_b128 v[146:149], v144
	ds_read_b128 v[150:153], v144 offset:1024
	ds_read_b128 v[154:157], v144 offset:2048
	ds_read_b128 v[158:161], v144 offset:3072
	s_mov_b32 m0, s21
	v_add_u32_e32 v194, s50, v137
	ds_read_b128 v[162:165], v142 offset:32768
	ds_read_b128 v[166:169], v142 offset:33792
	ds_read_b128 v[170:173], v142 offset:34816
	ds_read_b128 v[174:177], v142 offset:35840
	ds_read_b128 v[178:181], v142 offset:36864
	ds_read_b128 v[182:185], v142 offset:37888
	ds_read_b128 v[186:189], v142 offset:38912
	ds_read_b128 v[190:193], v142 offset:39936
	global_load_lds_dwordx4 v194, s[4:5]
	v_add_u32_e32 v194, s50, v138
	s_mov_b32 m0, s22
	s_nop 0
	global_load_lds_dwordx4 v194, s[4:5]
	s_waitcnt lgkmcnt(8)
	s_barrier
	s_waitcnt lgkmcnt(0)


	v_mfma_f32_16x16x32_bf16 v[122:125], v[146:149], v[162:165], v[122:125]
	v_mfma_f32_16x16x32_bf16 v[126:129], v[154:157], v[162:165], v[126:129]
	v_mfma_f32_16x16x32_bf16 v[110:113], v[146:149], v[170:173], v[110:113]
	v_mfma_f32_16x16x32_bf16 v[106:109], v[154:157], v[170:173], v[106:109]
	v_mfma_f32_16x16x32_bf16 v[94:97], v[146:149], v[178:181], v[94:97]
	v_mfma_f32_16x16x32_bf16 v[90:93], v[154:157], v[178:181], v[90:93]
	v_mfma_f32_16x16x32_bf16 v[78:81], v[146:149], v[186:189], v[78:81]
	v_mfma_f32_16x16x32_bf16 v[74:77], v[154:157], v[186:189], v[74:77]
	v_mfma_f32_16x16x32_bf16 v[122:125], v[150:153], v[166:169], v[122:125]
	v_mfma_f32_16x16x32_bf16 v[126:129], v[158:161], v[166:169], v[126:129]
	v_mfma_f32_16x16x32_bf16 v[110:113], v[150:153], v[174:177], v[110:113]
	v_mfma_f32_16x16x32_bf16 v[106:109], v[158:161], v[174:177], v[106:109]
	v_mfma_f32_16x16x32_bf16 v[94:97], v[150:153], v[182:185], v[94:97]
	v_mfma_f32_16x16x32_bf16 v[90:93], v[158:161], v[182:185], v[90:93]
	v_mfma_f32_16x16x32_bf16 v[78:81], v[150:153], v[190:193], v[78:81]
	v_mfma_f32_16x16x32_bf16 v[74:77], v[158:161], v[190:193], v[74:77]

	s_barrier
	s_or_b32 s50, s48, 0x80
	s_add_i32 s51, s37, s17
	v_add_u32_e32 v210, s50, v1
	s_mov_b32 m0, s51
	ds_read_b128 v[194:197], v145
	ds_read_b128 v[198:201], v145 offset:1024
	ds_read_b128 v[202:205], v145 offset:2048
	ds_read_b128 v[206:209], v145 offset:3072
	global_load_lds_dwordx4 v210, s[6:7]
	v_add_u32_e32 v210, s50, v134
	s_add_i32 m0, s51, 0x2000
	s_nop 0
	global_load_lds_dwordx4 v210, s[6:7]
	s_barrier
	s_waitcnt lgkmcnt(0)


	v_mfma_f32_16x16x32_bf16 v[118:121], v[194:197], v[162:165], v[118:121]
	v_mfma_f32_16x16x32_bf16 v[114:117], v[202:205], v[162:165], v[114:117]
	v_mfma_f32_16x16x32_bf16 v[102:105], v[194:197], v[170:173], v[102:105]
	v_mfma_f32_16x16x32_bf16 v[98:101], v[202:205], v[170:173], v[98:101]
	v_mfma_f32_16x16x32_bf16 v[86:89], v[194:197], v[178:181], v[86:89]
	v_mfma_f32_16x16x32_bf16 v[82:85], v[202:205], v[178:181], v[82:85]
	v_mfma_f32_16x16x32_bf16 v[70:73], v[194:197], v[186:189], v[70:73]
	v_mfma_f32_16x16x32_bf16 v[66:69], v[202:205], v[186:189], v[66:69]
	v_mfma_f32_16x16x32_bf16 v[118:121], v[198:201], v[166:169], v[118:121]
	v_mfma_f32_16x16x32_bf16 v[114:117], v[206:209], v[166:169], v[114:117]
	v_mfma_f32_16x16x32_bf16 v[102:105], v[198:201], v[174:177], v[102:105]
	v_mfma_f32_16x16x32_bf16 v[98:101], v[206:209], v[174:177], v[98:101]
	v_mfma_f32_16x16x32_bf16 v[86:89], v[198:201], v[182:185], v[86:89]
	v_mfma_f32_16x16x32_bf16 v[82:85], v[206:209], v[182:185], v[82:85]
	v_mfma_f32_16x16x32_bf16 v[70:73], v[198:201], v[190:193], v[70:73]
	v_mfma_f32_16x16x32_bf16 v[66:69], v[206:209], v[190:193], v[66:69]

	s_mov_b32 m0, s24
	v_add_u32_e32 v210, s49, v135
	s_barrier
	ds_read_b128 v[162:165], v142 offset:49152
	ds_read_b128 v[166:169], v142 offset:50176
	ds_read_b128 v[170:173], v142 offset:51200
	ds_read_b128 v[174:177], v142 offset:52224
	ds_read_b128 v[178:181], v142 offset:53248
	ds_read_b128 v[182:185], v142 offset:54272
	ds_read_b128 v[186:189], v142 offset:55296
	ds_read_b128 v[190:193], v142 offset:56320
	global_load_lds_dwordx4 v210, s[4:5]
	v_add_u32_e32 v210, s49, v136
	s_mov_b32 m0, s25
	s_nop 0
	global_load_lds_dwordx4 v210, s[4:5]
	s_barrier
	s_waitcnt lgkmcnt(0)


	v_mfma_f32_16x16x32_bf16 v[62:65], v[146:149], v[162:165], v[62:65]
	v_mfma_f32_16x16x32_bf16 v[58:61], v[154:157], v[162:165], v[58:61]
	v_mfma_f32_16x16x32_bf16 v[46:49], v[146:149], v[170:173], v[46:49]
	v_mfma_f32_16x16x32_bf16 v[42:45], v[154:157], v[170:173], v[42:45]
	v_mfma_f32_16x16x32_bf16 v[30:33], v[146:149], v[178:181], v[30:33]
	v_mfma_f32_16x16x32_bf16 v[26:29], v[154:157], v[178:181], v[26:29]
	v_mfma_f32_16x16x32_bf16 v[14:17], v[146:149], v[186:189], v[14:17]
	v_mfma_f32_16x16x32_bf16 v[10:13], v[154:157], v[186:189], v[10:13]
	v_mfma_f32_16x16x32_bf16 v[62:65], v[150:153], v[166:169], v[62:65]
	v_mfma_f32_16x16x32_bf16 v[58:61], v[158:161], v[166:169], v[58:61]
	v_mfma_f32_16x16x32_bf16 v[46:49], v[150:153], v[174:177], v[46:49]
	v_mfma_f32_16x16x32_bf16 v[42:45], v[158:161], v[174:177], v[42:45]
	v_mfma_f32_16x16x32_bf16 v[30:33], v[150:153], v[182:185], v[30:33]
	v_mfma_f32_16x16x32_bf16 v[26:29], v[158:161], v[182:185], v[26:29]
	v_mfma_f32_16x16x32_bf16 v[14:17], v[150:153], v[190:193], v[14:17]
	v_mfma_f32_16x16x32_bf16 v[10:13], v[158:161], v[190:193], v[10:13]

	s_barrier
	s_add_i32 s48, s48, 0x80080
	s_add_i32 s49, s38, s17
	v_add_u32_e32 v146, s48, v1
	s_mov_b32 m0, s49
	s_nop 0
	global_load_lds_dwordx4 v146, s[6:7]
	v_add_u32_e32 v146, s48, v134
	s_add_i32 m0, s49, 0x2000
	s_nop 0
	global_load_lds_dwordx4 v146, s[6:7]
	s_waitcnt vmcnt(6)
	s_barrier

	v_mfma_f32_16x16x32_bf16 v[54:57], v[194:197], v[162:165], v[54:57]
	v_mfma_f32_16x16x32_bf16 v[50:53], v[202:205], v[162:165], v[50:53]
	v_mfma_f32_16x16x32_bf16 v[38:41], v[194:197], v[170:173], v[38:41]
	v_mfma_f32_16x16x32_bf16 v[34:37], v[202:205], v[170:173], v[34:37]
	v_mfma_f32_16x16x32_bf16 v[22:25], v[194:197], v[178:181], v[22:25]
	v_mfma_f32_16x16x32_bf16 v[18:21], v[202:205], v[178:181], v[18:21]
	v_mfma_f32_16x16x32_bf16 v[6:9], v[194:197], v[186:189], v[6:9]
	v_mfma_f32_16x16x32_bf16 v[2:5], v[202:205], v[186:189], v[2:5]
	v_mfma_f32_16x16x32_bf16 v[54:57], v[198:201], v[166:169], v[54:57]
	v_mfma_f32_16x16x32_bf16 v[50:53], v[206:209], v[166:169], v[50:53]
	v_mfma_f32_16x16x32_bf16 v[38:41], v[198:201], v[174:177], v[38:41]
	v_mfma_f32_16x16x32_bf16 v[34:37], v[206:209], v[174:177], v[34:37]
	v_mfma_f32_16x16x32_bf16 v[22:25], v[198:201], v[182:185], v[22:25]
	v_mfma_f32_16x16x32_bf16 v[18:21], v[206:209], v[182:185], v[18:21]
	v_mfma_f32_16x16x32_bf16 v[6:9], v[198:201], v[190:193], v[6:9]
	v_mfma_f32_16x16x32_bf16 v[2:5], v[206:209], v[190:193], v[2:5]

	s_add_i32 s47, s47, 2
	s_addk_i32 s45, 0x100
	s_addk_i32 s46, 0x100
	s_cmp_ge_i32 s47, s26
	s_barrier
	s_cbranch_scc0 .LBB0_451
	s_branch .LBB0_446

.LBB0_464:
	ds_read_b128 v[152:155], v146
	ds_read_b128 v[156:159], v146 offset:1024
	ds_read_b128 v[160:163], v146 offset:2048
	ds_read_b128 v[164:167], v146 offset:3072
	s_add_i32 s46, s43, 0x80
	s_cmp_eq_u32 s30, s45
	s_cselect_b32 s48, s16, s46
	s_cselect_b32 s46, s17, s44
	s_or_b32 s47, s48, 0x80
	s_mov_b32 m0, s34
	v_add_u32_e32 v66, s43, v141
	ds_read_b128 v[168:171], v147
	ds_read_b128 v[172:175], v147 offset:1024
	ds_read_b128 v[176:179], v147 offset:2048
	ds_read_b128 v[180:183], v147 offset:3072
	ds_read_b128 v[184:187], v147 offset:4096
	ds_read_b128 v[188:191], v147 offset:5120
	ds_read_b128 v[192:195], v147 offset:6144
	ds_read_b128 v[196:199], v147 offset:7168
	global_load_lds_dwordx4 v66, s[4:5]
	v_add_u32_e32 v66, s43, v142
	s_mov_b32 m0, s35
	s_nop 0
	global_load_lds_dwordx4 v66, s[4:5]
	s_waitcnt lgkmcnt(8)
	s_barrier
	s_waitcnt lgkmcnt(0)


	v_mfma_scale_f32_16x16x128_f8f6f4 v[126:129], v[152:159], v[168:175], v[126:129], v149, v148 op_sel_hi:[0,0,0]
	v_mfma_scale_f32_16x16x128_f8f6f4 v[122:125], v[160:167], v[168:175], v[122:125], v149, v148 op_sel_hi:[0,0,0]
	v_mfma_scale_f32_16x16x128_f8f6f4 v[134:137], v[152:159], v[176:183], v[110:113], v149, v148 op_sel_hi:[0,0,0]
	v_mfma_scale_f32_16x16x128_f8f6f4 v[200:203], v[160:167], v[176:183], v[106:109], v149, v148 op_sel_hi:[0,0,0]
	v_mfma_scale_f32_16x16x128_f8f6f4 v[204:207], v[152:159], v[184:191], v[94:97], v149, v148 op_sel_hi:[0,0,0]
	v_mfma_scale_f32_16x16x128_f8f6f4 v[208:211], v[160:167], v[184:191], v[90:93], v149, v148 op_sel_hi:[0,0,0]
	v_mfma_scale_f32_16x16x128_f8f6f4 v[212:215], v[152:159], v[192:199], v[78:81], v149, v148 op_sel_hi:[0,0,0]
	v_mfma_scale_f32_16x16x128_f8f6f4 v[216:219], v[160:167], v[192:199], v[74:77], v149, v148 op_sel_hi:[0,0,0]

	s_barrier
	s_mov_b32 m0, s36
	v_add_u32_e32 v66, s46, v1
	s_nop 2
	ds_read_b128 v[74:77], v150
	ds_read_b128 v[78:81], v150 offset:1024
	ds_read_b128 v[90:93], v150 offset:2048
	ds_read_b128 v[94:97], v150 offset:3072
	global_load_lds_dwordx4 v66, s[10:11]
	v_add_u32_e32 v66, s46, v138
	s_add_i32 m0, s36, 0x2000
	s_nop 0
	global_load_lds_dwordx4 v66, s[10:11]
	s_barrier
	s_waitcnt lgkmcnt(0)


	v_mfma_scale_f32_16x16x128_f8f6f4 v[118:121], v[74:81], v[168:175], v[118:121], v149, v148 op_sel_hi:[0,0,0]
	v_mfma_scale_f32_16x16x128_f8f6f4 v[114:117], v[90:97], v[168:175], v[114:117], v149, v148 op_sel_hi:[0,0,0]
	v_mfma_scale_f32_16x16x128_f8f6f4 v[168:171], v[74:81], v[176:183], v[102:105], v149, v148 op_sel_hi:[0,0,0]
	v_mfma_scale_f32_16x16x128_f8f6f4 v[172:175], v[90:97], v[176:183], v[98:101], v149, v148 op_sel_hi:[0,0,0]
	v_mfma_scale_f32_16x16x128_f8f6f4 v[176:179], v[74:81], v[184:191], v[86:89], v149, v148 op_sel_hi:[0,0,0]
	v_mfma_scale_f32_16x16x128_f8f6f4 v[180:183], v[90:97], v[184:191], v[82:85], v149, v148 op_sel_hi:[0,0,0]
	v_mfma_scale_f32_16x16x128_f8f6f4 v[184:187], v[74:81], v[192:199], v[70:73], v149, v148 op_sel_hi:[0,0,0]
	v_mfma_scale_f32_16x16x128_f8f6f4 v[188:191], v[90:97], v[192:199], v[10:13], v149, v148 op_sel_hi:[0,0,0]

	s_mov_b32 m0, s21
	s_nop 4
	v_add_u32_e32 v10, s48, v139
	s_barrier
	ds_read_b128 v[66:69], v147 offset:16384
	ds_read_b128 v[70:73], v147 offset:17408
	ds_read_b128 v[82:85], v147 offset:18432
	ds_read_b128 v[86:89], v147 offset:19456
	ds_read_b128 v[98:101], v147 offset:20480
	ds_read_b128 v[102:105], v147 offset:21504
	ds_read_b128 v[106:109], v147 offset:22528
	ds_read_b128 v[110:113], v147 offset:23552
	global_load_lds_dwordx4 v10, s[4:5]
	v_add_u32_e32 v10, s48, v140
	s_mov_b32 m0, s22
	s_nop 0
	global_load_lds_dwordx4 v10, s[4:5]
	s_barrier
	s_waitcnt lgkmcnt(0)


	v_mfma_scale_f32_16x16x128_f8f6f4 v[62:65], v[152:159], v[66:73], v[62:65], v149, v148 op_sel_hi:[0,0,0]
	v_mfma_scale_f32_16x16x128_f8f6f4 v[58:61], v[160:167], v[66:73], v[58:61], v149, v148 op_sel_hi:[0,0,0]
	v_mfma_scale_f32_16x16x128_f8f6f4 v[232:235], v[160:167], v[106:113], v[232:235], v149, v148 op_sel_hi:[0,0,0]
	v_mfma_scale_f32_16x16x128_f8f6f4 v[192:195], v[152:159], v[82:89], v[46:49], v149, v148 op_sel_hi:[0,0,0]
	v_mfma_scale_f32_16x16x128_f8f6f4 v[196:199], v[160:167], v[82:89], v[42:45], v149, v148 op_sel_hi:[0,0,0]
	v_mfma_scale_f32_16x16x128_f8f6f4 v[220:223], v[152:159], v[98:105], v[30:33], v149, v148 op_sel_hi:[0,0,0]
	v_mfma_scale_f32_16x16x128_f8f6f4 v[224:227], v[160:167], v[98:105], v[26:29], v149, v148 op_sel_hi:[0,0,0]
	v_mfma_scale_f32_16x16x128_f8f6f4 v[228:231], v[152:159], v[106:113], v[14:17], v149, v148 op_sel_hi:[0,0,0]

	s_barrier
	s_add_i32 s49, s46, 0x40000
	s_add_i32 s50, s31, s19
	v_add_u32_e32 v10, s49, v1
	s_mov_b32 m0, s50
	s_nop 0
	global_load_lds_dwordx4 v10, s[10:11]
	v_add_u32_e32 v10, s49, v138
	s_add_i32 m0, s50, 0x2000
	s_nop 0
	global_load_lds_dwordx4 v10, s[10:11]
	s_waitcnt vmcnt(6)
	s_barrier

	v_mfma_scale_f32_16x16x128_f8f6f4 v[54:57], v[74:81], v[66:73], v[54:57], v149, v148 op_sel_hi:[0,0,0]
	v_mfma_scale_f32_16x16x128_f8f6f4 v[50:53], v[90:97], v[66:73], v[50:53], v149, v148 op_sel_hi:[0,0,0]
	v_mfma_scale_f32_16x16x128_f8f6f4 v[236:239], v[74:81], v[82:89], v[38:41], v149, v148 op_sel_hi:[0,0,0]
	v_mfma_scale_f32_16x16x128_f8f6f4 v[240:243], v[90:97], v[82:89], v[34:37], v149, v148 op_sel_hi:[0,0,0]
	v_mfma_scale_f32_16x16x128_f8f6f4 v[244:247], v[74:81], v[98:105], v[22:25], v149, v148 op_sel_hi:[0,0,0]
	v_mfma_scale_f32_16x16x128_f8f6f4 v[248:251], v[90:97], v[98:105], v[18:21], v149, v148 op_sel_hi:[0,0,0]
	v_mfma_scale_f32_16x16x128_f8f6f4 v[130:133], v[74:81], v[106:113], v[6:9], v149, v148 op_sel_hi:[0,0,0]
	v_mfma_scale_f32_16x16x128_f8f6f4 v[66:69], v[90:97], v[106:113], v[2:5], v149, v148 op_sel_hi:[0,0,0]

	s_add_i32 s49, 0, 0x18000
	v_add_u32_e32 v10, s49, v145
	s_barrier
	s_nop 2
	ds_read_b128 v[2:5], v10
	ds_read_b128 v[6:9], v10 offset:1024
	ds_read_b128 v[18:21], v10 offset:2048
	ds_read_b128 v[22:25], v10 offset:3072
	s_mov_b32 m0, s23
	v_add_u32_e32 v70, s48, v141
	ds_read_b128 v[10:13], v147 offset:32768
	ds_read_b128 v[14:17], v147 offset:33792
	ds_read_b128 v[26:29], v147 offset:34816
	ds_read_b128 v[30:33], v147 offset:35840
	ds_read_b128 v[34:37], v147 offset:36864
	ds_read_b128 v[38:41], v147 offset:37888
	ds_read_b128 v[42:45], v147 offset:38912
	ds_read_b128 v[46:49], v147 offset:39936
	global_load_lds_dwordx4 v70, s[4:5]
	v_add_u32_e32 v70, s48, v142
	s_mov_b32 m0, s24
	s_nop 0
	global_load_lds_dwordx4 v70, s[4:5]
	s_waitcnt lgkmcnt(8)
	s_barrier
	s_waitcnt lgkmcnt(0)


	v_mfma_scale_f32_16x16x128_f8f6f4 v[126:129], v[2:9], v[10:17], v[126:129], v149, v148 op_sel_hi:[0,0,0]
	v_mfma_scale_f32_16x16x128_f8f6f4 v[122:125], v[18:25], v[10:17], v[122:125], v149, v148 op_sel_hi:[0,0,0]
	v_mfma_scale_f32_16x16x128_f8f6f4 v[110:113], v[2:9], v[26:33], v[134:137], v149, v148 op_sel_hi:[0,0,0]
	v_mfma_scale_f32_16x16x128_f8f6f4 v[106:109], v[18:25], v[26:33], v[200:203], v149, v148 op_sel_hi:[0,0,0]
	v_mfma_scale_f32_16x16x128_f8f6f4 v[94:97], v[2:9], v[34:41], v[204:207], v149, v148 op_sel_hi:[0,0,0]
	v_mfma_scale_f32_16x16x128_f8f6f4 v[90:93], v[18:25], v[34:41], v[208:211], v149, v148 op_sel_hi:[0,0,0]
	v_mfma_scale_f32_16x16x128_f8f6f4 v[78:81], v[2:9], v[42:49], v[212:215], v149, v148 op_sel_hi:[0,0,0]
	v_mfma_scale_f32_16x16x128_f8f6f4 v[74:77], v[18:25], v[42:49], v[216:219], v149, v148 op_sel_hi:[0,0,0]

	s_barrier
	s_add_i32 s48, 0, 0x1c000
	v_add_u32_e32 v70, s48, v145
	s_or_b32 s50, s46, 0x80
	s_add_i32 s49, s49, s19
	ds_read_b128 v[152:155], v70
	ds_read_b128 v[156:159], v70 offset:1024
	ds_read_b128 v[160:163], v70 offset:2048
	ds_read_b128 v[164:167], v70 offset:3072
	v_add_u32_e32 v70, s50, v1
	s_mov_b32 m0, s49
	s_nop 0
	global_load_lds_dwordx4 v70, s[10:11]
	v_add_u32_e32 v70, s50, v138
	s_add_i32 m0, s49, 0x2000
	s_nop 0
	global_load_lds_dwordx4 v70, s[10:11]
	s_barrier
	s_waitcnt lgkmcnt(0)


	v_mfma_scale_f32_16x16x128_f8f6f4 v[118:121], v[152:159], v[10:17], v[118:121], v149, v148 op_sel_hi:[0,0,0]
	v_mfma_scale_f32_16x16x128_f8f6f4 v[114:117], v[160:167], v[10:17], v[114:117], v149, v148 op_sel_hi:[0,0,0]
	v_mfma_scale_f32_16x16x128_f8f6f4 v[102:105], v[152:159], v[26:33], v[168:171], v149, v148 op_sel_hi:[0,0,0]
	v_mfma_scale_f32_16x16x128_f8f6f4 v[98:101], v[160:167], v[26:33], v[172:175], v149, v148 op_sel_hi:[0,0,0]
	v_mfma_scale_f32_16x16x128_f8f6f4 v[86:89], v[152:159], v[34:41], v[176:179], v149, v148 op_sel_hi:[0,0,0]
	v_mfma_scale_f32_16x16x128_f8f6f4 v[82:85], v[160:167], v[34:41], v[180:183], v149, v148 op_sel_hi:[0,0,0]
	v_mfma_scale_f32_16x16x128_f8f6f4 v[70:73], v[152:159], v[42:49], v[184:187], v149, v148 op_sel_hi:[0,0,0]
	v_mfma_scale_f32_16x16x128_f8f6f4 v[10:13], v[160:167], v[42:49], v[188:191], v149, v148 op_sel_hi:[0,0,0]

	s_mov_b32 m0, s26
	v_add_u32_e32 v14, s47, v139
	s_barrier
	ds_read_b128 v[34:37], v147 offset:49152
	ds_read_b128 v[38:41], v147 offset:50176
	ds_read_b128 v[168:171], v147 offset:51200
	ds_read_b128 v[172:175], v147 offset:52224
	ds_read_b128 v[176:179], v147 offset:53248
	ds_read_b128 v[180:183], v147 offset:54272
	ds_read_b128 v[184:187], v147 offset:55296
	ds_read_b128 v[188:191], v147 offset:56320
	global_load_lds_dwordx4 v14, s[4:5]
	v_add_u32_e32 v14, s47, v140
	s_mov_b32 m0, s27
	s_nop 0
	global_load_lds_dwordx4 v14, s[4:5]
	s_barrier
	s_waitcnt lgkmcnt(0)


	v_mfma_scale_f32_16x16x128_f8f6f4 v[62:65], v[2:9], v[34:41], v[62:65], v149, v148 op_sel_hi:[0,0,0]
	v_mfma_scale_f32_16x16x128_f8f6f4 v[58:61], v[18:25], v[34:41], v[58:61], v149, v148 op_sel_hi:[0,0,0]
	v_mfma_scale_f32_16x16x128_f8f6f4 v[46:49], v[2:9], v[168:175], v[192:195], v149, v148 op_sel_hi:[0,0,0]
	v_mfma_scale_f32_16x16x128_f8f6f4 v[42:45], v[18:25], v[168:175], v[196:199], v149, v148 op_sel_hi:[0,0,0]
	v_mfma_scale_f32_16x16x128_f8f6f4 v[30:33], v[2:9], v[176:183], v[220:223], v149, v148 op_sel_hi:[0,0,0]
	v_mfma_scale_f32_16x16x128_f8f6f4 v[26:29], v[18:25], v[176:183], v[224:227], v149, v148 op_sel_hi:[0,0,0]
	v_mfma_scale_f32_16x16x128_f8f6f4 v[14:17], v[2:9], v[184:191], v[228:231], v149, v148 op_sel_hi:[0,0,0]
	v_mfma_scale_f32_16x16x128_f8f6f4 v[232:235], v[18:25], v[184:191], v[232:235], v149, v148 op_sel_hi:[0,0,0]

	s_barrier
	s_add_i32 s46, s46, 0x40080
	s_add_i32 s47, s48, s19
	v_add_u32_e32 v2, s46, v1
	s_mov_b32 m0, s47
	s_nop 0
	global_load_lds_dwordx4 v2, s[10:11]
	v_add_u32_e32 v2, s46, v138
	s_add_i32 m0, s47, 0x2000
	s_nop 0
	global_load_lds_dwordx4 v2, s[10:11]
	s_waitcnt vmcnt(6)
	s_barrier

	v_mfma_scale_f32_16x16x128_f8f6f4 v[54:57], v[152:159], v[34:41], v[54:57], v149, v148 op_sel_hi:[0,0,0]
	v_mfma_scale_f32_16x16x128_f8f6f4 v[50:53], v[160:167], v[34:41], v[50:53], v149, v148 op_sel_hi:[0,0,0]
	v_mfma_scale_f32_16x16x128_f8f6f4 v[38:41], v[152:159], v[168:175], v[236:239], v149, v148 op_sel_hi:[0,0,0]
	v_mfma_scale_f32_16x16x128_f8f6f4 v[34:37], v[160:167], v[168:175], v[240:243], v149, v148 op_sel_hi:[0,0,0]
	v_mfma_scale_f32_16x16x128_f8f6f4 v[22:25], v[152:159], v[176:183], v[244:247], v149, v148 op_sel_hi:[0,0,0]
	v_mfma_scale_f32_16x16x128_f8f6f4 v[18:21], v[160:167], v[176:183], v[248:251], v149, v148 op_sel_hi:[0,0,0]
	v_mfma_scale_f32_16x16x128_f8f6f4 v[6:9], v[152:159], v[184:191], v[130:133], v149, v148 op_sel_hi:[0,0,0]
	v_mfma_scale_f32_16x16x128_f8f6f4 v[2:5], v[160:167], v[184:191], v[66:69], v149, v148 op_sel_hi:[0,0,0]

	s_add_i32 s45, s45, 2
	s_addk_i32 s43, 0x100
	s_addk_i32 s44, 0x100
	s_cmp_ge_i32 s45, s28
	s_barrier
	s_cbranch_scc0 .LBB0_464
	s_branch .LBB0_466

.LBB0_620:
	ds_read_b128 v[146:149], v141
	ds_read_b128 v[150:153], v141 offset:1024
	ds_read_b128 v[154:157], v141 offset:2048
	ds_read_b128 v[158:161], v141 offset:3072
	s_add_i32 s50, s47, 0x80
	s_cmp_eq_u32 s30, s49
	s_cselect_b32 s52, s16, s50
	s_cselect_b32 s50, s17, s48
	s_or_b32 s51, s52, 0x80
	s_mov_b32 m0, s31
	v_add_u32_e32 v194, s47, v131
	ds_read_b128 v[162:165], v142
	ds_read_b128 v[166:169], v142 offset:1024
	ds_read_b128 v[170:173], v142 offset:2048
	ds_read_b128 v[174:177], v142 offset:3072
	ds_read_b128 v[178:181], v142 offset:4096
	ds_read_b128 v[182:185], v142 offset:5120
	ds_read_b128 v[186:189], v142 offset:6144
	ds_read_b128 v[190:193], v142 offset:7168
	global_load_lds_dwordx4 v194, s[6:7]
	v_add_u32_e32 v194, s47, v133
	s_mov_b32 m0, s33
	s_nop 0
	global_load_lds_dwordx4 v194, s[6:7]
	s_waitcnt lgkmcnt(8)
	s_barrier
	s_waitcnt lgkmcnt(0)


	v_mfma_f32_16x16x32_bf16 v[122:125], v[146:149], v[162:165], v[122:125]
	v_mfma_f32_16x16x32_bf16 v[126:129], v[154:157], v[162:165], v[126:129]
	v_mfma_f32_16x16x32_bf16 v[110:113], v[146:149], v[170:173], v[110:113]
	v_mfma_f32_16x16x32_bf16 v[106:109], v[154:157], v[170:173], v[106:109]
	v_mfma_f32_16x16x32_bf16 v[94:97], v[146:149], v[178:181], v[94:97]
	v_mfma_f32_16x16x32_bf16 v[90:93], v[154:157], v[178:181], v[90:93]
	v_mfma_f32_16x16x32_bf16 v[78:81], v[146:149], v[186:189], v[78:81]
	v_mfma_f32_16x16x32_bf16 v[74:77], v[154:157], v[186:189], v[74:77]
	v_mfma_f32_16x16x32_bf16 v[122:125], v[150:153], v[166:169], v[122:125]
	v_mfma_f32_16x16x32_bf16 v[126:129], v[158:161], v[166:169], v[126:129]
	v_mfma_f32_16x16x32_bf16 v[110:113], v[150:153], v[174:177], v[110:113]
	v_mfma_f32_16x16x32_bf16 v[106:109], v[158:161], v[174:177], v[106:109]
	v_mfma_f32_16x16x32_bf16 v[94:97], v[150:153], v[182:185], v[94:97]
	v_mfma_f32_16x16x32_bf16 v[90:93], v[158:161], v[182:185], v[90:93]
	v_mfma_f32_16x16x32_bf16 v[78:81], v[150:153], v[190:193], v[78:81]
	v_mfma_f32_16x16x32_bf16 v[74:77], v[158:161], v[190:193], v[74:77]

	s_barrier
	s_mov_b32 m0, s35
	v_add_u32_e32 v210, s50, v1
	ds_read_b128 v[194:197], v143
	ds_read_b128 v[198:201], v143 offset:1024
	ds_read_b128 v[202:205], v143 offset:2048
	ds_read_b128 v[206:209], v143 offset:3072
	global_load_lds_dwordx4 v210, s[10:11]
	v_add_u32_e32 v210, s50, v138
	s_mov_b32 m0, s36
	s_nop 0
	global_load_lds_dwordx4 v210, s[10:11]
	s_barrier
	s_waitcnt lgkmcnt(0)


	v_mfma_f32_16x16x32_bf16 v[118:121], v[194:197], v[162:165], v[118:121]
	v_mfma_f32_16x16x32_bf16 v[114:117], v[202:205], v[162:165], v[114:117]
	v_mfma_f32_16x16x32_bf16 v[102:105], v[194:197], v[170:173], v[102:105]
	v_mfma_f32_16x16x32_bf16 v[98:101], v[202:205], v[170:173], v[98:101]
	v_mfma_f32_16x16x32_bf16 v[86:89], v[194:197], v[178:181], v[86:89]
	v_mfma_f32_16x16x32_bf16 v[82:85], v[202:205], v[178:181], v[82:85]
	v_mfma_f32_16x16x32_bf16 v[70:73], v[194:197], v[186:189], v[70:73]
	v_mfma_f32_16x16x32_bf16 v[66:69], v[202:205], v[186:189], v[66:69]
	v_mfma_f32_16x16x32_bf16 v[118:121], v[198:201], v[166:169], v[118:121]
	v_mfma_f32_16x16x32_bf16 v[114:117], v[206:209], v[166:169], v[114:117]
	v_mfma_f32_16x16x32_bf16 v[102:105], v[198:201], v[174:177], v[102:105]
	v_mfma_f32_16x16x32_bf16 v[98:101], v[206:209], v[174:177], v[98:101]
	v_mfma_f32_16x16x32_bf16 v[86:89], v[198:201], v[182:185], v[86:89]
	v_mfma_f32_16x16x32_bf16 v[82:85], v[206:209], v[182:185], v[82:85]
	v_mfma_f32_16x16x32_bf16 v[70:73], v[198:201], v[190:193], v[70:73]
	v_mfma_f32_16x16x32_bf16 v[66:69], v[206:209], v[190:193], v[66:69]

	s_mov_b32 m0, s21
	v_add_u32_e32 v210, s52, v130
	s_barrier
	ds_read_b128 v[162:165], v142 offset:16384
	ds_read_b128 v[166:169], v142 offset:17408
	ds_read_b128 v[170:173], v142 offset:18432
	ds_read_b128 v[174:177], v142 offset:19456
	ds_read_b128 v[178:181], v142 offset:20480
	ds_read_b128 v[182:185], v142 offset:21504
	ds_read_b128 v[186:189], v142 offset:22528
	ds_read_b128 v[190:193], v142 offset:23552
	global_load_lds_dwordx4 v210, s[6:7]
	v_add_u32_e32 v210, s52, v132
	s_mov_b32 m0, s22
	s_nop 0
	global_load_lds_dwordx4 v210, s[6:7]
	s_barrier
	s_waitcnt lgkmcnt(0)


	v_mfma_f32_16x16x32_bf16 v[62:65], v[146:149], v[162:165], v[62:65]
	v_mfma_f32_16x16x32_bf16 v[58:61], v[154:157], v[162:165], v[58:61]
	v_mfma_f32_16x16x32_bf16 v[46:49], v[146:149], v[170:173], v[46:49]
	v_mfma_f32_16x16x32_bf16 v[42:45], v[154:157], v[170:173], v[42:45]
	v_mfma_f32_16x16x32_bf16 v[30:33], v[146:149], v[178:181], v[30:33]
	v_mfma_f32_16x16x32_bf16 v[26:29], v[154:157], v[178:181], v[26:29]
	v_mfma_f32_16x16x32_bf16 v[14:17], v[146:149], v[186:189], v[14:17]
	v_mfma_f32_16x16x32_bf16 v[10:13], v[154:157], v[186:189], v[10:13]
	v_mfma_f32_16x16x32_bf16 v[62:65], v[150:153], v[166:169], v[62:65]
	v_mfma_f32_16x16x32_bf16 v[58:61], v[158:161], v[166:169], v[58:61]
	v_mfma_f32_16x16x32_bf16 v[46:49], v[150:153], v[174:177], v[46:49]
	v_mfma_f32_16x16x32_bf16 v[42:45], v[158:161], v[174:177], v[42:45]
	v_mfma_f32_16x16x32_bf16 v[30:33], v[150:153], v[182:185], v[30:33]
	v_mfma_f32_16x16x32_bf16 v[26:29], v[158:161], v[182:185], v[26:29]
	v_mfma_f32_16x16x32_bf16 v[14:17], v[150:153], v[190:193], v[14:17]
	v_mfma_f32_16x16x32_bf16 v[10:13], v[158:161], v[190:193], v[10:13]

	s_barrier
	s_add_i32 s53, s50, 0x20000
	s_mov_b32 m0, s37
	v_add_u32_e32 v146, s53, v1
	global_load_lds_dwordx4 v146, s[10:11]
	v_add_u32_e32 v146, s53, v138
	s_mov_b32 m0, s38
	s_nop 0
	global_load_lds_dwordx4 v146, s[10:11]
	s_waitcnt vmcnt(6)
	s_barrier

	v_mfma_f32_16x16x32_bf16 v[54:57], v[194:197], v[162:165], v[54:57]
	v_mfma_f32_16x16x32_bf16 v[50:53], v[202:205], v[162:165], v[50:53]
	v_mfma_f32_16x16x32_bf16 v[38:41], v[194:197], v[170:173], v[38:41]
	v_mfma_f32_16x16x32_bf16 v[34:37], v[202:205], v[170:173], v[34:37]
	v_mfma_f32_16x16x32_bf16 v[22:25], v[194:197], v[178:181], v[22:25]
	v_mfma_f32_16x16x32_bf16 v[18:21], v[202:205], v[178:181], v[18:21]
	v_mfma_f32_16x16x32_bf16 v[6:9], v[194:197], v[186:189], v[6:9]
	v_mfma_f32_16x16x32_bf16 v[2:5], v[202:205], v[186:189], v[2:5]
	v_mfma_f32_16x16x32_bf16 v[54:57], v[198:201], v[166:169], v[54:57]
	v_mfma_f32_16x16x32_bf16 v[50:53], v[206:209], v[166:169], v[50:53]
	v_mfma_f32_16x16x32_bf16 v[38:41], v[198:201], v[174:177], v[38:41]
	v_mfma_f32_16x16x32_bf16 v[34:37], v[206:209], v[174:177], v[34:37]
	v_mfma_f32_16x16x32_bf16 v[22:25], v[198:201], v[182:185], v[22:25]
	v_mfma_f32_16x16x32_bf16 v[18:21], v[206:209], v[182:185], v[18:21]
	v_mfma_f32_16x16x32_bf16 v[6:9], v[198:201], v[190:193], v[6:9]
	v_mfma_f32_16x16x32_bf16 v[2:5], v[206:209], v[190:193], v[2:5]

	s_barrier
	ds_read_b128 v[146:149], v144
	ds_read_b128 v[150:153], v144 offset:1024
	ds_read_b128 v[154:157], v144 offset:2048
	ds_read_b128 v[158:161], v144 offset:3072
	s_mov_b32 m0, s23
	v_add_u32_e32 v194, s52, v131
	ds_read_b128 v[162:165], v142 offset:32768
	ds_read_b128 v[166:169], v142 offset:33792
	ds_read_b128 v[170:173], v142 offset:34816
	ds_read_b128 v[174:177], v142 offset:35840
	ds_read_b128 v[178:181], v142 offset:36864
	ds_read_b128 v[182:185], v142 offset:37888
	ds_read_b128 v[186:189], v142 offset:38912
	ds_read_b128 v[190:193], v142 offset:39936
	global_load_lds_dwordx4 v194, s[6:7]
	v_add_u32_e32 v194, s52, v133
	s_mov_b32 m0, s24
	s_nop 0
	global_load_lds_dwordx4 v194, s[6:7]
	s_waitcnt lgkmcnt(8)
	s_barrier
	s_waitcnt lgkmcnt(0)


	v_mfma_f32_16x16x32_bf16 v[122:125], v[146:149], v[162:165], v[122:125]
	v_mfma_f32_16x16x32_bf16 v[126:129], v[154:157], v[162:165], v[126:129]
	v_mfma_f32_16x16x32_bf16 v[110:113], v[146:149], v[170:173], v[110:113]
	v_mfma_f32_16x16x32_bf16 v[106:109], v[154:157], v[170:173], v[106:109]
	v_mfma_f32_16x16x32_bf16 v[94:97], v[146:149], v[178:181], v[94:97]
	v_mfma_f32_16x16x32_bf16 v[90:93], v[154:157], v[178:181], v[90:93]
	v_mfma_f32_16x16x32_bf16 v[78:81], v[146:149], v[186:189], v[78:81]
	v_mfma_f32_16x16x32_bf16 v[74:77], v[154:157], v[186:189], v[74:77]
	v_mfma_f32_16x16x32_bf16 v[122:125], v[150:153], v[166:169], v[122:125]
	v_mfma_f32_16x16x32_bf16 v[126:129], v[158:161], v[166:169], v[126:129]
	v_mfma_f32_16x16x32_bf16 v[110:113], v[150:153], v[174:177], v[110:113]
	v_mfma_f32_16x16x32_bf16 v[106:109], v[158:161], v[174:177], v[106:109]
	v_mfma_f32_16x16x32_bf16 v[94:97], v[150:153], v[182:185], v[94:97]
	v_mfma_f32_16x16x32_bf16 v[90:93], v[158:161], v[182:185], v[90:93]
	v_mfma_f32_16x16x32_bf16 v[78:81], v[150:153], v[190:193], v[78:81]
	v_mfma_f32_16x16x32_bf16 v[74:77], v[158:161], v[190:193], v[74:77]

	s_barrier
	s_or_b32 s52, s50, 0x80
	s_add_i32 s53, s39, s19
	v_add_u32_e32 v210, s52, v1
	s_mov_b32 m0, s53
	ds_read_b128 v[194:197], v145
	ds_read_b128 v[198:201], v145 offset:1024
	ds_read_b128 v[202:205], v145 offset:2048
	ds_read_b128 v[206:209], v145 offset:3072
	global_load_lds_dwordx4 v210, s[10:11]
	v_add_u32_e32 v210, s52, v138
	s_add_i32 m0, s53, 0x2000
	s_nop 0
	global_load_lds_dwordx4 v210, s[10:11]
	s_barrier
	s_waitcnt lgkmcnt(0)


	v_mfma_f32_16x16x32_bf16 v[118:121], v[194:197], v[162:165], v[118:121]
	v_mfma_f32_16x16x32_bf16 v[114:117], v[202:205], v[162:165], v[114:117]
	v_mfma_f32_16x16x32_bf16 v[102:105], v[194:197], v[170:173], v[102:105]
	v_mfma_f32_16x16x32_bf16 v[98:101], v[202:205], v[170:173], v[98:101]
	v_mfma_f32_16x16x32_bf16 v[86:89], v[194:197], v[178:181], v[86:89]
	v_mfma_f32_16x16x32_bf16 v[82:85], v[202:205], v[178:181], v[82:85]
	v_mfma_f32_16x16x32_bf16 v[70:73], v[194:197], v[186:189], v[70:73]
	v_mfma_f32_16x16x32_bf16 v[66:69], v[202:205], v[186:189], v[66:69]
	v_mfma_f32_16x16x32_bf16 v[118:121], v[198:201], v[166:169], v[118:121]
	v_mfma_f32_16x16x32_bf16 v[114:117], v[206:209], v[166:169], v[114:117]
	v_mfma_f32_16x16x32_bf16 v[102:105], v[198:201], v[174:177], v[102:105]
	v_mfma_f32_16x16x32_bf16 v[98:101], v[206:209], v[174:177], v[98:101]
	v_mfma_f32_16x16x32_bf16 v[86:89], v[198:201], v[182:185], v[86:89]
	v_mfma_f32_16x16x32_bf16 v[82:85], v[206:209], v[182:185], v[82:85]
	v_mfma_f32_16x16x32_bf16 v[70:73], v[198:201], v[190:193], v[70:73]
	v_mfma_f32_16x16x32_bf16 v[66:69], v[206:209], v[190:193], v[66:69]

	s_mov_b32 m0, s26
	v_add_u32_e32 v210, s51, v130
	s_barrier
	ds_read_b128 v[162:165], v142 offset:49152
	ds_read_b128 v[166:169], v142 offset:50176
	ds_read_b128 v[170:173], v142 offset:51200
	ds_read_b128 v[174:177], v142 offset:52224
	ds_read_b128 v[178:181], v142 offset:53248
	ds_read_b128 v[182:185], v142 offset:54272
	ds_read_b128 v[186:189], v142 offset:55296
	ds_read_b128 v[190:193], v142 offset:56320
	global_load_lds_dwordx4 v210, s[6:7]
	v_add_u32_e32 v210, s51, v132
	s_mov_b32 m0, s27
	s_nop 0
	global_load_lds_dwordx4 v210, s[6:7]
	s_barrier
	s_waitcnt lgkmcnt(0)


	v_mfma_f32_16x16x32_bf16 v[62:65], v[146:149], v[162:165], v[62:65]
	v_mfma_f32_16x16x32_bf16 v[58:61], v[154:157], v[162:165], v[58:61]
	v_mfma_f32_16x16x32_bf16 v[46:49], v[146:149], v[170:173], v[46:49]
	v_mfma_f32_16x16x32_bf16 v[42:45], v[154:157], v[170:173], v[42:45]
	v_mfma_f32_16x16x32_bf16 v[30:33], v[146:149], v[178:181], v[30:33]
	v_mfma_f32_16x16x32_bf16 v[26:29], v[154:157], v[178:181], v[26:29]
	v_mfma_f32_16x16x32_bf16 v[14:17], v[146:149], v[186:189], v[14:17]
	v_mfma_f32_16x16x32_bf16 v[10:13], v[154:157], v[186:189], v[10:13]
	v_mfma_f32_16x16x32_bf16 v[62:65], v[150:153], v[166:169], v[62:65]
	v_mfma_f32_16x16x32_bf16 v[58:61], v[158:161], v[166:169], v[58:61]
	v_mfma_f32_16x16x32_bf16 v[46:49], v[150:153], v[174:177], v[46:49]
	v_mfma_f32_16x16x32_bf16 v[42:45], v[158:161], v[174:177], v[42:45]
	v_mfma_f32_16x16x32_bf16 v[30:33], v[150:153], v[182:185], v[30:33]
	v_mfma_f32_16x16x32_bf16 v[26:29], v[158:161], v[182:185], v[26:29]
	v_mfma_f32_16x16x32_bf16 v[14:17], v[150:153], v[190:193], v[14:17]
	v_mfma_f32_16x16x32_bf16 v[10:13], v[158:161], v[190:193], v[10:13]

	s_barrier
	s_add_i32 s50, s50, 0x20080
	s_add_i32 s51, s40, s19
	v_add_u32_e32 v146, s50, v1
	s_mov_b32 m0, s51
	s_nop 0
	global_load_lds_dwordx4 v146, s[10:11]
	v_add_u32_e32 v146, s50, v138
	s_add_i32 m0, s51, 0x2000
	s_nop 0
	global_load_lds_dwordx4 v146, s[10:11]
	s_waitcnt vmcnt(6)
	s_barrier

	v_mfma_f32_16x16x32_bf16 v[54:57], v[194:197], v[162:165], v[54:57]
	v_mfma_f32_16x16x32_bf16 v[50:53], v[202:205], v[162:165], v[50:53]
	v_mfma_f32_16x16x32_bf16 v[38:41], v[194:197], v[170:173], v[38:41]
	v_mfma_f32_16x16x32_bf16 v[34:37], v[202:205], v[170:173], v[34:37]
	v_mfma_f32_16x16x32_bf16 v[22:25], v[194:197], v[178:181], v[22:25]
	v_mfma_f32_16x16x32_bf16 v[18:21], v[202:205], v[178:181], v[18:21]
	v_mfma_f32_16x16x32_bf16 v[6:9], v[194:197], v[186:189], v[6:9]
	v_mfma_f32_16x16x32_bf16 v[2:5], v[202:205], v[186:189], v[2:5]
	v_mfma_f32_16x16x32_bf16 v[54:57], v[198:201], v[166:169], v[54:57]
	v_mfma_f32_16x16x32_bf16 v[50:53], v[206:209], v[166:169], v[50:53]
	v_mfma_f32_16x16x32_bf16 v[38:41], v[198:201], v[174:177], v[38:41]
	v_mfma_f32_16x16x32_bf16 v[34:37], v[206:209], v[174:177], v[34:37]
	v_mfma_f32_16x16x32_bf16 v[22:25], v[198:201], v[182:185], v[22:25]
	v_mfma_f32_16x16x32_bf16 v[18:21], v[206:209], v[182:185], v[18:21]
	v_mfma_f32_16x16x32_bf16 v[6:9], v[198:201], v[190:193], v[6:9]
	v_mfma_f32_16x16x32_bf16 v[2:5], v[206:209], v[190:193], v[2:5]

	s_add_i32 s49, s49, 2
	s_addk_i32 s47, 0x100
	s_addk_i32 s48, 0x100
	s_cmp_ge_i32 s49, s28
	s_barrier
	s_cbranch_scc0 .LBB0_620
	s_branch .LBB0_615

.LBB0_638:
	s_add_i32 s47, s4, 0x80
	s_cmp_eq_u32 s38, s7
	s_cselect_b32 s49, s2, s47
	s_cselect_b32 s47, s3, s5
	s_add_i32 s50, 0, 0x10000
	v_add_u32_e32 v146, s50, v159
	ds_read_b128 v[138:141], v146
	ds_read_b128 v[142:145], v146 offset:1024
	ds_read_b128 v[166:169], v146 offset:2048
	ds_read_b128 v[170:173], v146 offset:3072
	s_or_b32 s48, s49, 0x80
	v_add_u32_e32 v146, s4, v131
	s_add_i32 m0, s28, 0xc000
	ds_read_b128 v[174:177], v163
	ds_read_b128 v[178:181], v163 offset:1024
	ds_read_b128 v[182:185], v163 offset:2048
	ds_read_b128 v[186:189], v163 offset:3072
	ds_read_b128 v[190:193], v163 offset:4096
	ds_read_b128 v[194:197], v163 offset:5120
	ds_read_b128 v[198:201], v163 offset:6144
	ds_read_b128 v[202:205], v163 offset:7168
	global_load_lds_dwordx4 v146, s[10:11]
	v_add_u32_e32 v146, s4, v133
	s_add_i32 m0, s28, 0xe000
	s_nop 0
	global_load_lds_dwordx4 v146, s[10:11]
	s_waitcnt lgkmcnt(8)
	s_barrier
	s_waitcnt lgkmcnt(0)


	v_mfma_f32_16x16x32_bf16 v[126:129], v[138:141], v[174:177], v[126:129]
	v_mfma_f32_16x16x32_bf16 v[122:125], v[166:169], v[174:177], v[122:125]
	v_mfma_f32_16x16x32_bf16 v[110:113], v[138:141], v[182:185], v[110:113]
	v_mfma_f32_16x16x32_bf16 v[106:109], v[166:169], v[182:185], v[106:109]
	v_mfma_f32_16x16x32_bf16 v[94:97], v[138:141], v[190:193], v[94:97]
	v_mfma_f32_16x16x32_bf16 v[90:93], v[166:169], v[190:193], v[90:93]
	v_mfma_f32_16x16x32_bf16 v[78:81], v[138:141], v[198:201], v[78:81]
	v_mfma_f32_16x16x32_bf16 v[74:77], v[166:169], v[198:201], v[74:77]
	v_mfma_f32_16x16x32_bf16 v[126:129], v[142:145], v[178:181], v[126:129]
	v_mfma_f32_16x16x32_bf16 v[122:125], v[170:173], v[178:181], v[122:125]
	v_mfma_f32_16x16x32_bf16 v[110:113], v[142:145], v[186:189], v[110:113]
	v_mfma_f32_16x16x32_bf16 v[106:109], v[170:173], v[186:189], v[106:109]
	v_mfma_f32_16x16x32_bf16 v[94:97], v[142:145], v[194:197], v[94:97]
	v_mfma_f32_16x16x32_bf16 v[90:93], v[170:173], v[194:197], v[90:93]
	v_mfma_f32_16x16x32_bf16 v[78:81], v[142:145], v[202:205], v[78:81]
	v_mfma_f32_16x16x32_bf16 v[74:77], v[170:173], v[202:205], v[74:77]

	s_barrier
	s_add_i32 s50, s50, s27
	v_add_u32_e32 v146, s47, v1
	s_mov_b32 m0, s50
	ds_read_b128 v[206:209], v164
	ds_read_b128 v[210:213], v164 offset:1024
	ds_read_b128 v[214:217], v164 offset:2048
	ds_read_b128 v[218:221], v164 offset:3072
	global_load_lds_dwordx4 v146, s[14:15]
	v_add_u32_e32 v146, s47, v147
	s_add_i32 m0, s50, 0x2000
	s_nop 0
	global_load_lds_dwordx4 v146, s[14:15]
	s_barrier
	s_waitcnt lgkmcnt(0)


	v_mfma_f32_16x16x32_bf16 v[118:121], v[206:209], v[174:177], v[118:121]
	v_mfma_f32_16x16x32_bf16 v[114:117], v[214:217], v[174:177], v[114:117]
	v_mfma_f32_16x16x32_bf16 v[102:105], v[206:209], v[182:185], v[102:105]
	v_mfma_f32_16x16x32_bf16 v[98:101], v[214:217], v[182:185], v[98:101]
	v_mfma_f32_16x16x32_bf16 v[86:89], v[206:209], v[190:193], v[86:89]
	v_mfma_f32_16x16x32_bf16 v[82:85], v[214:217], v[190:193], v[82:85]
	v_mfma_f32_16x16x32_bf16 v[70:73], v[206:209], v[198:201], v[70:73]
	v_mfma_f32_16x16x32_bf16 v[66:69], v[214:217], v[198:201], v[66:69]
	v_mfma_f32_16x16x32_bf16 v[118:121], v[210:213], v[178:181], v[118:121]
	v_mfma_f32_16x16x32_bf16 v[114:117], v[218:221], v[178:181], v[114:117]
	v_mfma_f32_16x16x32_bf16 v[102:105], v[210:213], v[186:189], v[102:105]
	v_mfma_f32_16x16x32_bf16 v[98:101], v[218:221], v[186:189], v[98:101]
	v_mfma_f32_16x16x32_bf16 v[86:89], v[210:213], v[194:197], v[86:89]
	v_mfma_f32_16x16x32_bf16 v[82:85], v[218:221], v[194:197], v[82:85]
	v_mfma_f32_16x16x32_bf16 v[70:73], v[210:213], v[202:205], v[70:73]
	v_mfma_f32_16x16x32_bf16 v[66:69], v[218:221], v[202:205], v[66:69]

	s_mov_b32 m0, s28
	v_add_u32_e32 v146, s49, v130
	s_barrier
	ds_read_b128 v[174:177], v163 offset:16384
	ds_read_b128 v[178:181], v163 offset:17408
	ds_read_b128 v[182:185], v163 offset:18432
	ds_read_b128 v[186:189], v163 offset:19456
	ds_read_b128 v[190:193], v163 offset:20480
	ds_read_b128 v[194:197], v163 offset:21504
	ds_read_b128 v[198:201], v163 offset:22528
	ds_read_b128 v[202:205], v163 offset:23552
	global_load_lds_dwordx4 v146, s[10:11]
	v_add_u32_e32 v146, s49, v132
	s_mov_b32 m0, s29
	s_nop 0
	global_load_lds_dwordx4 v146, s[10:11]
	s_barrier
	s_waitcnt lgkmcnt(0)


	v_mfma_f32_16x16x32_bf16 v[62:65], v[138:141], v[174:177], v[62:65]
	v_mfma_f32_16x16x32_bf16 v[58:61], v[166:169], v[174:177], v[58:61]
	v_mfma_f32_16x16x32_bf16 v[46:49], v[138:141], v[182:185], v[46:49]
	v_mfma_f32_16x16x32_bf16 v[42:45], v[166:169], v[182:185], v[42:45]
	v_mfma_f32_16x16x32_bf16 v[30:33], v[138:141], v[190:193], v[30:33]
	v_mfma_f32_16x16x32_bf16 v[26:29], v[166:169], v[190:193], v[26:29]
	v_mfma_f32_16x16x32_bf16 v[14:17], v[138:141], v[198:201], v[14:17]
	v_mfma_f32_16x16x32_bf16 v[10:13], v[166:169], v[198:201], v[10:13]
	v_mfma_f32_16x16x32_bf16 v[62:65], v[142:145], v[178:181], v[62:65]
	v_mfma_f32_16x16x32_bf16 v[58:61], v[170:173], v[178:181], v[58:61]
	v_mfma_f32_16x16x32_bf16 v[46:49], v[142:145], v[186:189], v[46:49]
	v_mfma_f32_16x16x32_bf16 v[42:45], v[170:173], v[186:189], v[42:45]
	v_mfma_f32_16x16x32_bf16 v[30:33], v[142:145], v[194:197], v[30:33]
	v_mfma_f32_16x16x32_bf16 v[26:29], v[170:173], v[194:197], v[26:29]
	v_mfma_f32_16x16x32_bf16 v[14:17], v[142:145], v[202:205], v[14:17]
	v_mfma_f32_16x16x32_bf16 v[10:13], v[170:173], v[202:205], v[10:13]

	s_barrier
	s_add_i32 s50, s47, 0x10000
	s_add_i32 s51, s39, s27
	v_add_u32_e32 v138, s50, v1
	s_mov_b32 m0, s51
	s_nop 0
	global_load_lds_dwordx4 v138, s[14:15]
	v_add_u32_e32 v138, s50, v147
	s_add_i32 m0, s51, 0x2000
	s_nop 0
	global_load_lds_dwordx4 v138, s[14:15]
	s_waitcnt vmcnt(6)
	s_barrier

	v_mfma_f32_16x16x32_bf16 v[54:57], v[206:209], v[174:177], v[54:57]
	v_mfma_f32_16x16x32_bf16 v[50:53], v[214:217], v[174:177], v[50:53]
	v_mfma_f32_16x16x32_bf16 v[38:41], v[206:209], v[182:185], v[38:41]
	v_mfma_f32_16x16x32_bf16 v[34:37], v[214:217], v[182:185], v[34:37]
	v_mfma_f32_16x16x32_bf16 v[22:25], v[206:209], v[190:193], v[22:25]
	v_mfma_f32_16x16x32_bf16 v[18:21], v[214:217], v[190:193], v[18:21]
	v_mfma_f32_16x16x32_bf16 v[6:9], v[206:209], v[198:201], v[6:9]
	v_mfma_f32_16x16x32_bf16 v[2:5], v[214:217], v[198:201], v[2:5]
	v_mfma_f32_16x16x32_bf16 v[54:57], v[210:213], v[178:181], v[54:57]
	v_mfma_f32_16x16x32_bf16 v[50:53], v[218:221], v[178:181], v[50:53]
	v_mfma_f32_16x16x32_bf16 v[38:41], v[210:213], v[186:189], v[38:41]
	v_mfma_f32_16x16x32_bf16 v[34:37], v[218:221], v[186:189], v[34:37]
	v_mfma_f32_16x16x32_bf16 v[22:25], v[210:213], v[194:197], v[22:25]
	v_mfma_f32_16x16x32_bf16 v[18:21], v[218:221], v[194:197], v[18:21]
	v_mfma_f32_16x16x32_bf16 v[6:9], v[210:213], v[202:205], v[6:9]
	v_mfma_f32_16x16x32_bf16 v[2:5], v[218:221], v[202:205], v[2:5]

	s_add_i32 s50, 0, 0x18000
	v_add_u32_e32 v146, s50, v159
	s_barrier
	ds_read_b128 v[138:141], v146
	ds_read_b128 v[142:145], v146 offset:1024
	ds_read_b128 v[166:169], v146 offset:2048
	ds_read_b128 v[170:173], v146 offset:3072
	s_mov_b32 m0, s30
	v_add_u32_e32 v146, s49, v131
	ds_read_b128 v[174:177], v163 offset:32768
	ds_read_b128 v[178:181], v163 offset:33792
	ds_read_b128 v[182:185], v163 offset:34816
	ds_read_b128 v[186:189], v163 offset:35840
	ds_read_b128 v[190:193], v163 offset:36864
	ds_read_b128 v[194:197], v163 offset:37888
	ds_read_b128 v[198:201], v163 offset:38912
	ds_read_b128 v[202:205], v163 offset:39936
	global_load_lds_dwordx4 v146, s[10:11]
	v_add_u32_e32 v146, s49, v133
	s_mov_b32 m0, s31
	s_nop 0
	global_load_lds_dwordx4 v146, s[10:11]
	s_waitcnt lgkmcnt(8)
	s_barrier
	s_waitcnt lgkmcnt(0)


	v_mfma_f32_16x16x32_bf16 v[126:129], v[138:141], v[174:177], v[126:129]
	v_mfma_f32_16x16x32_bf16 v[122:125], v[166:169], v[174:177], v[122:125]
	v_mfma_f32_16x16x32_bf16 v[110:113], v[138:141], v[182:185], v[110:113]
	v_mfma_f32_16x16x32_bf16 v[106:109], v[166:169], v[182:185], v[106:109]
	v_mfma_f32_16x16x32_bf16 v[94:97], v[138:141], v[190:193], v[94:97]
	v_mfma_f32_16x16x32_bf16 v[90:93], v[166:169], v[190:193], v[90:93]
	v_mfma_f32_16x16x32_bf16 v[78:81], v[138:141], v[198:201], v[78:81]
	v_mfma_f32_16x16x32_bf16 v[74:77], v[166:169], v[198:201], v[74:77]
	v_mfma_f32_16x16x32_bf16 v[126:129], v[142:145], v[178:181], v[126:129]
	v_mfma_f32_16x16x32_bf16 v[122:125], v[170:173], v[178:181], v[122:125]
	v_mfma_f32_16x16x32_bf16 v[110:113], v[142:145], v[186:189], v[110:113]
	v_mfma_f32_16x16x32_bf16 v[106:109], v[170:173], v[186:189], v[106:109]
	v_mfma_f32_16x16x32_bf16 v[94:97], v[142:145], v[194:197], v[94:97]
	v_mfma_f32_16x16x32_bf16 v[90:93], v[170:173], v[194:197], v[90:93]
	v_mfma_f32_16x16x32_bf16 v[78:81], v[142:145], v[202:205], v[78:81]
	v_mfma_f32_16x16x32_bf16 v[74:77], v[170:173], v[202:205], v[74:77]

	s_barrier
	s_add_i32 s49, 0, 0x1c000
	v_add_u32_e32 v146, s49, v159
	s_or_b32 s51, s47, 0x80
	s_add_i32 s50, s50, s27
	ds_read_b128 v[206:209], v146
	ds_read_b128 v[210:213], v146 offset:1024
	ds_read_b128 v[214:217], v146 offset:2048
	ds_read_b128 v[218:221], v146 offset:3072
	v_add_u32_e32 v146, s51, v1
	s_mov_b32 m0, s50
	s_nop 0
	global_load_lds_dwordx4 v146, s[14:15]
	v_add_u32_e32 v146, s51, v147
	s_add_i32 m0, s50, 0x2000
	s_nop 0
	global_load_lds_dwordx4 v146, s[14:15]
	s_barrier
	s_waitcnt lgkmcnt(0)


	v_mfma_f32_16x16x32_bf16 v[118:121], v[206:209], v[174:177], v[118:121]
	v_mfma_f32_16x16x32_bf16 v[114:117], v[214:217], v[174:177], v[114:117]
	v_mfma_f32_16x16x32_bf16 v[102:105], v[206:209], v[182:185], v[102:105]
	v_mfma_f32_16x16x32_bf16 v[98:101], v[214:217], v[182:185], v[98:101]
	v_mfma_f32_16x16x32_bf16 v[86:89], v[206:209], v[190:193], v[86:89]
	v_mfma_f32_16x16x32_bf16 v[82:85], v[214:217], v[190:193], v[82:85]
	v_mfma_f32_16x16x32_bf16 v[70:73], v[206:209], v[198:201], v[70:73]
	v_mfma_f32_16x16x32_bf16 v[66:69], v[214:217], v[198:201], v[66:69]
	v_mfma_f32_16x16x32_bf16 v[118:121], v[210:213], v[178:181], v[118:121]
	v_mfma_f32_16x16x32_bf16 v[114:117], v[218:221], v[178:181], v[114:117]
	v_mfma_f32_16x16x32_bf16 v[102:105], v[210:213], v[186:189], v[102:105]
	v_mfma_f32_16x16x32_bf16 v[98:101], v[218:221], v[186:189], v[98:101]
	v_mfma_f32_16x16x32_bf16 v[86:89], v[210:213], v[194:197], v[86:89]
	v_mfma_f32_16x16x32_bf16 v[82:85], v[218:221], v[194:197], v[82:85]
	v_mfma_f32_16x16x32_bf16 v[70:73], v[210:213], v[202:205], v[70:73]
	v_mfma_f32_16x16x32_bf16 v[66:69], v[218:221], v[202:205], v[66:69]

	s_mov_b32 m0, s36
	v_add_u32_e32 v146, s48, v130
	s_barrier
	ds_read_b128 v[174:177], v163 offset:49152
	ds_read_b128 v[178:181], v163 offset:50176
	ds_read_b128 v[182:185], v163 offset:51200
	ds_read_b128 v[186:189], v163 offset:52224
	ds_read_b128 v[190:193], v163 offset:53248
	ds_read_b128 v[194:197], v163 offset:54272
	ds_read_b128 v[198:201], v163 offset:55296
	ds_read_b128 v[202:205], v163 offset:56320
	global_load_lds_dwordx4 v146, s[10:11]
	v_add_u32_e32 v146, s48, v132
	s_mov_b32 m0, s37
	s_nop 0
	global_load_lds_dwordx4 v146, s[10:11]
	s_barrier
	s_waitcnt lgkmcnt(0)


	v_mfma_f32_16x16x32_bf16 v[62:65], v[138:141], v[174:177], v[62:65]
	v_mfma_f32_16x16x32_bf16 v[58:61], v[166:169], v[174:177], v[58:61]
	v_mfma_f32_16x16x32_bf16 v[46:49], v[138:141], v[182:185], v[46:49]
	v_mfma_f32_16x16x32_bf16 v[42:45], v[166:169], v[182:185], v[42:45]
	v_mfma_f32_16x16x32_bf16 v[30:33], v[138:141], v[190:193], v[30:33]
	v_mfma_f32_16x16x32_bf16 v[26:29], v[166:169], v[190:193], v[26:29]
	v_mfma_f32_16x16x32_bf16 v[14:17], v[138:141], v[198:201], v[14:17]
	v_mfma_f32_16x16x32_bf16 v[10:13], v[166:169], v[198:201], v[10:13]
	v_mfma_f32_16x16x32_bf16 v[62:65], v[142:145], v[178:181], v[62:65]
	v_mfma_f32_16x16x32_bf16 v[58:61], v[170:173], v[178:181], v[58:61]
	v_mfma_f32_16x16x32_bf16 v[46:49], v[142:145], v[186:189], v[46:49]
	v_mfma_f32_16x16x32_bf16 v[42:45], v[170:173], v[186:189], v[42:45]
	v_mfma_f32_16x16x32_bf16 v[30:33], v[142:145], v[194:197], v[30:33]
	v_mfma_f32_16x16x32_bf16 v[26:29], v[170:173], v[194:197], v[26:29]
	v_mfma_f32_16x16x32_bf16 v[14:17], v[142:145], v[202:205], v[14:17]
	v_mfma_f32_16x16x32_bf16 v[10:13], v[170:173], v[202:205], v[10:13]

	s_barrier
	s_add_i32 s47, s47, 0x10080
	s_add_i32 s48, s49, s27
	v_add_u32_e32 v138, s47, v1
	s_mov_b32 m0, s48
	s_nop 0
	global_load_lds_dwordx4 v138, s[14:15]
	v_add_u32_e32 v138, s47, v147
	s_add_i32 m0, s48, 0x2000
	s_nop 0
	global_load_lds_dwordx4 v138, s[14:15]
	s_waitcnt vmcnt(6)
	s_barrier

	v_mfma_f32_16x16x32_bf16 v[54:57], v[206:209], v[174:177], v[54:57]
	v_mfma_f32_16x16x32_bf16 v[50:53], v[214:217], v[174:177], v[50:53]
	v_mfma_f32_16x16x32_bf16 v[38:41], v[206:209], v[182:185], v[38:41]
	v_mfma_f32_16x16x32_bf16 v[34:37], v[214:217], v[182:185], v[34:37]
	v_mfma_f32_16x16x32_bf16 v[22:25], v[206:209], v[190:193], v[22:25]
	v_mfma_f32_16x16x32_bf16 v[18:21], v[214:217], v[190:193], v[18:21]
	v_mfma_f32_16x16x32_bf16 v[6:9], v[206:209], v[198:201], v[6:9]
	v_mfma_f32_16x16x32_bf16 v[2:5], v[214:217], v[198:201], v[2:5]
	v_mfma_f32_16x16x32_bf16 v[54:57], v[210:213], v[178:181], v[54:57]
	v_mfma_f32_16x16x32_bf16 v[50:53], v[218:221], v[178:181], v[50:53]
	v_mfma_f32_16x16x32_bf16 v[38:41], v[210:213], v[186:189], v[38:41]
	v_mfma_f32_16x16x32_bf16 v[34:37], v[218:221], v[186:189], v[34:37]
	v_mfma_f32_16x16x32_bf16 v[22:25], v[210:213], v[194:197], v[22:25]
	v_mfma_f32_16x16x32_bf16 v[18:21], v[218:221], v[194:197], v[18:21]
	v_mfma_f32_16x16x32_bf16 v[6:9], v[210:213], v[202:205], v[6:9]
	v_mfma_f32_16x16x32_bf16 v[2:5], v[218:221], v[202:205], v[2:5]

	s_add_i32 s7, s7, 2
	s_addk_i32 s4, 0x100
	s_addk_i32 s5, 0x100
	s_cmp_ge_i32 s7, s34
	s_barrier
	s_cbranch_scc0 .LBB0_638
	s_branch .LBB0_629

.LBB0_1154:
	ds_read_b128 v[146:149], v141
	ds_read_b128 v[150:153], v141 offset:1024
	ds_read_b128 v[154:157], v141 offset:2048
	ds_read_b128 v[158:161], v141 offset:3072
	s_add_i32 s44, s41, 0x80
	s_cmp_eq_u32 s24, s43
	s_cselect_b32 s46, s10, s44
	s_cselect_b32 s44, s11, s42
	s_or_b32 s45, s46, 0x80
	s_mov_b32 m0, s25
	v_add_u32_e32 v194, s41, v137
	ds_read_b128 v[162:165], v142
	ds_read_b128 v[166:169], v142 offset:1024
	ds_read_b128 v[170:173], v142 offset:2048
	ds_read_b128 v[174:177], v142 offset:3072
	ds_read_b128 v[178:181], v142 offset:4096
	ds_read_b128 v[182:185], v142 offset:5120
	ds_read_b128 v[186:189], v142 offset:6144
	ds_read_b128 v[190:193], v142 offset:7168
	global_load_lds_dwordx4 v194, s[4:5]
	v_add_u32_e32 v194, s41, v138
	s_mov_b32 m0, s26
	s_nop 0
	global_load_lds_dwordx4 v194, s[4:5]
	s_waitcnt lgkmcnt(8)
	s_barrier
	s_waitcnt lgkmcnt(0)


	v_mfma_f32_16x16x32_bf16 v[122:125], v[146:149], v[162:165], v[122:125]
	v_mfma_f32_16x16x32_bf16 v[126:129], v[154:157], v[162:165], v[126:129]
	v_mfma_f32_16x16x32_bf16 v[110:113], v[146:149], v[170:173], v[110:113]
	v_mfma_f32_16x16x32_bf16 v[106:109], v[154:157], v[170:173], v[106:109]
	v_mfma_f32_16x16x32_bf16 v[94:97], v[146:149], v[178:181], v[94:97]
	v_mfma_f32_16x16x32_bf16 v[90:93], v[154:157], v[178:181], v[90:93]
	v_mfma_f32_16x16x32_bf16 v[78:81], v[146:149], v[186:189], v[78:81]
	v_mfma_f32_16x16x32_bf16 v[74:77], v[154:157], v[186:189], v[74:77]
	v_mfma_f32_16x16x32_bf16 v[122:125], v[150:153], v[166:169], v[122:125]
	v_mfma_f32_16x16x32_bf16 v[126:129], v[158:161], v[166:169], v[126:129]
	v_mfma_f32_16x16x32_bf16 v[110:113], v[150:153], v[174:177], v[110:113]
	v_mfma_f32_16x16x32_bf16 v[106:109], v[158:161], v[174:177], v[106:109]
	v_mfma_f32_16x16x32_bf16 v[94:97], v[150:153], v[182:185], v[94:97]
	v_mfma_f32_16x16x32_bf16 v[90:93], v[158:161], v[182:185], v[90:93]
	v_mfma_f32_16x16x32_bf16 v[78:81], v[150:153], v[190:193], v[78:81]
	v_mfma_f32_16x16x32_bf16 v[74:77], v[158:161], v[190:193], v[74:77]

	s_barrier
	s_mov_b32 m0, s28
	v_add_u32_e32 v210, s44, v1
	ds_read_b128 v[194:197], v143
	ds_read_b128 v[198:201], v143 offset:1024
	ds_read_b128 v[202:205], v143 offset:2048
	ds_read_b128 v[206:209], v143 offset:3072
	global_load_lds_dwordx4 v210, s[6:7]
	v_add_u32_e32 v210, s44, v134
	s_mov_b32 m0, s29
	s_nop 0
	global_load_lds_dwordx4 v210, s[6:7]
	s_barrier
	s_waitcnt lgkmcnt(0)


	v_mfma_f32_16x16x32_bf16 v[118:121], v[194:197], v[162:165], v[118:121]
	v_mfma_f32_16x16x32_bf16 v[114:117], v[202:205], v[162:165], v[114:117]
	v_mfma_f32_16x16x32_bf16 v[102:105], v[194:197], v[170:173], v[102:105]
	v_mfma_f32_16x16x32_bf16 v[98:101], v[202:205], v[170:173], v[98:101]
	v_mfma_f32_16x16x32_bf16 v[86:89], v[194:197], v[178:181], v[86:89]
	v_mfma_f32_16x16x32_bf16 v[82:85], v[202:205], v[178:181], v[82:85]
	v_mfma_f32_16x16x32_bf16 v[70:73], v[194:197], v[186:189], v[70:73]
	v_mfma_f32_16x16x32_bf16 v[66:69], v[202:205], v[186:189], v[66:69]
	v_mfma_f32_16x16x32_bf16 v[118:121], v[198:201], v[166:169], v[118:121]
	v_mfma_f32_16x16x32_bf16 v[114:117], v[206:209], v[166:169], v[114:117]
	v_mfma_f32_16x16x32_bf16 v[102:105], v[198:201], v[174:177], v[102:105]
	v_mfma_f32_16x16x32_bf16 v[98:101], v[206:209], v[174:177], v[98:101]
	v_mfma_f32_16x16x32_bf16 v[86:89], v[198:201], v[182:185], v[86:89]
	v_mfma_f32_16x16x32_bf16 v[82:85], v[206:209], v[182:185], v[82:85]
	v_mfma_f32_16x16x32_bf16 v[70:73], v[198:201], v[190:193], v[70:73]
	v_mfma_f32_16x16x32_bf16 v[66:69], v[206:209], v[190:193], v[66:69]

	s_mov_b32 m0, s15
	v_add_u32_e32 v210, s46, v135
	s_barrier
	ds_read_b128 v[162:165], v142 offset:16384
	ds_read_b128 v[166:169], v142 offset:17408
	ds_read_b128 v[170:173], v142 offset:18432
	ds_read_b128 v[174:177], v142 offset:19456
	ds_read_b128 v[178:181], v142 offset:20480
	ds_read_b128 v[182:185], v142 offset:21504
	ds_read_b128 v[186:189], v142 offset:22528
	ds_read_b128 v[190:193], v142 offset:23552
	global_load_lds_dwordx4 v210, s[4:5]
	v_add_u32_e32 v210, s46, v136
	s_mov_b32 m0, s16
	s_nop 0
	global_load_lds_dwordx4 v210, s[4:5]
	s_barrier
	s_waitcnt lgkmcnt(0)


	v_mfma_f32_16x16x32_bf16 v[62:65], v[146:149], v[162:165], v[62:65]
	v_mfma_f32_16x16x32_bf16 v[58:61], v[154:157], v[162:165], v[58:61]
	v_mfma_f32_16x16x32_bf16 v[46:49], v[146:149], v[170:173], v[46:49]
	v_mfma_f32_16x16x32_bf16 v[42:45], v[154:157], v[170:173], v[42:45]
	v_mfma_f32_16x16x32_bf16 v[30:33], v[146:149], v[178:181], v[30:33]
	v_mfma_f32_16x16x32_bf16 v[26:29], v[154:157], v[178:181], v[26:29]
	v_mfma_f32_16x16x32_bf16 v[14:17], v[146:149], v[186:189], v[14:17]
	v_mfma_f32_16x16x32_bf16 v[10:13], v[154:157], v[186:189], v[10:13]
	v_mfma_f32_16x16x32_bf16 v[62:65], v[150:153], v[166:169], v[62:65]
	v_mfma_f32_16x16x32_bf16 v[58:61], v[158:161], v[166:169], v[58:61]
	v_mfma_f32_16x16x32_bf16 v[46:49], v[150:153], v[174:177], v[46:49]
	v_mfma_f32_16x16x32_bf16 v[42:45], v[158:161], v[174:177], v[42:45]
	v_mfma_f32_16x16x32_bf16 v[30:33], v[150:153], v[182:185], v[30:33]
	v_mfma_f32_16x16x32_bf16 v[26:29], v[158:161], v[182:185], v[26:29]
	v_mfma_f32_16x16x32_bf16 v[14:17], v[150:153], v[190:193], v[14:17]
	v_mfma_f32_16x16x32_bf16 v[10:13], v[158:161], v[190:193], v[10:13]

	s_barrier
	s_add_i32 s47, s44, 0x18000
	s_mov_b32 m0, s30
	v_add_u32_e32 v146, s47, v1
	global_load_lds_dwordx4 v146, s[6:7]
	v_add_u32_e32 v146, s47, v134
	s_mov_b32 m0, s31
	s_nop 0
	global_load_lds_dwordx4 v146, s[6:7]
	s_waitcnt vmcnt(6)
	s_barrier

	v_mfma_f32_16x16x32_bf16 v[54:57], v[194:197], v[162:165], v[54:57]
	v_mfma_f32_16x16x32_bf16 v[50:53], v[202:205], v[162:165], v[50:53]
	v_mfma_f32_16x16x32_bf16 v[38:41], v[194:197], v[170:173], v[38:41]
	v_mfma_f32_16x16x32_bf16 v[34:37], v[202:205], v[170:173], v[34:37]
	v_mfma_f32_16x16x32_bf16 v[22:25], v[194:197], v[178:181], v[22:25]
	v_mfma_f32_16x16x32_bf16 v[18:21], v[202:205], v[178:181], v[18:21]
	v_mfma_f32_16x16x32_bf16 v[6:9], v[194:197], v[186:189], v[6:9]
	v_mfma_f32_16x16x32_bf16 v[2:5], v[202:205], v[186:189], v[2:5]
	v_mfma_f32_16x16x32_bf16 v[54:57], v[198:201], v[166:169], v[54:57]
	v_mfma_f32_16x16x32_bf16 v[50:53], v[206:209], v[166:169], v[50:53]
	v_mfma_f32_16x16x32_bf16 v[38:41], v[198:201], v[174:177], v[38:41]
	v_mfma_f32_16x16x32_bf16 v[34:37], v[206:209], v[174:177], v[34:37]
	v_mfma_f32_16x16x32_bf16 v[22:25], v[198:201], v[182:185], v[22:25]
	v_mfma_f32_16x16x32_bf16 v[18:21], v[206:209], v[182:185], v[18:21]
	v_mfma_f32_16x16x32_bf16 v[6:9], v[198:201], v[190:193], v[6:9]
	v_mfma_f32_16x16x32_bf16 v[2:5], v[206:209], v[190:193], v[2:5]

	s_barrier
	ds_read_b128 v[146:149], v144
	ds_read_b128 v[150:153], v144 offset:1024
	ds_read_b128 v[154:157], v144 offset:2048
	ds_read_b128 v[158:161], v144 offset:3072
	s_mov_b32 m0, s17
	v_add_u32_e32 v194, s46, v137
	ds_read_b128 v[162:165], v142 offset:32768
	ds_read_b128 v[166:169], v142 offset:33792
	ds_read_b128 v[170:173], v142 offset:34816
	ds_read_b128 v[174:177], v142 offset:35840
	ds_read_b128 v[178:181], v142 offset:36864
	ds_read_b128 v[182:185], v142 offset:37888
	ds_read_b128 v[186:189], v142 offset:38912
	ds_read_b128 v[190:193], v142 offset:39936
	global_load_lds_dwordx4 v194, s[4:5]
	v_add_u32_e32 v194, s46, v138
	s_mov_b32 m0, s18
	s_nop 0
	global_load_lds_dwordx4 v194, s[4:5]
	s_waitcnt lgkmcnt(8)
	s_barrier
	s_waitcnt lgkmcnt(0)


	v_mfma_f32_16x16x32_bf16 v[122:125], v[146:149], v[162:165], v[122:125]
	v_mfma_f32_16x16x32_bf16 v[126:129], v[154:157], v[162:165], v[126:129]
	v_mfma_f32_16x16x32_bf16 v[110:113], v[146:149], v[170:173], v[110:113]
	v_mfma_f32_16x16x32_bf16 v[106:109], v[154:157], v[170:173], v[106:109]
	v_mfma_f32_16x16x32_bf16 v[94:97], v[146:149], v[178:181], v[94:97]
	v_mfma_f32_16x16x32_bf16 v[90:93], v[154:157], v[178:181], v[90:93]
	v_mfma_f32_16x16x32_bf16 v[78:81], v[146:149], v[186:189], v[78:81]
	v_mfma_f32_16x16x32_bf16 v[74:77], v[154:157], v[186:189], v[74:77]
	v_mfma_f32_16x16x32_bf16 v[122:125], v[150:153], v[166:169], v[122:125]
	v_mfma_f32_16x16x32_bf16 v[126:129], v[158:161], v[166:169], v[126:129]
	v_mfma_f32_16x16x32_bf16 v[110:113], v[150:153], v[174:177], v[110:113]
	v_mfma_f32_16x16x32_bf16 v[106:109], v[158:161], v[174:177], v[106:109]
	v_mfma_f32_16x16x32_bf16 v[94:97], v[150:153], v[182:185], v[94:97]
	v_mfma_f32_16x16x32_bf16 v[90:93], v[158:161], v[182:185], v[90:93]
	v_mfma_f32_16x16x32_bf16 v[78:81], v[150:153], v[190:193], v[78:81]
	v_mfma_f32_16x16x32_bf16 v[74:77], v[158:161], v[190:193], v[74:77]

	s_barrier
	s_or_b32 s46, s44, 0x80
	s_add_i32 s47, s33, s13
	v_add_u32_e32 v210, s46, v1
	s_mov_b32 m0, s47
	ds_read_b128 v[194:197], v145
	ds_read_b128 v[198:201], v145 offset:1024
	ds_read_b128 v[202:205], v145 offset:2048
	ds_read_b128 v[206:209], v145 offset:3072
	global_load_lds_dwordx4 v210, s[6:7]
	v_add_u32_e32 v210, s46, v134
	s_add_i32 m0, s47, 0x2000
	s_nop 0
	global_load_lds_dwordx4 v210, s[6:7]
	s_barrier
	s_waitcnt lgkmcnt(0)


	v_mfma_f32_16x16x32_bf16 v[118:121], v[194:197], v[162:165], v[118:121]
	v_mfma_f32_16x16x32_bf16 v[114:117], v[202:205], v[162:165], v[114:117]
	v_mfma_f32_16x16x32_bf16 v[102:105], v[194:197], v[170:173], v[102:105]
	v_mfma_f32_16x16x32_bf16 v[98:101], v[202:205], v[170:173], v[98:101]
	v_mfma_f32_16x16x32_bf16 v[86:89], v[194:197], v[178:181], v[86:89]
	v_mfma_f32_16x16x32_bf16 v[82:85], v[202:205], v[178:181], v[82:85]
	v_mfma_f32_16x16x32_bf16 v[70:73], v[194:197], v[186:189], v[70:73]
	v_mfma_f32_16x16x32_bf16 v[66:69], v[202:205], v[186:189], v[66:69]
	v_mfma_f32_16x16x32_bf16 v[118:121], v[198:201], v[166:169], v[118:121]
	v_mfma_f32_16x16x32_bf16 v[114:117], v[206:209], v[166:169], v[114:117]
	v_mfma_f32_16x16x32_bf16 v[102:105], v[198:201], v[174:177], v[102:105]
	v_mfma_f32_16x16x32_bf16 v[98:101], v[206:209], v[174:177], v[98:101]
	v_mfma_f32_16x16x32_bf16 v[86:89], v[198:201], v[182:185], v[86:89]
	v_mfma_f32_16x16x32_bf16 v[82:85], v[206:209], v[182:185], v[82:85]
	v_mfma_f32_16x16x32_bf16 v[70:73], v[198:201], v[190:193], v[70:73]
	v_mfma_f32_16x16x32_bf16 v[66:69], v[206:209], v[190:193], v[66:69]

	s_mov_b32 m0, s20
	v_add_u32_e32 v210, s45, v135
	s_barrier
	ds_read_b128 v[162:165], v142 offset:49152
	ds_read_b128 v[166:169], v142 offset:50176
	ds_read_b128 v[170:173], v142 offset:51200
	ds_read_b128 v[174:177], v142 offset:52224
	ds_read_b128 v[178:181], v142 offset:53248
	ds_read_b128 v[182:185], v142 offset:54272
	ds_read_b128 v[186:189], v142 offset:55296
	ds_read_b128 v[190:193], v142 offset:56320
	global_load_lds_dwordx4 v210, s[4:5]
	v_add_u32_e32 v210, s45, v136
	s_mov_b32 m0, s21
	s_nop 0
	global_load_lds_dwordx4 v210, s[4:5]
	s_barrier
	s_waitcnt lgkmcnt(0)


	v_mfma_f32_16x16x32_bf16 v[62:65], v[146:149], v[162:165], v[62:65]
	v_mfma_f32_16x16x32_bf16 v[58:61], v[154:157], v[162:165], v[58:61]
	v_mfma_f32_16x16x32_bf16 v[46:49], v[146:149], v[170:173], v[46:49]
	v_mfma_f32_16x16x32_bf16 v[42:45], v[154:157], v[170:173], v[42:45]
	v_mfma_f32_16x16x32_bf16 v[30:33], v[146:149], v[178:181], v[30:33]
	v_mfma_f32_16x16x32_bf16 v[26:29], v[154:157], v[178:181], v[26:29]
	v_mfma_f32_16x16x32_bf16 v[14:17], v[146:149], v[186:189], v[14:17]
	v_mfma_f32_16x16x32_bf16 v[10:13], v[154:157], v[186:189], v[10:13]
	v_mfma_f32_16x16x32_bf16 v[62:65], v[150:153], v[166:169], v[62:65]
	v_mfma_f32_16x16x32_bf16 v[58:61], v[158:161], v[166:169], v[58:61]
	v_mfma_f32_16x16x32_bf16 v[46:49], v[150:153], v[174:177], v[46:49]
	v_mfma_f32_16x16x32_bf16 v[42:45], v[158:161], v[174:177], v[42:45]
	v_mfma_f32_16x16x32_bf16 v[30:33], v[150:153], v[182:185], v[30:33]
	v_mfma_f32_16x16x32_bf16 v[26:29], v[158:161], v[182:185], v[26:29]
	v_mfma_f32_16x16x32_bf16 v[14:17], v[150:153], v[190:193], v[14:17]
	v_mfma_f32_16x16x32_bf16 v[10:13], v[158:161], v[190:193], v[10:13]

	s_barrier
	s_add_i32 s44, s44, 0x18080
	s_add_i32 s45, s34, s13
	v_add_u32_e32 v146, s44, v1
	s_mov_b32 m0, s45
	s_nop 0
	global_load_lds_dwordx4 v146, s[6:7]
	v_add_u32_e32 v146, s44, v134
	s_add_i32 m0, s45, 0x2000
	s_nop 0
	global_load_lds_dwordx4 v146, s[6:7]
	s_waitcnt vmcnt(6)
	s_barrier

	v_mfma_f32_16x16x32_bf16 v[54:57], v[194:197], v[162:165], v[54:57]
	v_mfma_f32_16x16x32_bf16 v[50:53], v[202:205], v[162:165], v[50:53]
	v_mfma_f32_16x16x32_bf16 v[38:41], v[194:197], v[170:173], v[38:41]
	v_mfma_f32_16x16x32_bf16 v[34:37], v[202:205], v[170:173], v[34:37]
	v_mfma_f32_16x16x32_bf16 v[22:25], v[194:197], v[178:181], v[22:25]
	v_mfma_f32_16x16x32_bf16 v[18:21], v[202:205], v[178:181], v[18:21]
	v_mfma_f32_16x16x32_bf16 v[6:9], v[194:197], v[186:189], v[6:9]
	v_mfma_f32_16x16x32_bf16 v[2:5], v[202:205], v[186:189], v[2:5]
	v_mfma_f32_16x16x32_bf16 v[54:57], v[198:201], v[166:169], v[54:57]
	v_mfma_f32_16x16x32_bf16 v[50:53], v[206:209], v[166:169], v[50:53]
	v_mfma_f32_16x16x32_bf16 v[38:41], v[198:201], v[174:177], v[38:41]
	v_mfma_f32_16x16x32_bf16 v[34:37], v[206:209], v[174:177], v[34:37]
	v_mfma_f32_16x16x32_bf16 v[22:25], v[198:201], v[182:185], v[22:25]
	v_mfma_f32_16x16x32_bf16 v[18:21], v[206:209], v[182:185], v[18:21]
	v_mfma_f32_16x16x32_bf16 v[6:9], v[198:201], v[190:193], v[6:9]
	v_mfma_f32_16x16x32_bf16 v[2:5], v[206:209], v[190:193], v[2:5]

	s_add_i32 s43, s43, 2
	s_addk_i32 s41, 0x100
	s_addk_i32 s42, 0x100
	s_cmp_ge_i32 s43, s22
	s_barrier
	s_cbranch_scc0 .LBB0_1154
	s_branch .LBB0_1149

.LBB0_1522:
	ds_read_b128 v[130:133], v162
	ds_read_b128 v[134:137], v162 offset:1024
	ds_read_b128 v[146:149], v162 offset:2048
	ds_read_b128 v[150:153], v162 offset:3072
	s_add_i32 s55, s52, 0x80
	s_cmp_eq_u32 s42, s54
	s_cselect_b32 s57, s4, s55
	s_cselect_b32 s55, s5, s53
	s_or_b32 s56, s57, 0x80
	s_mov_b32 m0, s44
	v_add_u32_e32 v66, s52, v157
	ds_read_b128 v[168:171], v163
	ds_read_b128 v[172:175], v163 offset:1024
	ds_read_b128 v[176:179], v163 offset:2048
	ds_read_b128 v[180:183], v163 offset:3072
	ds_read_b128 v[184:187], v163 offset:4096
	ds_read_b128 v[188:191], v163 offset:5120
	ds_read_b128 v[192:195], v163 offset:6144
	ds_read_b128 v[196:199], v163 offset:7168
	global_load_lds_dwordx4 v66, s[12:13]
	v_add_u32_e32 v66, s52, v158
	s_mov_b32 m0, s45
	s_nop 0
	global_load_lds_dwordx4 v66, s[12:13]
	s_waitcnt lgkmcnt(8)
	s_barrier
	s_waitcnt lgkmcnt(0)


	v_mfma_scale_f32_16x16x128_f8f6f4 v[118:121], v[130:137], v[168:175], v[118:121], v165, v164 op_sel_hi:[0,0,0]
	v_mfma_scale_f32_16x16x128_f8f6f4 v[122:125], v[146:153], v[168:175], v[122:125], v165, v164 op_sel_hi:[0,0,0]
	v_mfma_scale_f32_16x16x128_f8f6f4 v[138:141], v[130:137], v[176:183], v[110:113], v165, v164 op_sel_hi:[0,0,0]
	v_mfma_scale_f32_16x16x128_f8f6f4 v[200:203], v[146:153], v[176:183], v[102:105], v165, v164 op_sel_hi:[0,0,0]
	v_mfma_scale_f32_16x16x128_f8f6f4 v[204:207], v[130:137], v[184:191], v[94:97], v165, v164 op_sel_hi:[0,0,0]
	v_mfma_scale_f32_16x16x128_f8f6f4 v[208:211], v[146:153], v[184:191], v[90:93], v165, v164 op_sel_hi:[0,0,0]
	v_mfma_scale_f32_16x16x128_f8f6f4 v[212:215], v[130:137], v[192:199], v[78:81], v165, v164 op_sel_hi:[0,0,0]
	v_mfma_scale_f32_16x16x128_f8f6f4 v[216:219], v[146:153], v[192:199], v[74:77], v165, v164 op_sel_hi:[0,0,0]

	s_barrier
	s_add_i32 s58, s43, s31
	v_add_u32_e32 v66, s55, v1
	s_mov_b32 m0, s58
	s_nop 1
	ds_read_b128 v[74:77], v166
	ds_read_b128 v[78:81], v166 offset:1024
	ds_read_b128 v[90:93], v166 offset:2048
	ds_read_b128 v[94:97], v166 offset:3072
	global_load_lds_dwordx4 v66, s[10:11]
	v_add_u32_e32 v66, s55, v154
	s_add_i32 m0, s58, 0x2000
	s_nop 0
	global_load_lds_dwordx4 v66, s[10:11]
	s_barrier
	s_waitcnt lgkmcnt(0)


	v_mfma_scale_f32_16x16x128_f8f6f4 v[126:129], v[74:81], v[168:175], v[126:129], v165, v164 op_sel_hi:[0,0,0]
	v_mfma_scale_f32_16x16x128_f8f6f4 v[114:117], v[90:97], v[168:175], v[114:117], v165, v164 op_sel_hi:[0,0,0]
	v_mfma_scale_f32_16x16x128_f8f6f4 v[168:171], v[74:81], v[176:183], v[106:109], v165, v164 op_sel_hi:[0,0,0]
	v_mfma_scale_f32_16x16x128_f8f6f4 v[172:175], v[90:97], v[176:183], v[98:101], v165, v164 op_sel_hi:[0,0,0]
	v_mfma_scale_f32_16x16x128_f8f6f4 v[176:179], v[74:81], v[184:191], v[86:89], v165, v164 op_sel_hi:[0,0,0]
	v_mfma_scale_f32_16x16x128_f8f6f4 v[180:183], v[90:97], v[184:191], v[82:85], v165, v164 op_sel_hi:[0,0,0]
	v_mfma_scale_f32_16x16x128_f8f6f4 v[184:187], v[74:81], v[192:199], v[70:73], v165, v164 op_sel_hi:[0,0,0]
	v_mfma_scale_f32_16x16x128_f8f6f4 v[188:191], v[90:97], v[192:199], v[10:13], v165, v164 op_sel_hi:[0,0,0]

	s_mov_b32 m0, s33
	s_nop 4
	v_add_u32_e32 v10, s57, v155
	s_barrier
	ds_read_b128 v[66:69], v163 offset:16384
	ds_read_b128 v[70:73], v163 offset:17408
	ds_read_b128 v[82:85], v163 offset:18432
	ds_read_b128 v[86:89], v163 offset:19456
	ds_read_b128 v[98:101], v163 offset:20480
	ds_read_b128 v[102:105], v163 offset:21504
	ds_read_b128 v[106:109], v163 offset:22528
	ds_read_b128 v[110:113], v163 offset:23552
	global_load_lds_dwordx4 v10, s[12:13]
	v_add_u32_e32 v10, s57, v156
	s_mov_b32 m0, s34
	s_nop 0
	global_load_lds_dwordx4 v10, s[12:13]
	s_barrier
	s_waitcnt lgkmcnt(0)


	v_mfma_scale_f32_16x16x128_f8f6f4 v[62:65], v[130:137], v[66:73], v[62:65], v165, v164 op_sel_hi:[0,0,0]
	v_mfma_scale_f32_16x16x128_f8f6f4 v[58:61], v[146:153], v[66:73], v[58:61], v165, v164 op_sel_hi:[0,0,0]
	v_mfma_scale_f32_16x16x128_f8f6f4 v[232:235], v[146:153], v[106:113], v[232:235], v165, v164 op_sel_hi:[0,0,0]
	v_mfma_scale_f32_16x16x128_f8f6f4 v[192:195], v[130:137], v[82:89], v[46:49], v165, v164 op_sel_hi:[0,0,0]
	v_mfma_scale_f32_16x16x128_f8f6f4 v[196:199], v[146:153], v[82:89], v[42:45], v165, v164 op_sel_hi:[0,0,0]
	v_mfma_scale_f32_16x16x128_f8f6f4 v[220:223], v[130:137], v[98:105], v[30:33], v165, v164 op_sel_hi:[0,0,0]
	v_mfma_scale_f32_16x16x128_f8f6f4 v[224:227], v[146:153], v[98:105], v[26:29], v165, v164 op_sel_hi:[0,0,0]
	v_mfma_scale_f32_16x16x128_f8f6f4 v[228:231], v[130:137], v[106:113], v[14:17], v165, v164 op_sel_hi:[0,0,0]

	s_barrier
	s_add_i32 s58, s55, 0x40000
	s_add_i32 s59, s46, s31
	v_add_u32_e32 v10, s58, v1
	s_mov_b32 m0, s59
	s_nop 0
	global_load_lds_dwordx4 v10, s[10:11]
	v_add_u32_e32 v10, s58, v154
	s_add_i32 m0, s59, 0x2000
	s_nop 0
	global_load_lds_dwordx4 v10, s[10:11]
	s_waitcnt vmcnt(6)
	s_barrier

	v_mfma_scale_f32_16x16x128_f8f6f4 v[54:57], v[74:81], v[66:73], v[54:57], v165, v164 op_sel_hi:[0,0,0]
	v_mfma_scale_f32_16x16x128_f8f6f4 v[50:53], v[90:97], v[66:73], v[50:53], v165, v164 op_sel_hi:[0,0,0]
	v_mfma_scale_f32_16x16x128_f8f6f4 v[236:239], v[74:81], v[82:89], v[38:41], v165, v164 op_sel_hi:[0,0,0]
	v_mfma_scale_f32_16x16x128_f8f6f4 v[240:243], v[90:97], v[82:89], v[34:37], v165, v164 op_sel_hi:[0,0,0]
	v_mfma_scale_f32_16x16x128_f8f6f4 v[244:247], v[74:81], v[98:105], v[22:25], v165, v164 op_sel_hi:[0,0,0]
	v_mfma_scale_f32_16x16x128_f8f6f4 v[248:251], v[90:97], v[98:105], v[18:21], v165, v164 op_sel_hi:[0,0,0]
	v_mfma_scale_f32_16x16x128_f8f6f4 v[142:145], v[74:81], v[106:113], v[6:9], v165, v164 op_sel_hi:[0,0,0]
	v_mfma_scale_f32_16x16x128_f8f6f4 v[66:69], v[90:97], v[106:113], v[2:5], v165, v164 op_sel_hi:[0,0,0]

	s_add_i32 s58, 0, 0x18000
	v_add_u32_e32 v10, s58, v161
	s_barrier
	s_nop 2
	ds_read_b128 v[2:5], v10
	ds_read_b128 v[6:9], v10 offset:1024
	ds_read_b128 v[18:21], v10 offset:2048
	ds_read_b128 v[22:25], v10 offset:3072
	s_mov_b32 m0, s35
	v_add_u32_e32 v70, s57, v157
	ds_read_b128 v[10:13], v163 offset:32768
	ds_read_b128 v[14:17], v163 offset:33792
	ds_read_b128 v[26:29], v163 offset:34816
	ds_read_b128 v[30:33], v163 offset:35840
	ds_read_b128 v[34:37], v163 offset:36864
	ds_read_b128 v[38:41], v163 offset:37888
	ds_read_b128 v[42:45], v163 offset:38912
	ds_read_b128 v[46:49], v163 offset:39936
	global_load_lds_dwordx4 v70, s[12:13]
	v_add_u32_e32 v70, s57, v158
	s_mov_b32 m0, s36
	s_nop 0
	global_load_lds_dwordx4 v70, s[12:13]
	s_waitcnt lgkmcnt(8)
	s_barrier
	s_waitcnt lgkmcnt(0)


	v_mfma_scale_f32_16x16x128_f8f6f4 v[118:121], v[2:9], v[10:17], v[118:121], v165, v164 op_sel_hi:[0,0,0]
	v_mfma_scale_f32_16x16x128_f8f6f4 v[122:125], v[18:25], v[10:17], v[122:125], v165, v164 op_sel_hi:[0,0,0]
	v_mfma_scale_f32_16x16x128_f8f6f4 v[110:113], v[2:9], v[26:33], v[138:141], v165, v164 op_sel_hi:[0,0,0]
	v_mfma_scale_f32_16x16x128_f8f6f4 v[102:105], v[18:25], v[26:33], v[200:203], v165, v164 op_sel_hi:[0,0,0]
	v_mfma_scale_f32_16x16x128_f8f6f4 v[94:97], v[2:9], v[34:41], v[204:207], v165, v164 op_sel_hi:[0,0,0]
	v_mfma_scale_f32_16x16x128_f8f6f4 v[90:93], v[18:25], v[34:41], v[208:211], v165, v164 op_sel_hi:[0,0,0]
	v_mfma_scale_f32_16x16x128_f8f6f4 v[78:81], v[2:9], v[42:49], v[212:215], v165, v164 op_sel_hi:[0,0,0]
	v_mfma_scale_f32_16x16x128_f8f6f4 v[74:77], v[18:25], v[42:49], v[216:219], v165, v164 op_sel_hi:[0,0,0]

	s_barrier
	s_add_i32 s57, 0, 0x1c000
	v_add_u32_e32 v70, s57, v161
	s_or_b32 s59, s55, 0x80
	s_add_i32 s58, s58, s31
	ds_read_b128 v[130:133], v70
	ds_read_b128 v[134:137], v70 offset:1024
	ds_read_b128 v[146:149], v70 offset:2048
	ds_read_b128 v[150:153], v70 offset:3072
	v_add_u32_e32 v70, s59, v1
	s_mov_b32 m0, s58
	s_nop 0
	global_load_lds_dwordx4 v70, s[10:11]
	v_add_u32_e32 v70, s59, v154
	s_add_i32 m0, s58, 0x2000
	s_nop 0
	global_load_lds_dwordx4 v70, s[10:11]
	s_barrier
	s_waitcnt lgkmcnt(0)


	v_mfma_scale_f32_16x16x128_f8f6f4 v[126:129], v[130:137], v[10:17], v[126:129], v165, v164 op_sel_hi:[0,0,0]
	v_mfma_scale_f32_16x16x128_f8f6f4 v[114:117], v[146:153], v[10:17], v[114:117], v165, v164 op_sel_hi:[0,0,0]
	v_mfma_scale_f32_16x16x128_f8f6f4 v[106:109], v[130:137], v[26:33], v[168:171], v165, v164 op_sel_hi:[0,0,0]
	v_mfma_scale_f32_16x16x128_f8f6f4 v[98:101], v[146:153], v[26:33], v[172:175], v165, v164 op_sel_hi:[0,0,0]
	v_mfma_scale_f32_16x16x128_f8f6f4 v[86:89], v[130:137], v[34:41], v[176:179], v165, v164 op_sel_hi:[0,0,0]
	v_mfma_scale_f32_16x16x128_f8f6f4 v[82:85], v[146:153], v[34:41], v[180:183], v165, v164 op_sel_hi:[0,0,0]
	v_mfma_scale_f32_16x16x128_f8f6f4 v[70:73], v[130:137], v[42:49], v[184:187], v165, v164 op_sel_hi:[0,0,0]
	v_mfma_scale_f32_16x16x128_f8f6f4 v[10:13], v[146:153], v[42:49], v[188:191], v165, v164 op_sel_hi:[0,0,0]

	s_mov_b32 m0, s38
	v_add_u32_e32 v14, s56, v155
	s_barrier
	ds_read_b128 v[34:37], v163 offset:49152
	ds_read_b128 v[38:41], v163 offset:50176
	ds_read_b128 v[168:171], v163 offset:51200
	ds_read_b128 v[172:175], v163 offset:52224
	ds_read_b128 v[176:179], v163 offset:53248
	ds_read_b128 v[180:183], v163 offset:54272
	ds_read_b128 v[184:187], v163 offset:55296
	ds_read_b128 v[188:191], v163 offset:56320
	global_load_lds_dwordx4 v14, s[12:13]
	v_add_u32_e32 v14, s56, v156
	s_mov_b32 m0, s39
	s_nop 0
	global_load_lds_dwordx4 v14, s[12:13]
	s_barrier
	s_waitcnt lgkmcnt(0)


	v_mfma_scale_f32_16x16x128_f8f6f4 v[62:65], v[2:9], v[34:41], v[62:65], v165, v164 op_sel_hi:[0,0,0]
	v_mfma_scale_f32_16x16x128_f8f6f4 v[58:61], v[18:25], v[34:41], v[58:61], v165, v164 op_sel_hi:[0,0,0]
	v_mfma_scale_f32_16x16x128_f8f6f4 v[46:49], v[2:9], v[168:175], v[192:195], v165, v164 op_sel_hi:[0,0,0]
	v_mfma_scale_f32_16x16x128_f8f6f4 v[42:45], v[18:25], v[168:175], v[196:199], v165, v164 op_sel_hi:[0,0,0]
	v_mfma_scale_f32_16x16x128_f8f6f4 v[30:33], v[2:9], v[176:183], v[220:223], v165, v164 op_sel_hi:[0,0,0]
	v_mfma_scale_f32_16x16x128_f8f6f4 v[26:29], v[18:25], v[176:183], v[224:227], v165, v164 op_sel_hi:[0,0,0]
	v_mfma_scale_f32_16x16x128_f8f6f4 v[14:17], v[2:9], v[184:191], v[228:231], v165, v164 op_sel_hi:[0,0,0]
	v_mfma_scale_f32_16x16x128_f8f6f4 v[232:235], v[18:25], v[184:191], v[232:235], v165, v164 op_sel_hi:[0,0,0]

	s_barrier
	s_add_i32 s55, s55, 0x40080
	s_add_i32 s56, s57, s31
	v_add_u32_e32 v2, s55, v1
	s_mov_b32 m0, s56
	s_nop 0
	global_load_lds_dwordx4 v2, s[10:11]
	v_add_u32_e32 v2, s55, v154
	s_add_i32 m0, s56, 0x2000
	s_nop 0
	global_load_lds_dwordx4 v2, s[10:11]
	s_waitcnt vmcnt(6)
	s_barrier

	v_mfma_scale_f32_16x16x128_f8f6f4 v[54:57], v[130:137], v[34:41], v[54:57], v165, v164 op_sel_hi:[0,0,0]
	v_mfma_scale_f32_16x16x128_f8f6f4 v[50:53], v[146:153], v[34:41], v[50:53], v165, v164 op_sel_hi:[0,0,0]
	v_mfma_scale_f32_16x16x128_f8f6f4 v[38:41], v[130:137], v[168:175], v[236:239], v165, v164 op_sel_hi:[0,0,0]
	v_mfma_scale_f32_16x16x128_f8f6f4 v[34:37], v[146:153], v[168:175], v[240:243], v165, v164 op_sel_hi:[0,0,0]
	v_mfma_scale_f32_16x16x128_f8f6f4 v[22:25], v[130:137], v[176:183], v[244:247], v165, v164 op_sel_hi:[0,0,0]
	v_mfma_scale_f32_16x16x128_f8f6f4 v[18:21], v[146:153], v[176:183], v[248:251], v165, v164 op_sel_hi:[0,0,0]
	v_mfma_scale_f32_16x16x128_f8f6f4 v[6:9], v[130:137], v[184:191], v[142:145], v165, v164 op_sel_hi:[0,0,0]
	v_mfma_scale_f32_16x16x128_f8f6f4 v[2:5], v[146:153], v[184:191], v[66:69], v165, v164 op_sel_hi:[0,0,0]

	s_add_i32 s54, s54, 2
	s_addk_i32 s52, 0x100
	s_addk_i32 s53, 0x100
	s_cmp_ge_i32 s54, s40
	s_barrier
	s_cbranch_scc0 .LBB0_1522
	v_readlane_b32 s54, v254, 20
	v_readlane_b32 s55, v254, 21
	v_readlane_b32 s57, v254, 22
	v_readlane_b32 s56, v254, 23
	v_mov_b64_e32 v[220:221], 0x400
	s_branch .LBB0_1513

.LBB0_1840:
	s_add_i32 s74, s73, 0x80
	s_and_b64 s[30:31], s[10:11], exec
	s_cselect_b32 s31, 0, s74
	s_add_i32 s74, s74, s70
	s_or_b32 s30, s31, 0x80
	s_waitcnt lgkmcnt(8)
	s_barrier
	s_waitcnt lgkmcnt(0)
	s_and_b64 s[10:11], s[10:11], exec
	s_cselect_b32 s10, s71, s74
	s_add_i32 s11, s10, 0x80

	s_waitcnt lgkmcnt(0)
	v_mfma_scale_f32_16x16x128_f8f6f4 v[170:173], v[2:9], v[42:49], v[170:173], v193, v193 op_sel_hi:[0,0,0]
	v_mfma_scale_f32_16x16x128_f8f6f4 v[162:165], v[10:17], v[42:49], v[162:165], v193, v193 op_sel_hi:[0,0,0]
	v_mfma_scale_f32_16x16x128_f8f6f4 v[154:157], v[2:9], v[34:41], v[154:157], v193, v193 op_sel_hi:[0,0,0]
	v_mfma_scale_f32_16x16x128_f8f6f4 v[146:149], v[10:17], v[34:41], v[146:149], v193, v193 op_sel_hi:[0,0,0]
	v_mfma_scale_f32_16x16x128_f8f6f4 v[138:141], v[2:9], v[26:33], v[138:141], v193, v193 op_sel_hi:[0,0,0]
	v_mfma_scale_f32_16x16x128_f8f6f4 v[130:133], v[10:17], v[26:33], v[130:133], v193, v193 op_sel_hi:[0,0,0]
	v_mfma_scale_f32_16x16x128_f8f6f4 v[122:125], v[2:9], v[18:25], v[122:125], v193, v193 op_sel_hi:[0,0,0]
	v_mfma_scale_f32_16x16x128_f8f6f4 v[114:117], v[10:17], v[18:25], v[114:117], v193, v193 op_sel_hi:[0,0,0]

	s_barrier
	s_mov_b32 m0, s38
	v_add_u32_e32 v216, s59, v189
	v_add_u32_e32 v220, s10, v181
	ds_read_b128 v[204:207], v216
	ds_read_b128 v[208:211], v216 offset:1024
	ds_read_b128 v[212:215], v216 offset:2048
	ds_read_b128 v[216:219], v216 offset:3072
	global_load_lds_dwordx4 v220, s[20:21]
	v_add_u32_e32 v220, s10, v182
	s_mov_b32 m0, s39
	s_nop 0
	global_load_lds_dwordx4 v220, s[20:21]
	s_barrier
	s_waitcnt lgkmcnt(0)


	v_mfma_scale_f32_16x16x128_f8f6f4 v[174:177], v[204:211], v[42:49], v[174:177], v193, v193 op_sel_hi:[0,0,0]
	v_mfma_scale_f32_16x16x128_f8f6f4 v[166:169], v[212:219], v[42:49], v[166:169], v193, v193 op_sel_hi:[0,0,0]
	v_mfma_scale_f32_16x16x128_f8f6f4 v[158:161], v[204:211], v[34:41], v[158:161], v193, v193 op_sel_hi:[0,0,0]
	v_mfma_scale_f32_16x16x128_f8f6f4 v[150:153], v[212:219], v[34:41], v[150:153], v193, v193 op_sel_hi:[0,0,0]
	v_mfma_scale_f32_16x16x128_f8f6f4 v[142:145], v[204:211], v[26:33], v[142:145], v193, v193 op_sel_hi:[0,0,0]
	v_mfma_scale_f32_16x16x128_f8f6f4 v[134:137], v[212:219], v[26:33], v[134:137], v193, v193 op_sel_hi:[0,0,0]
	v_mfma_scale_f32_16x16x128_f8f6f4 v[126:129], v[204:211], v[18:25], v[126:129], v193, v193 op_sel_hi:[0,0,0]
	v_mfma_scale_f32_16x16x128_f8f6f4 v[118:121], v[212:219], v[18:25], v[118:121], v193, v193 op_sel_hi:[0,0,0]

	s_mov_b32 m0, s37
	v_add_u32_e32 v220, s31, v183
	s_barrier
	ds_read_b128 v[18:21], v194 offset:16384
	ds_read_b128 v[22:25], v194 offset:17408
	ds_read_b128 v[26:29], v194 offset:18432
	ds_read_b128 v[30:33], v194 offset:19456
	ds_read_b128 v[34:37], v194 offset:20480
	ds_read_b128 v[38:41], v194 offset:21504
	ds_read_b128 v[42:45], v194 offset:22528
	ds_read_b128 v[46:49], v194 offset:23552
	global_load_lds_dwordx4 v220, s[18:19]
	v_add_u32_e32 v220, s31, v184
	s_mov_b32 m0, s40
	s_nop 0
	global_load_lds_dwordx4 v220, s[18:19]
	s_barrier
	s_waitcnt lgkmcnt(0)


	v_mfma_scale_f32_16x16x128_f8f6f4 v[110:113], v[2:9], v[18:25], v[110:113], v193, v193 op_sel_hi:[0,0,0]
	v_mfma_scale_f32_16x16x128_f8f6f4 v[102:105], v[10:17], v[18:25], v[102:105], v193, v193 op_sel_hi:[0,0,0]
	v_mfma_scale_f32_16x16x128_f8f6f4 v[94:97], v[2:9], v[26:33], v[94:97], v193, v193 op_sel_hi:[0,0,0]
	v_mfma_scale_f32_16x16x128_f8f6f4 v[86:89], v[10:17], v[26:33], v[86:89], v193, v193 op_sel_hi:[0,0,0]
	v_mfma_scale_f32_16x16x128_f8f6f4 v[78:81], v[2:9], v[34:41], v[78:81], v193, v193 op_sel_hi:[0,0,0]
	v_mfma_scale_f32_16x16x128_f8f6f4 v[70:73], v[10:17], v[34:41], v[70:73], v193, v193 op_sel_hi:[0,0,0]
	v_mfma_scale_f32_16x16x128_f8f6f4 v[62:65], v[2:9], v[42:49], v[62:65], v193, v193 op_sel_hi:[0,0,0]
	v_mfma_scale_f32_16x16x128_f8f6f4 v[54:57], v[10:17], v[42:49], v[54:57], v193, v193 op_sel_hi:[0,0,0]

	s_barrier
	s_add_i32 s74, s10, 0x40000
	s_add_i32 s75, s59, s36
	v_add_u32_e32 v2, s74, v181
	s_mov_b32 m0, s75
	s_nop 0
	global_load_lds_dwordx4 v2, s[20:21]
	v_add_u32_e32 v2, s74, v182
	s_add_i32 m0, s75, 0x2000
	s_nop 0
	global_load_lds_dwordx4 v2, s[20:21]
	s_waitcnt vmcnt(6)
	s_barrier

	v_mfma_scale_f32_16x16x128_f8f6f4 v[106:109], v[204:211], v[18:25], v[106:109], v193, v193 op_sel_hi:[0,0,0]
	v_mfma_scale_f32_16x16x128_f8f6f4 v[98:101], v[212:219], v[18:25], v[98:101], v193, v193 op_sel_hi:[0,0,0]
	v_mfma_scale_f32_16x16x128_f8f6f4 v[90:93], v[204:211], v[26:33], v[90:93], v193, v193 op_sel_hi:[0,0,0]
	v_mfma_scale_f32_16x16x128_f8f6f4 v[82:85], v[212:219], v[26:33], v[82:85], v193, v193 op_sel_hi:[0,0,0]
	v_mfma_scale_f32_16x16x128_f8f6f4 v[74:77], v[204:211], v[34:41], v[74:77], v193, v193 op_sel_hi:[0,0,0]
	v_mfma_scale_f32_16x16x128_f8f6f4 v[66:69], v[212:219], v[34:41], v[66:69], v193, v193 op_sel_hi:[0,0,0]
	v_mfma_scale_f32_16x16x128_f8f6f4 v[58:61], v[204:211], v[42:49], v[58:61], v193, v193 op_sel_hi:[0,0,0]
	v_mfma_scale_f32_16x16x128_f8f6f4 v[50:53], v[212:219], v[42:49], v[50:53], v193, v193 op_sel_hi:[0,0,0]

	s_add_i32 s74, 0, 0x18000
	v_add_u32_e32 v14, s74, v189
	s_barrier
	ds_read_b128 v[2:5], v14
	ds_read_b128 v[6:9], v14 offset:1024
	ds_read_b128 v[10:13], v14 offset:2048
	ds_read_b128 v[14:17], v14 offset:3072
	s_mov_b32 m0, s41
	v_add_u32_e32 v204, s31, v185
	ds_read_b128 v[18:21], v194 offset:32768
	ds_read_b128 v[22:25], v194 offset:33792
	ds_read_b128 v[26:29], v194 offset:34816
	ds_read_b128 v[30:33], v194 offset:35840
	ds_read_b128 v[34:37], v194 offset:36864
	ds_read_b128 v[38:41], v194 offset:37888
	ds_read_b128 v[42:45], v194 offset:38912
	ds_read_b128 v[46:49], v194 offset:39936
	global_load_lds_dwordx4 v204, s[18:19]
	v_add_u32_e32 v204, s31, v186
	s_mov_b32 m0, s42
	s_nop 0
	global_load_lds_dwordx4 v204, s[18:19]
	s_waitcnt lgkmcnt(8)
	s_barrier
	s_waitcnt lgkmcnt(0)


	v_mfma_scale_f32_16x16x128_f8f6f4 v[170:173], v[2:9], v[18:25], v[170:173], v193, v193 op_sel_hi:[0,0,0]
	v_mfma_scale_f32_16x16x128_f8f6f4 v[162:165], v[10:17], v[18:25], v[162:165], v193, v193 op_sel_hi:[0,0,0]
	v_mfma_scale_f32_16x16x128_f8f6f4 v[154:157], v[2:9], v[26:33], v[154:157], v193, v193 op_sel_hi:[0,0,0]
	v_mfma_scale_f32_16x16x128_f8f6f4 v[146:149], v[10:17], v[26:33], v[146:149], v193, v193 op_sel_hi:[0,0,0]
	v_mfma_scale_f32_16x16x128_f8f6f4 v[138:141], v[2:9], v[34:41], v[138:141], v193, v193 op_sel_hi:[0,0,0]
	v_mfma_scale_f32_16x16x128_f8f6f4 v[130:133], v[10:17], v[34:41], v[130:133], v193, v193 op_sel_hi:[0,0,0]
	v_mfma_scale_f32_16x16x128_f8f6f4 v[122:125], v[2:9], v[42:49], v[122:125], v193, v193 op_sel_hi:[0,0,0]
	v_mfma_scale_f32_16x16x128_f8f6f4 v[114:117], v[10:17], v[42:49], v[114:117], v193, v193 op_sel_hi:[0,0,0]

	s_barrier
	s_add_i32 s31, 0, 0x1c000
	s_add_i32 s74, s74, s36
	v_add_u32_e32 v216, s31, v189
	v_add_u32_e32 v220, s11, v181
	s_mov_b32 m0, s74
	ds_read_b128 v[204:207], v216
	ds_read_b128 v[208:211], v216 offset:1024
	ds_read_b128 v[212:215], v216 offset:2048
	ds_read_b128 v[216:219], v216 offset:3072
	global_load_lds_dwordx4 v220, s[20:21]
	v_add_u32_e32 v220, s11, v182
	s_add_i32 m0, s74, 0x2000
	s_nop 0
	global_load_lds_dwordx4 v220, s[20:21]
	s_barrier
	s_waitcnt lgkmcnt(0)


	v_mfma_scale_f32_16x16x128_f8f6f4 v[174:177], v[204:211], v[18:25], v[174:177], v193, v193 op_sel_hi:[0,0,0]
	v_mfma_scale_f32_16x16x128_f8f6f4 v[166:169], v[212:219], v[18:25], v[166:169], v193, v193 op_sel_hi:[0,0,0]
	v_mfma_scale_f32_16x16x128_f8f6f4 v[158:161], v[204:211], v[26:33], v[158:161], v193, v193 op_sel_hi:[0,0,0]
	v_mfma_scale_f32_16x16x128_f8f6f4 v[150:153], v[212:219], v[26:33], v[150:153], v193, v193 op_sel_hi:[0,0,0]
	v_mfma_scale_f32_16x16x128_f8f6f4 v[142:145], v[204:211], v[34:41], v[142:145], v193, v193 op_sel_hi:[0,0,0]
	v_mfma_scale_f32_16x16x128_f8f6f4 v[134:137], v[212:219], v[34:41], v[134:137], v193, v193 op_sel_hi:[0,0,0]
	v_mfma_scale_f32_16x16x128_f8f6f4 v[126:129], v[204:211], v[42:49], v[126:129], v193, v193 op_sel_hi:[0,0,0]
	v_mfma_scale_f32_16x16x128_f8f6f4 v[118:121], v[212:219], v[42:49], v[118:121], v193, v193 op_sel_hi:[0,0,0]

	s_mov_b32 m0, s49
	v_add_u32_e32 v220, s30, v183
	s_barrier
	ds_read_b128 v[18:21], v194 offset:49152
	ds_read_b128 v[22:25], v194 offset:50176
	ds_read_b128 v[26:29], v194 offset:51200
	ds_read_b128 v[30:33], v194 offset:52224
	ds_read_b128 v[34:37], v194 offset:53248
	ds_read_b128 v[38:41], v194 offset:54272
	ds_read_b128 v[42:45], v194 offset:55296
	ds_read_b128 v[46:49], v194 offset:56320
	global_load_lds_dwordx4 v220, s[18:19]
	v_add_u32_e32 v220, s30, v184
	s_mov_b32 m0, s50
	s_nop 0
	global_load_lds_dwordx4 v220, s[18:19]
	s_barrier
	s_waitcnt lgkmcnt(0)


	v_mfma_scale_f32_16x16x128_f8f6f4 v[110:113], v[2:9], v[18:25], v[110:113], v193, v193 op_sel_hi:[0,0,0]
	v_mfma_scale_f32_16x16x128_f8f6f4 v[102:105], v[10:17], v[18:25], v[102:105], v193, v193 op_sel_hi:[0,0,0]
	v_mfma_scale_f32_16x16x128_f8f6f4 v[94:97], v[2:9], v[26:33], v[94:97], v193, v193 op_sel_hi:[0,0,0]
	v_mfma_scale_f32_16x16x128_f8f6f4 v[86:89], v[10:17], v[26:33], v[86:89], v193, v193 op_sel_hi:[0,0,0]
	v_mfma_scale_f32_16x16x128_f8f6f4 v[78:81], v[2:9], v[34:41], v[78:81], v193, v193 op_sel_hi:[0,0,0]
	v_mfma_scale_f32_16x16x128_f8f6f4 v[70:73], v[10:17], v[34:41], v[70:73], v193, v193 op_sel_hi:[0,0,0]
	v_mfma_scale_f32_16x16x128_f8f6f4 v[62:65], v[2:9], v[42:49], v[62:65], v193, v193 op_sel_hi:[0,0,0]
	v_mfma_scale_f32_16x16x128_f8f6f4 v[54:57], v[10:17], v[42:49], v[54:57], v193, v193 op_sel_hi:[0,0,0]

	s_barrier
	s_add_i32 s10, s10, 0x40080
	s_add_i32 s11, s31, s36
	v_add_u32_e32 v2, s10, v181
	s_mov_b32 m0, s11
	s_nop 0
	global_load_lds_dwordx4 v2, s[20:21]
	v_add_u32_e32 v2, s10, v182
	s_add_i32 m0, s11, 0x2000
	s_nop 0
	global_load_lds_dwordx4 v2, s[20:21]
	s_waitcnt vmcnt(6)
	s_barrier

	v_mfma_scale_f32_16x16x128_f8f6f4 v[106:109], v[204:211], v[18:25], v[106:109], v193, v193 op_sel_hi:[0,0,0]
	v_mfma_scale_f32_16x16x128_f8f6f4 v[98:101], v[212:219], v[18:25], v[98:101], v193, v193 op_sel_hi:[0,0,0]
	v_mfma_scale_f32_16x16x128_f8f6f4 v[90:93], v[204:211], v[26:33], v[90:93], v193, v193 op_sel_hi:[0,0,0]
	v_mfma_scale_f32_16x16x128_f8f6f4 v[82:85], v[212:219], v[26:33], v[82:85], v193, v193 op_sel_hi:[0,0,0]
	v_mfma_scale_f32_16x16x128_f8f6f4 v[74:77], v[204:211], v[34:41], v[74:77], v193, v193 op_sel_hi:[0,0,0]
	v_mfma_scale_f32_16x16x128_f8f6f4 v[66:69], v[212:219], v[34:41], v[66:69], v193, v193 op_sel_hi:[0,0,0]
	v_mfma_scale_f32_16x16x128_f8f6f4 v[58:61], v[204:211], v[42:49], v[58:61], v193, v193 op_sel_hi:[0,0,0]
	v_mfma_scale_f32_16x16x128_f8f6f4 v[50:53], v[212:219], v[42:49], v[50:53], v193, v193 op_sel_hi:[0,0,0]

	s_add_i32 s72, s72, 2
	s_addk_i32 s73, 0x100
	s_cmp_ge_i32 s72, s51
	s_barrier
	s_cbranch_scc1 .LBB0_1830

.LBB0_1864:
	s_add_i32 s58, s55, 0x80
	s_cmp_eq_u32 s44, s57
	s_cselect_b32 s60, s4, s58
	s_cselect_b32 s58, s5, s56
	s_add_i32 s61, 0, 0x10000
	v_add_u32_e32 v156, s61, v141
	ds_read_b128 v[144:147], v156
	ds_read_b128 v[148:151], v156 offset:1024
	ds_read_b128 v[152:155], v156 offset:2048
	ds_read_b128 v[156:159], v156 offset:3072
	s_or_b32 s59, s60, 0x80
	v_add_u32_e32 v192, s55, v137
	s_add_i32 m0, s33, 0xc000
	ds_read_b128 v[160:163], v142
	ds_read_b128 v[164:167], v142 offset:1024
	ds_read_b128 v[168:171], v142 offset:2048
	ds_read_b128 v[172:175], v142 offset:3072
	ds_read_b128 v[176:179], v142 offset:4096
	ds_read_b128 v[180:183], v142 offset:5120
	ds_read_b128 v[184:187], v142 offset:6144
	ds_read_b128 v[188:191], v142 offset:7168
	global_load_lds_dwordx4 v192, s[6:7]
	v_add_u32_e32 v192, s55, v138
	s_add_i32 m0, s33, 0xe000
	s_nop 0
	global_load_lds_dwordx4 v192, s[6:7]
	s_waitcnt lgkmcnt(8)
	s_barrier
	s_waitcnt lgkmcnt(0)


	v_mfma_f32_16x16x32_bf16 v[122:125], v[144:147], v[160:163], v[122:125]
	v_mfma_f32_16x16x32_bf16 v[126:129], v[152:155], v[160:163], v[126:129]
	v_mfma_f32_16x16x32_bf16 v[110:113], v[144:147], v[168:171], v[110:113]
	v_mfma_f32_16x16x32_bf16 v[106:109], v[152:155], v[168:171], v[106:109]
	v_mfma_f32_16x16x32_bf16 v[94:97], v[144:147], v[176:179], v[94:97]
	v_mfma_f32_16x16x32_bf16 v[90:93], v[152:155], v[176:179], v[90:93]
	v_mfma_f32_16x16x32_bf16 v[78:81], v[144:147], v[184:187], v[78:81]
	v_mfma_f32_16x16x32_bf16 v[74:77], v[152:155], v[184:187], v[74:77]
	v_mfma_f32_16x16x32_bf16 v[122:125], v[148:151], v[164:167], v[122:125]
	v_mfma_f32_16x16x32_bf16 v[126:129], v[156:159], v[164:167], v[126:129]
	v_mfma_f32_16x16x32_bf16 v[110:113], v[148:151], v[172:175], v[110:113]
	v_mfma_f32_16x16x32_bf16 v[106:109], v[156:159], v[172:175], v[106:109]
	v_mfma_f32_16x16x32_bf16 v[94:97], v[148:151], v[180:183], v[94:97]
	v_mfma_f32_16x16x32_bf16 v[90:93], v[156:159], v[180:183], v[90:93]
	v_mfma_f32_16x16x32_bf16 v[78:81], v[148:151], v[188:191], v[78:81]
	v_mfma_f32_16x16x32_bf16 v[74:77], v[156:159], v[188:191], v[74:77]

	s_barrier
	s_add_i32 s61, s61, s31
	v_add_u32_e32 v208, s58, v1
	s_mov_b32 m0, s61
	ds_read_b128 v[192:195], v143
	ds_read_b128 v[196:199], v143 offset:1024
	ds_read_b128 v[200:203], v143 offset:2048
	ds_read_b128 v[204:207], v143 offset:3072
	global_load_lds_dwordx4 v208, s[8:9]
	v_add_u32_e32 v208, s58, v134
	s_add_i32 m0, s61, 0x2000
	s_nop 0
	global_load_lds_dwordx4 v208, s[8:9]
	s_barrier
	s_waitcnt lgkmcnt(0)


	v_mfma_f32_16x16x32_bf16 v[118:121], v[192:195], v[160:163], v[118:121]
	v_mfma_f32_16x16x32_bf16 v[114:117], v[200:203], v[160:163], v[114:117]
	v_mfma_f32_16x16x32_bf16 v[102:105], v[192:195], v[168:171], v[102:105]
	v_mfma_f32_16x16x32_bf16 v[98:101], v[200:203], v[168:171], v[98:101]
	v_mfma_f32_16x16x32_bf16 v[86:89], v[192:195], v[176:179], v[86:89]
	v_mfma_f32_16x16x32_bf16 v[82:85], v[200:203], v[176:179], v[82:85]
	v_mfma_f32_16x16x32_bf16 v[70:73], v[192:195], v[184:187], v[70:73]
	v_mfma_f32_16x16x32_bf16 v[66:69], v[200:203], v[184:187], v[66:69]
	v_mfma_f32_16x16x32_bf16 v[118:121], v[196:199], v[164:167], v[118:121]
	v_mfma_f32_16x16x32_bf16 v[114:117], v[204:207], v[164:167], v[114:117]
	v_mfma_f32_16x16x32_bf16 v[102:105], v[196:199], v[172:175], v[102:105]
	v_mfma_f32_16x16x32_bf16 v[98:101], v[204:207], v[172:175], v[98:101]
	v_mfma_f32_16x16x32_bf16 v[86:89], v[196:199], v[180:183], v[86:89]
	v_mfma_f32_16x16x32_bf16 v[82:85], v[204:207], v[180:183], v[82:85]
	v_mfma_f32_16x16x32_bf16 v[70:73], v[196:199], v[188:191], v[70:73]
	v_mfma_f32_16x16x32_bf16 v[66:69], v[204:207], v[188:191], v[66:69]

	s_mov_b32 m0, s33
	v_add_u32_e32 v208, s60, v135
	s_barrier
	ds_read_b128 v[160:163], v142 offset:16384
	ds_read_b128 v[164:167], v142 offset:17408
	ds_read_b128 v[168:171], v142 offset:18432
	ds_read_b128 v[172:175], v142 offset:19456
	ds_read_b128 v[176:179], v142 offset:20480
	ds_read_b128 v[180:183], v142 offset:21504
	ds_read_b128 v[184:187], v142 offset:22528
	ds_read_b128 v[188:191], v142 offset:23552
	global_load_lds_dwordx4 v208, s[6:7]
	v_add_u32_e32 v208, s60, v136
	s_mov_b32 m0, s35
	s_nop 0
	global_load_lds_dwordx4 v208, s[6:7]
	s_barrier
	s_waitcnt lgkmcnt(0)


	v_mfma_f32_16x16x32_bf16 v[62:65], v[144:147], v[160:163], v[62:65]
	v_mfma_f32_16x16x32_bf16 v[58:61], v[152:155], v[160:163], v[58:61]
	v_mfma_f32_16x16x32_bf16 v[46:49], v[144:147], v[168:171], v[46:49]
	v_mfma_f32_16x16x32_bf16 v[42:45], v[152:155], v[168:171], v[42:45]
	v_mfma_f32_16x16x32_bf16 v[30:33], v[144:147], v[176:179], v[30:33]
	v_mfma_f32_16x16x32_bf16 v[26:29], v[152:155], v[176:179], v[26:29]
	v_mfma_f32_16x16x32_bf16 v[14:17], v[144:147], v[184:187], v[14:17]
	v_mfma_f32_16x16x32_bf16 v[10:13], v[152:155], v[184:187], v[10:13]
	v_mfma_f32_16x16x32_bf16 v[62:65], v[148:151], v[164:167], v[62:65]
	v_mfma_f32_16x16x32_bf16 v[58:61], v[156:159], v[164:167], v[58:61]
	v_mfma_f32_16x16x32_bf16 v[46:49], v[148:151], v[172:175], v[46:49]
	v_mfma_f32_16x16x32_bf16 v[42:45], v[156:159], v[172:175], v[42:45]
	v_mfma_f32_16x16x32_bf16 v[30:33], v[148:151], v[180:183], v[30:33]
	v_mfma_f32_16x16x32_bf16 v[26:29], v[156:159], v[180:183], v[26:29]
	v_mfma_f32_16x16x32_bf16 v[14:17], v[148:151], v[188:191], v[14:17]
	v_mfma_f32_16x16x32_bf16 v[10:13], v[156:159], v[188:191], v[10:13]

	s_barrier
	s_add_i32 s61, s58, 0x10000
	s_add_i32 s62, s45, s31
	v_add_u32_e32 v144, s61, v1
	s_mov_b32 m0, s62
	s_nop 0
	global_load_lds_dwordx4 v144, s[8:9]
	v_add_u32_e32 v144, s61, v134
	s_add_i32 m0, s62, 0x2000
	s_nop 0
	global_load_lds_dwordx4 v144, s[8:9]
	s_waitcnt vmcnt(6)
	s_barrier

	v_mfma_f32_16x16x32_bf16 v[54:57], v[192:195], v[160:163], v[54:57]
	v_mfma_f32_16x16x32_bf16 v[50:53], v[200:203], v[160:163], v[50:53]
	v_mfma_f32_16x16x32_bf16 v[38:41], v[192:195], v[168:171], v[38:41]
	v_mfma_f32_16x16x32_bf16 v[34:37], v[200:203], v[168:171], v[34:37]
	v_mfma_f32_16x16x32_bf16 v[22:25], v[192:195], v[176:179], v[22:25]
	v_mfma_f32_16x16x32_bf16 v[18:21], v[200:203], v[176:179], v[18:21]
	v_mfma_f32_16x16x32_bf16 v[6:9], v[192:195], v[184:187], v[6:9]
	v_mfma_f32_16x16x32_bf16 v[2:5], v[200:203], v[184:187], v[2:5]
	v_mfma_f32_16x16x32_bf16 v[54:57], v[196:199], v[164:167], v[54:57]
	v_mfma_f32_16x16x32_bf16 v[50:53], v[204:207], v[164:167], v[50:53]
	v_mfma_f32_16x16x32_bf16 v[38:41], v[196:199], v[172:175], v[38:41]
	v_mfma_f32_16x16x32_bf16 v[34:37], v[204:207], v[172:175], v[34:37]
	v_mfma_f32_16x16x32_bf16 v[22:25], v[196:199], v[180:183], v[22:25]
	v_mfma_f32_16x16x32_bf16 v[18:21], v[204:207], v[180:183], v[18:21]
	v_mfma_f32_16x16x32_bf16 v[6:9], v[196:199], v[188:191], v[6:9]
	v_mfma_f32_16x16x32_bf16 v[2:5], v[204:207], v[188:191], v[2:5]

	s_add_i32 s61, 0, 0x18000
	v_add_u32_e32 v156, s61, v141
	s_barrier
	ds_read_b128 v[144:147], v156
	ds_read_b128 v[148:151], v156 offset:1024
	ds_read_b128 v[152:155], v156 offset:2048
	ds_read_b128 v[156:159], v156 offset:3072
	s_mov_b32 m0, s36
	v_add_u32_e32 v192, s60, v137
	ds_read_b128 v[160:163], v142 offset:32768
	ds_read_b128 v[164:167], v142 offset:33792
	ds_read_b128 v[168:171], v142 offset:34816
	ds_read_b128 v[172:175], v142 offset:35840
	ds_read_b128 v[176:179], v142 offset:36864
	ds_read_b128 v[180:183], v142 offset:37888
	ds_read_b128 v[184:187], v142 offset:38912
	ds_read_b128 v[188:191], v142 offset:39936
	global_load_lds_dwordx4 v192, s[6:7]
	v_add_u32_e32 v192, s60, v138
	s_mov_b32 m0, s37
	s_nop 0
	global_load_lds_dwordx4 v192, s[6:7]
	s_waitcnt lgkmcnt(8)
	s_barrier
	s_waitcnt lgkmcnt(0)


	v_mfma_f32_16x16x32_bf16 v[122:125], v[144:147], v[160:163], v[122:125]
	v_mfma_f32_16x16x32_bf16 v[126:129], v[152:155], v[160:163], v[126:129]
	v_mfma_f32_16x16x32_bf16 v[110:113], v[144:147], v[168:171], v[110:113]
	v_mfma_f32_16x16x32_bf16 v[106:109], v[152:155], v[168:171], v[106:109]
	v_mfma_f32_16x16x32_bf16 v[94:97], v[144:147], v[176:179], v[94:97]
	v_mfma_f32_16x16x32_bf16 v[90:93], v[152:155], v[176:179], v[90:93]
	v_mfma_f32_16x16x32_bf16 v[78:81], v[144:147], v[184:187], v[78:81]
	v_mfma_f32_16x16x32_bf16 v[74:77], v[152:155], v[184:187], v[74:77]
	v_mfma_f32_16x16x32_bf16 v[122:125], v[148:151], v[164:167], v[122:125]
	v_mfma_f32_16x16x32_bf16 v[126:129], v[156:159], v[164:167], v[126:129]
	v_mfma_f32_16x16x32_bf16 v[110:113], v[148:151], v[172:175], v[110:113]
	v_mfma_f32_16x16x32_bf16 v[106:109], v[156:159], v[172:175], v[106:109]
	v_mfma_f32_16x16x32_bf16 v[94:97], v[148:151], v[180:183], v[94:97]
	v_mfma_f32_16x16x32_bf16 v[90:93], v[156:159], v[180:183], v[90:93]
	v_mfma_f32_16x16x32_bf16 v[78:81], v[148:151], v[188:191], v[78:81]
	v_mfma_f32_16x16x32_bf16 v[74:77], v[156:159], v[188:191], v[74:77]

	s_barrier
	s_add_i32 s60, 0, 0x1c000
	s_or_b32 s62, s58, 0x80
	s_add_i32 s61, s61, s31
	v_add_u32_e32 v204, s60, v141
	v_add_u32_e32 v208, s62, v1
	s_mov_b32 m0, s61
	ds_read_b128 v[192:195], v204
	ds_read_b128 v[196:199], v204 offset:1024
	ds_read_b128 v[200:203], v204 offset:2048
	ds_read_b128 v[204:207], v204 offset:3072
	global_load_lds_dwordx4 v208, s[8:9]
	v_add_u32_e32 v208, s62, v134
	s_add_i32 m0, s61, 0x2000
	s_nop 0
	global_load_lds_dwordx4 v208, s[8:9]
	s_barrier
	s_waitcnt lgkmcnt(0)


	v_mfma_f32_16x16x32_bf16 v[118:121], v[192:195], v[160:163], v[118:121]
	v_mfma_f32_16x16x32_bf16 v[114:117], v[200:203], v[160:163], v[114:117]
	v_mfma_f32_16x16x32_bf16 v[102:105], v[192:195], v[168:171], v[102:105]
	v_mfma_f32_16x16x32_bf16 v[98:101], v[200:203], v[168:171], v[98:101]
	v_mfma_f32_16x16x32_bf16 v[86:89], v[192:195], v[176:179], v[86:89]
	v_mfma_f32_16x16x32_bf16 v[82:85], v[200:203], v[176:179], v[82:85]
	v_mfma_f32_16x16x32_bf16 v[70:73], v[192:195], v[184:187], v[70:73]
	v_mfma_f32_16x16x32_bf16 v[66:69], v[200:203], v[184:187], v[66:69]
	v_mfma_f32_16x16x32_bf16 v[118:121], v[196:199], v[164:167], v[118:121]
	v_mfma_f32_16x16x32_bf16 v[114:117], v[204:207], v[164:167], v[114:117]
	v_mfma_f32_16x16x32_bf16 v[102:105], v[196:199], v[172:175], v[102:105]
	v_mfma_f32_16x16x32_bf16 v[98:101], v[204:207], v[172:175], v[98:101]
	v_mfma_f32_16x16x32_bf16 v[86:89], v[196:199], v[180:183], v[86:89]
	v_mfma_f32_16x16x32_bf16 v[82:85], v[204:207], v[180:183], v[82:85]
	v_mfma_f32_16x16x32_bf16 v[70:73], v[196:199], v[188:191], v[70:73]
	v_mfma_f32_16x16x32_bf16 v[66:69], v[204:207], v[188:191], v[66:69]

	s_mov_b32 m0, s40
	v_add_u32_e32 v208, s59, v135
	s_barrier
	ds_read_b128 v[160:163], v142 offset:49152
	ds_read_b128 v[164:167], v142 offset:50176
	ds_read_b128 v[168:171], v142 offset:51200
	ds_read_b128 v[172:175], v142 offset:52224
	ds_read_b128 v[176:179], v142 offset:53248
	ds_read_b128 v[180:183], v142 offset:54272
	ds_read_b128 v[184:187], v142 offset:55296
	ds_read_b128 v[188:191], v142 offset:56320
	global_load_lds_dwordx4 v208, s[6:7]
	v_add_u32_e32 v208, s59, v136
	s_mov_b32 m0, s41
	s_nop 0
	global_load_lds_dwordx4 v208, s[6:7]
	s_barrier
	s_waitcnt lgkmcnt(0)


	v_mfma_f32_16x16x32_bf16 v[62:65], v[144:147], v[160:163], v[62:65]
	v_mfma_f32_16x16x32_bf16 v[58:61], v[152:155], v[160:163], v[58:61]
	v_mfma_f32_16x16x32_bf16 v[46:49], v[144:147], v[168:171], v[46:49]
	v_mfma_f32_16x16x32_bf16 v[42:45], v[152:155], v[168:171], v[42:45]
	v_mfma_f32_16x16x32_bf16 v[30:33], v[144:147], v[176:179], v[30:33]
	v_mfma_f32_16x16x32_bf16 v[26:29], v[152:155], v[176:179], v[26:29]
	v_mfma_f32_16x16x32_bf16 v[14:17], v[144:147], v[184:187], v[14:17]
	v_mfma_f32_16x16x32_bf16 v[10:13], v[152:155], v[184:187], v[10:13]
	v_mfma_f32_16x16x32_bf16 v[62:65], v[148:151], v[164:167], v[62:65]
	v_mfma_f32_16x16x32_bf16 v[58:61], v[156:159], v[164:167], v[58:61]
	v_mfma_f32_16x16x32_bf16 v[46:49], v[148:151], v[172:175], v[46:49]
	v_mfma_f32_16x16x32_bf16 v[42:45], v[156:159], v[172:175], v[42:45]
	v_mfma_f32_16x16x32_bf16 v[30:33], v[148:151], v[180:183], v[30:33]
	v_mfma_f32_16x16x32_bf16 v[26:29], v[156:159], v[180:183], v[26:29]
	v_mfma_f32_16x16x32_bf16 v[14:17], v[148:151], v[188:191], v[14:17]
	v_mfma_f32_16x16x32_bf16 v[10:13], v[156:159], v[188:191], v[10:13]

	s_barrier
	s_add_i32 s58, s58, 0x10080
	s_add_i32 s59, s60, s31
	v_add_u32_e32 v144, s58, v1
	s_mov_b32 m0, s59
	s_nop 0
	global_load_lds_dwordx4 v144, s[8:9]
	v_add_u32_e32 v144, s58, v134
	s_add_i32 m0, s59, 0x2000
	s_nop 0
	global_load_lds_dwordx4 v144, s[8:9]
	s_waitcnt vmcnt(6)
	s_barrier

	v_mfma_f32_16x16x32_bf16 v[54:57], v[192:195], v[160:163], v[54:57]
	v_mfma_f32_16x16x32_bf16 v[50:53], v[200:203], v[160:163], v[50:53]
	v_mfma_f32_16x16x32_bf16 v[38:41], v[192:195], v[168:171], v[38:41]
	v_mfma_f32_16x16x32_bf16 v[34:37], v[200:203], v[168:171], v[34:37]
	v_mfma_f32_16x16x32_bf16 v[22:25], v[192:195], v[176:179], v[22:25]
	v_mfma_f32_16x16x32_bf16 v[18:21], v[200:203], v[176:179], v[18:21]
	v_mfma_f32_16x16x32_bf16 v[6:9], v[192:195], v[184:187], v[6:9]
	v_mfma_f32_16x16x32_bf16 v[2:5], v[200:203], v[184:187], v[2:5]
	v_mfma_f32_16x16x32_bf16 v[54:57], v[196:199], v[164:167], v[54:57]
	v_mfma_f32_16x16x32_bf16 v[50:53], v[204:207], v[164:167], v[50:53]
	v_mfma_f32_16x16x32_bf16 v[38:41], v[196:199], v[172:175], v[38:41]
	v_mfma_f32_16x16x32_bf16 v[34:37], v[204:207], v[172:175], v[34:37]
	v_mfma_f32_16x16x32_bf16 v[22:25], v[196:199], v[180:183], v[22:25]
	v_mfma_f32_16x16x32_bf16 v[18:21], v[204:207], v[180:183], v[18:21]
	v_mfma_f32_16x16x32_bf16 v[6:9], v[196:199], v[188:191], v[6:9]
	v_mfma_f32_16x16x32_bf16 v[2:5], v[204:207], v[188:191], v[2:5]

	s_add_i32 s57, s57, 2
	s_addk_i32 s55, 0x100
	s_addk_i32 s56, 0x100
	s_cmp_ge_i32 s57, s42
	s_barrier
	s_cbranch_scc0 .LBB0_1864
	v_readlane_b32 s57, v254, 22
	s_branch .LBB0_1855

.LBB0_1947:
	v_add_u32_e32 v66, s37, v138
	ds_read_b128 v[144:147], v66
	ds_read_b128 v[148:151], v66 offset:1024
	ds_read_b128 v[152:155], v66 offset:2048
	ds_read_b128 v[156:159], v66 offset:3072
	s_add_i32 s51, s48, 0x80
	s_and_b64 s[52:53], s[16:17], exec
	s_cselect_b32 s52, s46, s51
	s_or_b32 s51, s52, 0x80
	s_and_b64 s[16:17], s[16:17], exec
	s_cselect_b32 s16, s47, s49
	v_add_u32_e32 v66, s48, v135
	s_add_i32 m0, s21, 0xc000
	ds_read_b128 v[160:163], v141
	ds_read_b128 v[164:167], v141 offset:1024
	ds_read_b128 v[168:171], v141 offset:2048
	ds_read_b128 v[172:175], v141 offset:3072
	ds_read_b128 v[176:179], v141 offset:4096
	ds_read_b128 v[180:183], v141 offset:5120
	ds_read_b128 v[184:187], v141 offset:6144
	ds_read_b128 v[188:191], v141 offset:7168
	global_load_lds_dwordx4 v66, s[0:1]
	v_add_u32_e32 v66, s48, v136
	s_add_i32 m0, s21, 0xe000
	s_nop 0
	global_load_lds_dwordx4 v66, s[0:1]
	s_waitcnt lgkmcnt(8)
	s_barrier
	s_waitcnt lgkmcnt(0)


	v_mfma_scale_f32_16x16x128_f8f6f4 v[122:125], v[144:151], v[160:167], v[122:125], v142, v142 op_sel_hi:[0,0,0]
	v_mfma_scale_f32_16x16x128_f8f6f4 v[126:129], v[152:159], v[160:167], v[126:129], v142, v142 op_sel_hi:[0,0,0]
	v_mfma_scale_f32_16x16x128_f8f6f4 v[192:195], v[144:151], v[168:175], v[110:113], v142, v142 op_sel_hi:[0,0,0]
	v_mfma_scale_f32_16x16x128_f8f6f4 v[196:199], v[152:159], v[168:175], v[106:109], v142, v142 op_sel_hi:[0,0,0]
	v_mfma_scale_f32_16x16x128_f8f6f4 v[200:203], v[144:151], v[176:183], v[94:97], v142, v142 op_sel_hi:[0,0,0]
	v_mfma_scale_f32_16x16x128_f8f6f4 v[204:207], v[152:159], v[176:183], v[90:93], v142, v142 op_sel_hi:[0,0,0]
	v_mfma_scale_f32_16x16x128_f8f6f4 v[208:211], v[144:151], v[184:191], v[78:81], v142, v142 op_sel_hi:[0,0,0]
	v_mfma_scale_f32_16x16x128_f8f6f4 v[212:215], v[152:159], v[184:191], v[74:77], v142, v142 op_sel_hi:[0,0,0]

	s_barrier
	v_add_u32_e32 v66, s38, v138
	s_add_i32 s17, s37, s20
	s_nop 2
	ds_read_b128 v[74:77], v66
	ds_read_b128 v[78:81], v66 offset:1024
	ds_read_b128 v[90:93], v66 offset:2048
	ds_read_b128 v[94:97], v66 offset:3072
	v_add_u32_e32 v66, s16, v1
	s_mov_b32 m0, s17
	s_nop 0
	global_load_lds_dwordx4 v66, s[2:3]
	v_add_u32_e32 v66, s16, v132
	s_add_i32 m0, s17, 0x2000
	s_nop 0
	global_load_lds_dwordx4 v66, s[2:3]
	s_barrier
	s_waitcnt lgkmcnt(0)


	v_mfma_scale_f32_16x16x128_f8f6f4 v[118:121], v[74:81], v[160:167], v[118:121], v142, v142 op_sel_hi:[0,0,0]
	v_mfma_scale_f32_16x16x128_f8f6f4 v[114:117], v[90:97], v[160:167], v[114:117], v142, v142 op_sel_hi:[0,0,0]
	v_mfma_scale_f32_16x16x128_f8f6f4 v[160:163], v[74:81], v[168:175], v[102:105], v142, v142 op_sel_hi:[0,0,0]
	v_mfma_scale_f32_16x16x128_f8f6f4 v[164:167], v[90:97], v[168:175], v[98:101], v142, v142 op_sel_hi:[0,0,0]
	v_mfma_scale_f32_16x16x128_f8f6f4 v[168:171], v[74:81], v[176:183], v[86:89], v142, v142 op_sel_hi:[0,0,0]
	v_mfma_scale_f32_16x16x128_f8f6f4 v[172:175], v[90:97], v[176:183], v[82:85], v142, v142 op_sel_hi:[0,0,0]
	v_mfma_scale_f32_16x16x128_f8f6f4 v[176:179], v[74:81], v[184:191], v[70:73], v142, v142 op_sel_hi:[0,0,0]
	v_mfma_scale_f32_16x16x128_f8f6f4 v[180:183], v[90:97], v[184:191], v[10:13], v142, v142 op_sel_hi:[0,0,0]

	s_mov_b32 m0, s21
	s_nop 4
	v_add_u32_e32 v10, s52, v133
	s_barrier
	ds_read_b128 v[66:69], v141 offset:16384
	ds_read_b128 v[70:73], v141 offset:17408
	ds_read_b128 v[82:85], v141 offset:18432
	ds_read_b128 v[86:89], v141 offset:19456
	ds_read_b128 v[98:101], v141 offset:20480
	ds_read_b128 v[102:105], v141 offset:21504
	ds_read_b128 v[106:109], v141 offset:22528
	ds_read_b128 v[110:113], v141 offset:23552
	global_load_lds_dwordx4 v10, s[0:1]
	v_add_u32_e32 v10, s52, v134
	s_mov_b32 m0, s22
	s_nop 0
	global_load_lds_dwordx4 v10, s[0:1]
	s_barrier
	s_waitcnt lgkmcnt(0)


	v_mfma_scale_f32_16x16x128_f8f6f4 v[62:65], v[144:151], v[66:73], v[62:65], v142, v142 op_sel_hi:[0,0,0]
	v_mfma_scale_f32_16x16x128_f8f6f4 v[58:61], v[152:159], v[66:73], v[58:61], v142, v142 op_sel_hi:[0,0,0]
	v_mfma_scale_f32_16x16x128_f8f6f4 v[228:231], v[152:159], v[106:113], v[228:231], v142, v142 op_sel_hi:[0,0,0]
	v_mfma_scale_f32_16x16x128_f8f6f4 v[184:187], v[144:151], v[82:89], v[46:49], v142, v142 op_sel_hi:[0,0,0]
	v_mfma_scale_f32_16x16x128_f8f6f4 v[188:191], v[152:159], v[82:89], v[42:45], v142, v142 op_sel_hi:[0,0,0]
	v_mfma_scale_f32_16x16x128_f8f6f4 v[216:219], v[144:151], v[98:105], v[30:33], v142, v142 op_sel_hi:[0,0,0]
	v_mfma_scale_f32_16x16x128_f8f6f4 v[220:223], v[152:159], v[98:105], v[26:29], v142, v142 op_sel_hi:[0,0,0]
	v_mfma_scale_f32_16x16x128_f8f6f4 v[224:227], v[144:151], v[106:113], v[14:17], v142, v142 op_sel_hi:[0,0,0]

	s_barrier
	s_add_i32 s17, s16, 0x1000
	s_add_i32 s53, s38, s20
	v_add_u32_e32 v10, s17, v1
	s_mov_b32 m0, s53
	s_nop 0
	global_load_lds_dwordx4 v10, s[2:3]
	v_add_u32_e32 v10, s17, v132
	s_add_i32 m0, s53, 0x2000
	s_nop 0
	global_load_lds_dwordx4 v10, s[2:3]
	s_waitcnt vmcnt(6)
	s_barrier

	v_mfma_scale_f32_16x16x128_f8f6f4 v[54:57], v[74:81], v[66:73], v[54:57], v142, v142 op_sel_hi:[0,0,0]
	v_mfma_scale_f32_16x16x128_f8f6f4 v[50:53], v[90:97], v[66:73], v[50:53], v142, v142 op_sel_hi:[0,0,0]
	v_mfma_scale_f32_16x16x128_f8f6f4 v[232:235], v[74:81], v[82:89], v[38:41], v142, v142 op_sel_hi:[0,0,0]
	v_mfma_scale_f32_16x16x128_f8f6f4 v[236:239], v[90:97], v[82:89], v[34:37], v142, v142 op_sel_hi:[0,0,0]
	v_mfma_scale_f32_16x16x128_f8f6f4 v[240:243], v[74:81], v[98:105], v[22:25], v142, v142 op_sel_hi:[0,0,0]
	v_mfma_scale_f32_16x16x128_f8f6f4 v[244:247], v[90:97], v[98:105], v[18:21], v142, v142 op_sel_hi:[0,0,0]
	v_mfma_scale_f32_16x16x128_f8f6f4 v[248:251], v[74:81], v[106:113], v[6:9], v142, v142 op_sel_hi:[0,0,0]
	v_mfma_scale_f32_16x16x128_f8f6f4 v[66:69], v[90:97], v[106:113], v[2:5], v142, v142 op_sel_hi:[0,0,0]

	s_add_i32 s17, 0, 0x18000
	v_add_u32_e32 v10, s17, v138
	s_barrier
	s_nop 2
	ds_read_b128 v[2:5], v10
	ds_read_b128 v[6:9], v10 offset:1024
	ds_read_b128 v[18:21], v10 offset:2048
	ds_read_b128 v[22:25], v10 offset:3072
	s_mov_b32 m0, s23
	v_add_u32_e32 v70, s52, v135
	ds_read_b128 v[10:13], v141 offset:32768
	ds_read_b128 v[14:17], v141 offset:33792
	ds_read_b128 v[26:29], v141 offset:34816
	ds_read_b128 v[30:33], v141 offset:35840
	ds_read_b128 v[34:37], v141 offset:36864
	ds_read_b128 v[38:41], v141 offset:37888
	ds_read_b128 v[42:45], v141 offset:38912
	ds_read_b128 v[46:49], v141 offset:39936
	global_load_lds_dwordx4 v70, s[0:1]
	v_add_u32_e32 v70, s52, v136
	s_mov_b32 m0, s24
	s_nop 0
	global_load_lds_dwordx4 v70, s[0:1]
	s_waitcnt lgkmcnt(8)
	s_barrier
	s_waitcnt lgkmcnt(0)


	v_mfma_scale_f32_16x16x128_f8f6f4 v[122:125], v[2:9], v[10:17], v[122:125], v142, v142 op_sel_hi:[0,0,0]
	v_mfma_scale_f32_16x16x128_f8f6f4 v[126:129], v[18:25], v[10:17], v[126:129], v142, v142 op_sel_hi:[0,0,0]
	v_mfma_scale_f32_16x16x128_f8f6f4 v[110:113], v[2:9], v[26:33], v[192:195], v142, v142 op_sel_hi:[0,0,0]
	v_mfma_scale_f32_16x16x128_f8f6f4 v[106:109], v[18:25], v[26:33], v[196:199], v142, v142 op_sel_hi:[0,0,0]
	v_mfma_scale_f32_16x16x128_f8f6f4 v[94:97], v[2:9], v[34:41], v[200:203], v142, v142 op_sel_hi:[0,0,0]
	v_mfma_scale_f32_16x16x128_f8f6f4 v[90:93], v[18:25], v[34:41], v[204:207], v142, v142 op_sel_hi:[0,0,0]
	v_mfma_scale_f32_16x16x128_f8f6f4 v[78:81], v[2:9], v[42:49], v[208:211], v142, v142 op_sel_hi:[0,0,0]
	v_mfma_scale_f32_16x16x128_f8f6f4 v[74:77], v[18:25], v[42:49], v[212:215], v142, v142 op_sel_hi:[0,0,0]

	s_barrier
	s_add_i32 s52, 0, 0x1c000
	v_add_u32_e32 v70, s52, v138
	s_add_i32 s53, s16, 0x80
	s_add_i32 s17, s17, s20
	ds_read_b128 v[144:147], v70
	ds_read_b128 v[148:151], v70 offset:1024
	ds_read_b128 v[152:155], v70 offset:2048
	ds_read_b128 v[156:159], v70 offset:3072
	v_add_u32_e32 v70, s53, v1
	s_mov_b32 m0, s17
	s_nop 0
	global_load_lds_dwordx4 v70, s[2:3]
	v_add_u32_e32 v70, s53, v132
	s_add_i32 m0, s17, 0x2000
	s_nop 0
	global_load_lds_dwordx4 v70, s[2:3]
	s_barrier
	s_waitcnt lgkmcnt(0)


	v_mfma_scale_f32_16x16x128_f8f6f4 v[118:121], v[144:151], v[10:17], v[118:121], v142, v142 op_sel_hi:[0,0,0]
	v_mfma_scale_f32_16x16x128_f8f6f4 v[114:117], v[152:159], v[10:17], v[114:117], v142, v142 op_sel_hi:[0,0,0]
	v_mfma_scale_f32_16x16x128_f8f6f4 v[102:105], v[144:151], v[26:33], v[160:163], v142, v142 op_sel_hi:[0,0,0]
	v_mfma_scale_f32_16x16x128_f8f6f4 v[98:101], v[152:159], v[26:33], v[164:167], v142, v142 op_sel_hi:[0,0,0]
	v_mfma_scale_f32_16x16x128_f8f6f4 v[86:89], v[144:151], v[34:41], v[168:171], v142, v142 op_sel_hi:[0,0,0]
	v_mfma_scale_f32_16x16x128_f8f6f4 v[82:85], v[152:159], v[34:41], v[172:175], v142, v142 op_sel_hi:[0,0,0]
	v_mfma_scale_f32_16x16x128_f8f6f4 v[70:73], v[144:151], v[42:49], v[176:179], v142, v142 op_sel_hi:[0,0,0]
	v_mfma_scale_f32_16x16x128_f8f6f4 v[10:13], v[152:159], v[42:49], v[180:183], v142, v142 op_sel_hi:[0,0,0]

	s_mov_b32 m0, s26
	v_add_u32_e32 v14, s51, v133
	s_barrier
	ds_read_b128 v[34:37], v141 offset:49152
	ds_read_b128 v[38:41], v141 offset:50176
	ds_read_b128 v[160:163], v141 offset:51200
	ds_read_b128 v[164:167], v141 offset:52224
	ds_read_b128 v[168:171], v141 offset:53248
	ds_read_b128 v[172:175], v141 offset:54272
	ds_read_b128 v[176:179], v141 offset:55296
	ds_read_b128 v[180:183], v141 offset:56320
	global_load_lds_dwordx4 v14, s[0:1]
	v_add_u32_e32 v14, s51, v134
	s_mov_b32 m0, s27
	s_nop 0
	global_load_lds_dwordx4 v14, s[0:1]
	s_barrier
	s_waitcnt lgkmcnt(0)


	v_mfma_scale_f32_16x16x128_f8f6f4 v[62:65], v[2:9], v[34:41], v[62:65], v142, v142 op_sel_hi:[0,0,0]
	v_mfma_scale_f32_16x16x128_f8f6f4 v[58:61], v[18:25], v[34:41], v[58:61], v142, v142 op_sel_hi:[0,0,0]
	v_mfma_scale_f32_16x16x128_f8f6f4 v[46:49], v[2:9], v[160:167], v[184:187], v142, v142 op_sel_hi:[0,0,0]
	v_mfma_scale_f32_16x16x128_f8f6f4 v[42:45], v[18:25], v[160:167], v[188:191], v142, v142 op_sel_hi:[0,0,0]
	v_mfma_scale_f32_16x16x128_f8f6f4 v[30:33], v[2:9], v[168:175], v[216:219], v142, v142 op_sel_hi:[0,0,0]
	v_mfma_scale_f32_16x16x128_f8f6f4 v[26:29], v[18:25], v[168:175], v[220:223], v142, v142 op_sel_hi:[0,0,0]
	v_mfma_scale_f32_16x16x128_f8f6f4 v[14:17], v[2:9], v[176:183], v[224:227], v142, v142 op_sel_hi:[0,0,0]
	v_mfma_scale_f32_16x16x128_f8f6f4 v[228:231], v[18:25], v[176:183], v[228:231], v142, v142 op_sel_hi:[0,0,0]

	s_barrier
	s_addk_i32 s16, 0x1080
	s_add_i32 s17, s52, s20
	v_add_u32_e32 v2, s16, v1
	s_mov_b32 m0, s17
	s_nop 0
	global_load_lds_dwordx4 v2, s[2:3]
	v_add_u32_e32 v2, s16, v132
	s_add_i32 m0, s17, 0x2000
	s_nop 0
	global_load_lds_dwordx4 v2, s[2:3]
	s_waitcnt vmcnt(6)
	s_barrier

	v_mfma_scale_f32_16x16x128_f8f6f4 v[54:57], v[144:151], v[34:41], v[54:57], v142, v142 op_sel_hi:[0,0,0]
	v_mfma_scale_f32_16x16x128_f8f6f4 v[50:53], v[152:159], v[34:41], v[50:53], v142, v142 op_sel_hi:[0,0,0]
	v_mfma_scale_f32_16x16x128_f8f6f4 v[38:41], v[144:151], v[160:167], v[232:235], v142, v142 op_sel_hi:[0,0,0]
	v_mfma_scale_f32_16x16x128_f8f6f4 v[34:37], v[152:159], v[160:167], v[236:239], v142, v142 op_sel_hi:[0,0,0]
	v_mfma_scale_f32_16x16x128_f8f6f4 v[22:25], v[144:151], v[168:175], v[240:243], v142, v142 op_sel_hi:[0,0,0]
	v_mfma_scale_f32_16x16x128_f8f6f4 v[18:21], v[152:159], v[168:175], v[244:247], v142, v142 op_sel_hi:[0,0,0]
	v_mfma_scale_f32_16x16x128_f8f6f4 v[6:9], v[144:151], v[176:183], v[248:251], v142, v142 op_sel_hi:[0,0,0]
	v_mfma_scale_f32_16x16x128_f8f6f4 v[2:5], v[152:159], v[176:183], v[66:69], v142, v142 op_sel_hi:[0,0,0]

	s_add_i32 s50, s50, 2
	s_addk_i32 s48, 0x100
	s_addk_i32 s49, 0x100
	s_cmp_ge_i32 s50, s28
	s_barrier
	s_cbranch_scc1 .LBB0_1937

.LBB0_2037:
	v_add_u32_e32 v66, s37, v138
	ds_read_b128 v[144:147], v66
	ds_read_b128 v[148:151], v66 offset:1024
	ds_read_b128 v[152:155], v66 offset:2048
	ds_read_b128 v[156:159], v66 offset:3072
	s_add_i32 s51, s48, 0x80
	s_and_b64 s[52:53], s[16:17], exec
	s_cselect_b32 s52, s46, s51
	s_add_i32 s51, s52, 0x80
	s_and_b64 s[16:17], s[16:17], exec
	s_cselect_b32 s16, s47, s49
	v_add_u32_e32 v66, s48, v135
	s_add_i32 m0, s21, 0xc000
	ds_read_b128 v[160:163], v141
	ds_read_b128 v[164:167], v141 offset:1024
	ds_read_b128 v[168:171], v141 offset:2048
	ds_read_b128 v[172:175], v141 offset:3072
	ds_read_b128 v[176:179], v141 offset:4096
	ds_read_b128 v[180:183], v141 offset:5120
	ds_read_b128 v[184:187], v141 offset:6144
	ds_read_b128 v[188:191], v141 offset:7168
	global_load_lds_dwordx4 v66, s[0:1]
	v_add_u32_e32 v66, s48, v136
	s_add_i32 m0, s21, 0xe000
	s_nop 0
	global_load_lds_dwordx4 v66, s[0:1]
	s_waitcnt lgkmcnt(8)
	s_barrier
	s_waitcnt lgkmcnt(0)


	v_mfma_scale_f32_16x16x128_f8f6f4 v[122:125], v[144:151], v[160:167], v[122:125], v142, v142 op_sel_hi:[0,0,0]
	v_mfma_scale_f32_16x16x128_f8f6f4 v[126:129], v[152:159], v[160:167], v[126:129], v142, v142 op_sel_hi:[0,0,0]
	v_mfma_scale_f32_16x16x128_f8f6f4 v[192:195], v[144:151], v[168:175], v[110:113], v142, v142 op_sel_hi:[0,0,0]
	v_mfma_scale_f32_16x16x128_f8f6f4 v[196:199], v[152:159], v[168:175], v[106:109], v142, v142 op_sel_hi:[0,0,0]
	v_mfma_scale_f32_16x16x128_f8f6f4 v[200:203], v[144:151], v[176:183], v[94:97], v142, v142 op_sel_hi:[0,0,0]
	v_mfma_scale_f32_16x16x128_f8f6f4 v[204:207], v[152:159], v[176:183], v[90:93], v142, v142 op_sel_hi:[0,0,0]
	v_mfma_scale_f32_16x16x128_f8f6f4 v[208:211], v[144:151], v[184:191], v[78:81], v142, v142 op_sel_hi:[0,0,0]
	v_mfma_scale_f32_16x16x128_f8f6f4 v[212:215], v[152:159], v[184:191], v[74:77], v142, v142 op_sel_hi:[0,0,0]

	s_barrier
	v_add_u32_e32 v66, s38, v138
	s_add_i32 s17, s37, s20
	s_nop 2
	ds_read_b128 v[74:77], v66
	ds_read_b128 v[78:81], v66 offset:1024
	ds_read_b128 v[90:93], v66 offset:2048
	ds_read_b128 v[94:97], v66 offset:3072
	v_add_u32_e32 v66, s16, v1
	s_mov_b32 m0, s17
	s_nop 0
	global_load_lds_dwordx4 v66, s[2:3]
	v_add_u32_e32 v66, s16, v132
	s_add_i32 m0, s17, 0x2000
	s_nop 0
	global_load_lds_dwordx4 v66, s[2:3]
	s_barrier
	s_waitcnt lgkmcnt(0)


	v_mfma_scale_f32_16x16x128_f8f6f4 v[118:121], v[74:81], v[160:167], v[118:121], v142, v142 op_sel_hi:[0,0,0]
	v_mfma_scale_f32_16x16x128_f8f6f4 v[114:117], v[90:97], v[160:167], v[114:117], v142, v142 op_sel_hi:[0,0,0]
	v_mfma_scale_f32_16x16x128_f8f6f4 v[160:163], v[74:81], v[168:175], v[102:105], v142, v142 op_sel_hi:[0,0,0]
	v_mfma_scale_f32_16x16x128_f8f6f4 v[164:167], v[90:97], v[168:175], v[98:101], v142, v142 op_sel_hi:[0,0,0]
	v_mfma_scale_f32_16x16x128_f8f6f4 v[168:171], v[74:81], v[176:183], v[86:89], v142, v142 op_sel_hi:[0,0,0]
	v_mfma_scale_f32_16x16x128_f8f6f4 v[172:175], v[90:97], v[176:183], v[82:85], v142, v142 op_sel_hi:[0,0,0]
	v_mfma_scale_f32_16x16x128_f8f6f4 v[176:179], v[74:81], v[184:191], v[70:73], v142, v142 op_sel_hi:[0,0,0]
	v_mfma_scale_f32_16x16x128_f8f6f4 v[180:183], v[90:97], v[184:191], v[10:13], v142, v142 op_sel_hi:[0,0,0]

	s_mov_b32 m0, s21
	s_nop 4
	v_add_u32_e32 v10, s52, v133
	s_barrier
	ds_read_b128 v[66:69], v141 offset:16384
	ds_read_b128 v[70:73], v141 offset:17408
	ds_read_b128 v[82:85], v141 offset:18432
	ds_read_b128 v[86:89], v141 offset:19456
	ds_read_b128 v[98:101], v141 offset:20480
	ds_read_b128 v[102:105], v141 offset:21504
	ds_read_b128 v[106:109], v141 offset:22528
	ds_read_b128 v[110:113], v141 offset:23552
	global_load_lds_dwordx4 v10, s[0:1]
	v_add_u32_e32 v10, s52, v134
	s_mov_b32 m0, s22
	s_nop 0
	global_load_lds_dwordx4 v10, s[0:1]
	s_barrier
	s_waitcnt lgkmcnt(0)


	v_mfma_scale_f32_16x16x128_f8f6f4 v[62:65], v[144:151], v[66:73], v[62:65], v142, v142 op_sel_hi:[0,0,0]
	v_mfma_scale_f32_16x16x128_f8f6f4 v[58:61], v[152:159], v[66:73], v[58:61], v142, v142 op_sel_hi:[0,0,0]
	v_mfma_scale_f32_16x16x128_f8f6f4 v[228:231], v[152:159], v[106:113], v[228:231], v142, v142 op_sel_hi:[0,0,0]
	v_mfma_scale_f32_16x16x128_f8f6f4 v[184:187], v[144:151], v[82:89], v[46:49], v142, v142 op_sel_hi:[0,0,0]
	v_mfma_scale_f32_16x16x128_f8f6f4 v[188:191], v[152:159], v[82:89], v[42:45], v142, v142 op_sel_hi:[0,0,0]
	v_mfma_scale_f32_16x16x128_f8f6f4 v[216:219], v[144:151], v[98:105], v[30:33], v142, v142 op_sel_hi:[0,0,0]
	v_mfma_scale_f32_16x16x128_f8f6f4 v[220:223], v[152:159], v[98:105], v[26:29], v142, v142 op_sel_hi:[0,0,0]
	v_mfma_scale_f32_16x16x128_f8f6f4 v[224:227], v[144:151], v[106:113], v[14:17], v142, v142 op_sel_hi:[0,0,0]

	s_barrier
	s_add_i32 s17, s16, 0x1000
	s_add_i32 s53, s38, s20
	v_add_u32_e32 v10, s17, v1
	s_mov_b32 m0, s53
	s_nop 0
	global_load_lds_dwordx4 v10, s[2:3]
	v_add_u32_e32 v10, s17, v132
	s_add_i32 m0, s53, 0x2000
	s_nop 0
	global_load_lds_dwordx4 v10, s[2:3]
	s_waitcnt vmcnt(6)
	s_barrier

	v_mfma_scale_f32_16x16x128_f8f6f4 v[54:57], v[74:81], v[66:73], v[54:57], v142, v142 op_sel_hi:[0,0,0]
	v_mfma_scale_f32_16x16x128_f8f6f4 v[50:53], v[90:97], v[66:73], v[50:53], v142, v142 op_sel_hi:[0,0,0]
	v_mfma_scale_f32_16x16x128_f8f6f4 v[232:235], v[74:81], v[82:89], v[38:41], v142, v142 op_sel_hi:[0,0,0]
	v_mfma_scale_f32_16x16x128_f8f6f4 v[236:239], v[90:97], v[82:89], v[34:37], v142, v142 op_sel_hi:[0,0,0]
	v_mfma_scale_f32_16x16x128_f8f6f4 v[240:243], v[74:81], v[98:105], v[22:25], v142, v142 op_sel_hi:[0,0,0]
	v_mfma_scale_f32_16x16x128_f8f6f4 v[244:247], v[90:97], v[98:105], v[18:21], v142, v142 op_sel_hi:[0,0,0]
	v_mfma_scale_f32_16x16x128_f8f6f4 v[248:251], v[74:81], v[106:113], v[6:9], v142, v142 op_sel_hi:[0,0,0]
	v_mfma_scale_f32_16x16x128_f8f6f4 v[66:69], v[90:97], v[106:113], v[2:5], v142, v142 op_sel_hi:[0,0,0]

	s_add_i32 s17, 0, 0x18000
	v_add_u32_e32 v10, s17, v138
	s_barrier
	s_nop 2
	ds_read_b128 v[2:5], v10
	ds_read_b128 v[6:9], v10 offset:1024
	ds_read_b128 v[18:21], v10 offset:2048
	ds_read_b128 v[22:25], v10 offset:3072
	s_mov_b32 m0, s23
	v_add_u32_e32 v70, s52, v135
	ds_read_b128 v[10:13], v141 offset:32768
	ds_read_b128 v[14:17], v141 offset:33792
	ds_read_b128 v[26:29], v141 offset:34816
	ds_read_b128 v[30:33], v141 offset:35840
	ds_read_b128 v[34:37], v141 offset:36864
	ds_read_b128 v[38:41], v141 offset:37888
	ds_read_b128 v[42:45], v141 offset:38912
	ds_read_b128 v[46:49], v141 offset:39936
	global_load_lds_dwordx4 v70, s[0:1]
	v_add_u32_e32 v70, s52, v136
	s_mov_b32 m0, s24
	s_nop 0
	global_load_lds_dwordx4 v70, s[0:1]
	s_waitcnt lgkmcnt(8)
	s_barrier
	s_waitcnt lgkmcnt(0)


	v_mfma_scale_f32_16x16x128_f8f6f4 v[122:125], v[2:9], v[10:17], v[122:125], v142, v142 op_sel_hi:[0,0,0]
	v_mfma_scale_f32_16x16x128_f8f6f4 v[126:129], v[18:25], v[10:17], v[126:129], v142, v142 op_sel_hi:[0,0,0]
	v_mfma_scale_f32_16x16x128_f8f6f4 v[110:113], v[2:9], v[26:33], v[192:195], v142, v142 op_sel_hi:[0,0,0]
	v_mfma_scale_f32_16x16x128_f8f6f4 v[106:109], v[18:25], v[26:33], v[196:199], v142, v142 op_sel_hi:[0,0,0]
	v_mfma_scale_f32_16x16x128_f8f6f4 v[94:97], v[2:9], v[34:41], v[200:203], v142, v142 op_sel_hi:[0,0,0]
	v_mfma_scale_f32_16x16x128_f8f6f4 v[90:93], v[18:25], v[34:41], v[204:207], v142, v142 op_sel_hi:[0,0,0]
	v_mfma_scale_f32_16x16x128_f8f6f4 v[78:81], v[2:9], v[42:49], v[208:211], v142, v142 op_sel_hi:[0,0,0]
	v_mfma_scale_f32_16x16x128_f8f6f4 v[74:77], v[18:25], v[42:49], v[212:215], v142, v142 op_sel_hi:[0,0,0]

	s_barrier
	s_add_i32 s52, 0, 0x1c000
	v_add_u32_e32 v70, s52, v138
	s_add_i32 s53, s16, 0x80
	s_add_i32 s17, s17, s20
	ds_read_b128 v[144:147], v70
	ds_read_b128 v[148:151], v70 offset:1024
	ds_read_b128 v[152:155], v70 offset:2048
	ds_read_b128 v[156:159], v70 offset:3072
	v_add_u32_e32 v70, s53, v1
	s_mov_b32 m0, s17
	s_nop 0
	global_load_lds_dwordx4 v70, s[2:3]
	v_add_u32_e32 v70, s53, v132
	s_add_i32 m0, s17, 0x2000
	s_nop 0
	global_load_lds_dwordx4 v70, s[2:3]
	s_barrier
	s_waitcnt lgkmcnt(0)


	v_mfma_scale_f32_16x16x128_f8f6f4 v[118:121], v[144:151], v[10:17], v[118:121], v142, v142 op_sel_hi:[0,0,0]
	v_mfma_scale_f32_16x16x128_f8f6f4 v[114:117], v[152:159], v[10:17], v[114:117], v142, v142 op_sel_hi:[0,0,0]
	v_mfma_scale_f32_16x16x128_f8f6f4 v[102:105], v[144:151], v[26:33], v[160:163], v142, v142 op_sel_hi:[0,0,0]
	v_mfma_scale_f32_16x16x128_f8f6f4 v[98:101], v[152:159], v[26:33], v[164:167], v142, v142 op_sel_hi:[0,0,0]
	v_mfma_scale_f32_16x16x128_f8f6f4 v[86:89], v[144:151], v[34:41], v[168:171], v142, v142 op_sel_hi:[0,0,0]
	v_mfma_scale_f32_16x16x128_f8f6f4 v[82:85], v[152:159], v[34:41], v[172:175], v142, v142 op_sel_hi:[0,0,0]
	v_mfma_scale_f32_16x16x128_f8f6f4 v[70:73], v[144:151], v[42:49], v[176:179], v142, v142 op_sel_hi:[0,0,0]
	v_mfma_scale_f32_16x16x128_f8f6f4 v[10:13], v[152:159], v[42:49], v[180:183], v142, v142 op_sel_hi:[0,0,0]

	s_mov_b32 m0, s26
	v_add_u32_e32 v14, s51, v133
	s_barrier
	ds_read_b128 v[34:37], v141 offset:49152
	ds_read_b128 v[38:41], v141 offset:50176
	ds_read_b128 v[160:163], v141 offset:51200
	ds_read_b128 v[164:167], v141 offset:52224
	ds_read_b128 v[168:171], v141 offset:53248
	ds_read_b128 v[172:175], v141 offset:54272
	ds_read_b128 v[176:179], v141 offset:55296
	ds_read_b128 v[180:183], v141 offset:56320
	global_load_lds_dwordx4 v14, s[0:1]
	v_add_u32_e32 v14, s51, v134
	s_mov_b32 m0, s27
	s_nop 0
	global_load_lds_dwordx4 v14, s[0:1]
	s_barrier
	s_waitcnt lgkmcnt(0)


	v_mfma_scale_f32_16x16x128_f8f6f4 v[62:65], v[2:9], v[34:41], v[62:65], v142, v142 op_sel_hi:[0,0,0]
	v_mfma_scale_f32_16x16x128_f8f6f4 v[58:61], v[18:25], v[34:41], v[58:61], v142, v142 op_sel_hi:[0,0,0]
	v_mfma_scale_f32_16x16x128_f8f6f4 v[46:49], v[2:9], v[160:167], v[184:187], v142, v142 op_sel_hi:[0,0,0]
	v_mfma_scale_f32_16x16x128_f8f6f4 v[42:45], v[18:25], v[160:167], v[188:191], v142, v142 op_sel_hi:[0,0,0]
	v_mfma_scale_f32_16x16x128_f8f6f4 v[30:33], v[2:9], v[168:175], v[216:219], v142, v142 op_sel_hi:[0,0,0]
	v_mfma_scale_f32_16x16x128_f8f6f4 v[26:29], v[18:25], v[168:175], v[220:223], v142, v142 op_sel_hi:[0,0,0]
	v_mfma_scale_f32_16x16x128_f8f6f4 v[14:17], v[2:9], v[176:183], v[224:227], v142, v142 op_sel_hi:[0,0,0]
	v_mfma_scale_f32_16x16x128_f8f6f4 v[228:231], v[18:25], v[176:183], v[228:231], v142, v142 op_sel_hi:[0,0,0]

	s_barrier
	s_addk_i32 s16, 0x1080
	s_add_i32 s17, s52, s20
	v_add_u32_e32 v2, s16, v1
	s_mov_b32 m0, s17
	s_nop 0
	global_load_lds_dwordx4 v2, s[2:3]
	v_add_u32_e32 v2, s16, v132
	s_add_i32 m0, s17, 0x2000
	s_nop 0
	global_load_lds_dwordx4 v2, s[2:3]
	s_waitcnt vmcnt(6)
	s_barrier

	v_mfma_scale_f32_16x16x128_f8f6f4 v[54:57], v[144:151], v[34:41], v[54:57], v142, v142 op_sel_hi:[0,0,0]
	v_mfma_scale_f32_16x16x128_f8f6f4 v[50:53], v[152:159], v[34:41], v[50:53], v142, v142 op_sel_hi:[0,0,0]
	v_mfma_scale_f32_16x16x128_f8f6f4 v[38:41], v[144:151], v[160:167], v[232:235], v142, v142 op_sel_hi:[0,0,0]
	v_mfma_scale_f32_16x16x128_f8f6f4 v[34:37], v[152:159], v[160:167], v[236:239], v142, v142 op_sel_hi:[0,0,0]
	v_mfma_scale_f32_16x16x128_f8f6f4 v[22:25], v[144:151], v[168:175], v[240:243], v142, v142 op_sel_hi:[0,0,0]
	v_mfma_scale_f32_16x16x128_f8f6f4 v[18:21], v[152:159], v[168:175], v[244:247], v142, v142 op_sel_hi:[0,0,0]
	v_mfma_scale_f32_16x16x128_f8f6f4 v[6:9], v[144:151], v[176:183], v[248:251], v142, v142 op_sel_hi:[0,0,0]
	v_mfma_scale_f32_16x16x128_f8f6f4 v[2:5], v[152:159], v[176:183], v[66:69], v142, v142 op_sel_hi:[0,0,0]

	s_add_i32 s50, s50, 2
	s_addk_i32 s48, 0x100
	s_addk_i32 s49, 0x100
	s_cmp_ge_i32 s50, s28
	s_barrier
	s_cbranch_scc1 .LBB0_2027

.LBB0_2398:
	ds_read_b128 v[98:101], v212
	ds_read_b128 v[102:105], v212 offset:1024
	ds_read_b128 v[138:141], v212 offset:2048
	ds_read_b128 v[142:145], v212 offset:3072
	s_add_i32 s59, s56, 0x80
	s_cmp_eq_u32 s47, s58
	s_cselect_b32 s61, s34, s59
	s_cselect_b32 s59, s35, s57
	s_or_b32 s60, s61, 0x80
	v_add_u32_e32 v162, s56, v207
	s_add_i32 m0, s38, 0xc000
	ds_read_b128 v[146:149], v213
	ds_read_b128 v[150:153], v213 offset:1024
	ds_read_b128 v[154:157], v213 offset:2048
	ds_read_b128 v[158:161], v213 offset:3072
	ds_read_b128 v[170:173], v213 offset:4096
	ds_read_b128 v[174:177], v213 offset:5120
	ds_read_b128 v[178:181], v213 offset:6144
	ds_read_b128 v[182:185], v213 offset:7168
	global_load_lds_dwordx4 v162, s[4:5]
	v_add_u32_e32 v162, s56, v208
	s_add_i32 m0, s38, 0xe000
	s_nop 0
	global_load_lds_dwordx4 v162, s[4:5]
	s_waitcnt lgkmcnt(8)
	s_barrier
	s_waitcnt lgkmcnt(0)


	v_mfma_scale_f32_16x16x128_f8f6f4 v[134:137], v[98:105], v[146:153], v[134:137], v214, v214 op_sel_hi:[0,0,0]
	v_mfma_scale_f32_16x16x128_f8f6f4 v[130:133], v[138:145], v[146:153], v[130:133], v214, v214 op_sel_hi:[0,0,0]
	v_mfma_scale_f32_16x16x128_f8f6f4 v[126:129], v[98:105], v[154:161], v[126:129], v214, v214 op_sel_hi:[0,0,0]
	v_mfma_scale_f32_16x16x128_f8f6f4 v[122:125], v[138:145], v[154:161], v[122:125], v214, v214 op_sel_hi:[0,0,0]
	v_mfma_scale_f32_16x16x128_f8f6f4 v[162:165], v[98:105], v[170:177], v[118:121], v214, v214 op_sel_hi:[0,0,0]
	v_mfma_scale_f32_16x16x128_f8f6f4 v[186:189], v[138:145], v[170:177], v[114:117], v214, v214 op_sel_hi:[0,0,0]
	v_mfma_scale_f32_16x16x128_f8f6f4 v[190:193], v[98:105], v[178:185], v[110:113], v214, v214 op_sel_hi:[0,0,0]
	v_mfma_scale_f32_16x16x128_f8f6f4 v[194:197], v[138:145], v[178:185], v[106:109], v214, v214 op_sel_hi:[0,0,0]

	s_barrier
	s_add_i32 s62, s48, s36
	v_add_u32_e32 v198, s59, v1
	s_mov_b32 m0, s62
	s_nop 1
	ds_read_b128 v[106:109], v215
	ds_read_b128 v[110:113], v215 offset:1024
	ds_read_b128 v[114:117], v215 offset:2048
	ds_read_b128 v[118:121], v215 offset:3072
	global_load_lds_dwordx4 v198, s[6:7]
	v_add_u32_e32 v198, s59, v204
	s_add_i32 m0, s62, 0x2000
	s_nop 0
	global_load_lds_dwordx4 v198, s[6:7]
	s_barrier
	s_waitcnt lgkmcnt(0)


	v_mfma_scale_f32_16x16x128_f8f6f4 v[198:201], v[106:113], v[146:153], v[62:65], v214, v214 op_sel_hi:[0,0,0]
	v_mfma_scale_f32_16x16x128_f8f6f4 v[146:149], v[114:121], v[146:153], v[58:61], v214, v214 op_sel_hi:[0,0,0]
	v_mfma_scale_f32_16x16x128_f8f6f4 v[150:153], v[106:113], v[154:161], v[54:57], v214, v214 op_sel_hi:[0,0,0]
	v_mfma_scale_f32_16x16x128_f8f6f4 v[154:157], v[114:121], v[154:161], v[50:53], v214, v214 op_sel_hi:[0,0,0]
	v_mfma_scale_f32_16x16x128_f8f6f4 v[158:161], v[106:113], v[170:177], v[46:49], v214, v214 op_sel_hi:[0,0,0]
	v_mfma_scale_f32_16x16x128_f8f6f4 v[170:173], v[114:121], v[170:177], v[42:45], v214, v214 op_sel_hi:[0,0,0]
	v_mfma_scale_f32_16x16x128_f8f6f4 v[174:177], v[106:113], v[178:185], v[38:41], v214, v214 op_sel_hi:[0,0,0]
	v_mfma_scale_f32_16x16x128_f8f6f4 v[178:181], v[114:121], v[178:185], v[34:37], v214, v214 op_sel_hi:[0,0,0]

	s_mov_b32 m0, s38
	v_add_u32_e32 v182, s61, v205
	s_barrier
	s_nop 2
	ds_read_b128 v[34:37], v213 offset:16384
	ds_read_b128 v[38:41], v213 offset:17408
	ds_read_b128 v[42:45], v213 offset:18432
	ds_read_b128 v[46:49], v213 offset:19456
	ds_read_b128 v[50:53], v213 offset:20480
	ds_read_b128 v[54:57], v213 offset:21504
	ds_read_b128 v[58:61], v213 offset:22528
	ds_read_b128 v[62:65], v213 offset:23552
	global_load_lds_dwordx4 v182, s[4:5]
	v_add_u32_e32 v182, s61, v206
	s_mov_b32 m0, s39
	s_nop 0
	global_load_lds_dwordx4 v182, s[4:5]
	s_barrier
	s_waitcnt lgkmcnt(0)


	v_mfma_scale_f32_16x16x128_f8f6f4 v[94:97], v[98:105], v[34:41], v[94:97], v214, v214 op_sel_hi:[0,0,0]
	v_mfma_scale_f32_16x16x128_f8f6f4 v[90:93], v[138:145], v[34:41], v[90:93], v214, v214 op_sel_hi:[0,0,0]
	v_mfma_scale_f32_16x16x128_f8f6f4 v[86:89], v[98:105], v[42:49], v[86:89], v214, v214 op_sel_hi:[0,0,0]
	v_mfma_scale_f32_16x16x128_f8f6f4 v[82:85], v[138:145], v[42:49], v[82:85], v214, v214 op_sel_hi:[0,0,0]
	v_mfma_scale_f32_16x16x128_f8f6f4 v[78:81], v[98:105], v[50:57], v[78:81], v214, v214 op_sel_hi:[0,0,0]
	v_mfma_scale_f32_16x16x128_f8f6f4 v[74:77], v[138:145], v[50:57], v[74:77], v214, v214 op_sel_hi:[0,0,0]
	v_mfma_scale_f32_16x16x128_f8f6f4 v[182:185], v[98:105], v[58:65], v[70:73], v214, v214 op_sel_hi:[0,0,0]
	v_mfma_scale_f32_16x16x128_f8f6f4 v[216:219], v[138:145], v[58:65], v[66:69], v214, v214 op_sel_hi:[0,0,0]

	s_barrier
	s_add_i32 s62, s59, 0x40000
	s_add_i32 s63, s49, s36
	s_nop 2
	v_add_u32_e32 v66, s62, v1
	s_mov_b32 m0, s63
	s_nop 0
	global_load_lds_dwordx4 v66, s[6:7]
	v_add_u32_e32 v66, s62, v204
	s_add_i32 m0, s63, 0x2000
	s_nop 0
	global_load_lds_dwordx4 v66, s[6:7]
	s_waitcnt vmcnt(6)
	s_barrier

	v_mfma_scale_f32_16x16x128_f8f6f4 v[220:223], v[106:113], v[34:41], v[30:33], v214, v214 op_sel_hi:[0,0,0]
	v_mfma_scale_f32_16x16x128_f8f6f4 v[224:227], v[114:121], v[34:41], v[26:29], v214, v214 op_sel_hi:[0,0,0]
	v_mfma_scale_f32_16x16x128_f8f6f4 v[228:231], v[106:113], v[42:49], v[22:25], v214, v214 op_sel_hi:[0,0,0]
	v_mfma_scale_f32_16x16x128_f8f6f4 v[232:235], v[114:121], v[42:49], v[18:21], v214, v214 op_sel_hi:[0,0,0]
	v_mfma_scale_f32_16x16x128_f8f6f4 v[236:239], v[106:113], v[50:57], v[14:17], v214, v214 op_sel_hi:[0,0,0]
	v_mfma_scale_f32_16x16x128_f8f6f4 v[240:243], v[114:121], v[50:57], v[10:13], v214, v214 op_sel_hi:[0,0,0]
	v_mfma_scale_f32_16x16x128_f8f6f4 v[244:247], v[106:113], v[58:65], v[6:9], v214, v214 op_sel_hi:[0,0,0]
	v_mfma_scale_f32_16x16x128_f8f6f4 v[248:251], v[114:121], v[58:65], v[2:5], v214, v214 op_sel_hi:[0,0,0]

	s_add_i32 s62, 0, 0x18000
	s_nop 1
	v_add_u32_e32 v14, s62, v211
	s_barrier
	s_nop 0
	ds_read_b128 v[2:5], v14
	ds_read_b128 v[6:9], v14 offset:1024
	ds_read_b128 v[10:13], v14 offset:2048
	ds_read_b128 v[14:17], v14 offset:3072
	s_mov_b32 m0, s41
	v_add_u32_e32 v42, s61, v207
	ds_read_b128 v[18:21], v213 offset:32768
	ds_read_b128 v[22:25], v213 offset:33792
	ds_read_b128 v[26:29], v213 offset:34816
	ds_read_b128 v[30:33], v213 offset:35840
	ds_read_b128 v[34:37], v213 offset:36864
	ds_read_b128 v[38:41], v213 offset:37888
	ds_read_b128 v[66:69], v213 offset:38912
	ds_read_b128 v[70:73], v213 offset:39936
	global_load_lds_dwordx4 v42, s[4:5]
	v_add_u32_e32 v42, s61, v208
	s_mov_b32 m0, s42
	s_nop 0
	global_load_lds_dwordx4 v42, s[4:5]
	s_waitcnt lgkmcnt(8)
	s_barrier
	s_waitcnt lgkmcnt(0)


	v_mfma_scale_f32_16x16x128_f8f6f4 v[134:137], v[2:9], v[18:25], v[134:137], v214, v214 op_sel_hi:[0,0,0]
	v_mfma_scale_f32_16x16x128_f8f6f4 v[130:133], v[10:17], v[18:25], v[130:133], v214, v214 op_sel_hi:[0,0,0]
	v_mfma_scale_f32_16x16x128_f8f6f4 v[126:129], v[2:9], v[26:33], v[126:129], v214, v214 op_sel_hi:[0,0,0]
	v_mfma_scale_f32_16x16x128_f8f6f4 v[122:125], v[10:17], v[26:33], v[122:125], v214, v214 op_sel_hi:[0,0,0]
	v_mfma_scale_f32_16x16x128_f8f6f4 v[118:121], v[2:9], v[34:41], v[162:165], v214, v214 op_sel_hi:[0,0,0]
	v_mfma_scale_f32_16x16x128_f8f6f4 v[114:117], v[10:17], v[34:41], v[186:189], v214, v214 op_sel_hi:[0,0,0]
	v_mfma_scale_f32_16x16x128_f8f6f4 v[110:113], v[2:9], v[66:73], v[190:193], v214, v214 op_sel_hi:[0,0,0]
	v_mfma_scale_f32_16x16x128_f8f6f4 v[106:109], v[10:17], v[66:73], v[194:197], v214, v214 op_sel_hi:[0,0,0]

	s_barrier
	s_add_i32 s61, 0, 0x1c000
	v_add_u32_e32 v42, s61, v211
	s_or_b32 s63, s59, 0x80
	s_add_i32 s62, s62, s36
	ds_read_b128 v[98:101], v42
	ds_read_b128 v[102:105], v42 offset:1024
	ds_read_b128 v[138:141], v42 offset:2048
	ds_read_b128 v[142:145], v42 offset:3072
	v_add_u32_e32 v42, s63, v1
	s_mov_b32 m0, s62
	s_nop 0
	global_load_lds_dwordx4 v42, s[6:7]
	v_add_u32_e32 v42, s63, v204
	s_add_i32 m0, s62, 0x2000
	s_nop 0
	global_load_lds_dwordx4 v42, s[6:7]
	s_barrier
	s_waitcnt lgkmcnt(0)


	v_mfma_scale_f32_16x16x128_f8f6f4 v[62:65], v[98:105], v[18:25], v[198:201], v214, v214 op_sel_hi:[0,0,0]
	v_mfma_scale_f32_16x16x128_f8f6f4 v[58:61], v[138:145], v[18:25], v[146:149], v214, v214 op_sel_hi:[0,0,0]
	v_mfma_scale_f32_16x16x128_f8f6f4 v[54:57], v[98:105], v[26:33], v[150:153], v214, v214 op_sel_hi:[0,0,0]
	v_mfma_scale_f32_16x16x128_f8f6f4 v[50:53], v[138:145], v[26:33], v[154:157], v214, v214 op_sel_hi:[0,0,0]
	v_mfma_scale_f32_16x16x128_f8f6f4 v[46:49], v[98:105], v[34:41], v[158:161], v214, v214 op_sel_hi:[0,0,0]
	v_mfma_scale_f32_16x16x128_f8f6f4 v[42:45], v[138:145], v[34:41], v[170:173], v214, v214 op_sel_hi:[0,0,0]
	v_mfma_scale_f32_16x16x128_f8f6f4 v[38:41], v[98:105], v[66:73], v[174:177], v214, v214 op_sel_hi:[0,0,0]
	v_mfma_scale_f32_16x16x128_f8f6f4 v[34:37], v[138:145], v[66:73], v[178:181], v214, v214 op_sel_hi:[0,0,0]

	s_mov_b32 m0, s43
	v_add_u32_e32 v26, s60, v205
	s_barrier
	ds_read_b128 v[18:21], v213 offset:49152
	ds_read_b128 v[22:25], v213 offset:50176
	ds_read_b128 v[146:149], v213 offset:51200
	ds_read_b128 v[150:153], v213 offset:52224
	ds_read_b128 v[154:157], v213 offset:53248
	ds_read_b128 v[158:161], v213 offset:54272
	ds_read_b128 v[170:173], v213 offset:55296
	ds_read_b128 v[174:177], v213 offset:56320
	global_load_lds_dwordx4 v26, s[4:5]
	v_add_u32_e32 v26, s60, v206
	s_mov_b32 m0, s44
	s_nop 0
	global_load_lds_dwordx4 v26, s[4:5]
	s_barrier
	s_waitcnt lgkmcnt(0)


	v_mfma_scale_f32_16x16x128_f8f6f4 v[94:97], v[2:9], v[18:25], v[94:97], v214, v214 op_sel_hi:[0,0,0]
	v_mfma_scale_f32_16x16x128_f8f6f4 v[90:93], v[10:17], v[18:25], v[90:93], v214, v214 op_sel_hi:[0,0,0]
	v_mfma_scale_f32_16x16x128_f8f6f4 v[86:89], v[2:9], v[146:153], v[86:89], v214, v214 op_sel_hi:[0,0,0]
	v_mfma_scale_f32_16x16x128_f8f6f4 v[82:85], v[10:17], v[146:153], v[82:85], v214, v214 op_sel_hi:[0,0,0]
	v_mfma_scale_f32_16x16x128_f8f6f4 v[78:81], v[2:9], v[154:161], v[78:81], v214, v214 op_sel_hi:[0,0,0]
	v_mfma_scale_f32_16x16x128_f8f6f4 v[74:77], v[10:17], v[154:161], v[74:77], v214, v214 op_sel_hi:[0,0,0]
	v_mfma_scale_f32_16x16x128_f8f6f4 v[70:73], v[2:9], v[170:177], v[182:185], v214, v214 op_sel_hi:[0,0,0]
	v_mfma_scale_f32_16x16x128_f8f6f4 v[66:69], v[10:17], v[170:177], v[216:219], v214, v214 op_sel_hi:[0,0,0]

	s_barrier
	s_add_i32 s59, s59, 0x40080
	s_add_i32 s60, s61, s36
	v_add_u32_e32 v2, s59, v1
	s_mov_b32 m0, s60
	s_nop 0
	global_load_lds_dwordx4 v2, s[6:7]
	v_add_u32_e32 v2, s59, v204
	s_add_i32 m0, s60, 0x2000
	s_nop 0
	global_load_lds_dwordx4 v2, s[6:7]
	s_waitcnt vmcnt(6)
	s_barrier

	v_mfma_scale_f32_16x16x128_f8f6f4 v[30:33], v[98:105], v[18:25], v[220:223], v214, v214 op_sel_hi:[0,0,0]
	v_mfma_scale_f32_16x16x128_f8f6f4 v[26:29], v[138:145], v[18:25], v[224:227], v214, v214 op_sel_hi:[0,0,0]
	v_mfma_scale_f32_16x16x128_f8f6f4 v[22:25], v[98:105], v[146:153], v[228:231], v214, v214 op_sel_hi:[0,0,0]
	v_mfma_scale_f32_16x16x128_f8f6f4 v[18:21], v[138:145], v[146:153], v[232:235], v214, v214 op_sel_hi:[0,0,0]
	v_mfma_scale_f32_16x16x128_f8f6f4 v[14:17], v[98:105], v[154:161], v[236:239], v214, v214 op_sel_hi:[0,0,0]
	v_mfma_scale_f32_16x16x128_f8f6f4 v[10:13], v[138:145], v[154:161], v[240:243], v214, v214 op_sel_hi:[0,0,0]
	v_mfma_scale_f32_16x16x128_f8f6f4 v[6:9], v[98:105], v[170:177], v[244:247], v214, v214 op_sel_hi:[0,0,0]
	v_mfma_scale_f32_16x16x128_f8f6f4 v[2:5], v[138:145], v[170:177], v[248:251], v214, v214 op_sel_hi:[0,0,0]

	s_add_i32 s58, s58, 2
	s_addk_i32 s56, 0x100
	s_addk_i32 s57, 0x100
	s_cmp_ge_i32 s58, s45
	s_barrier
	s_cbranch_scc0 .LBB0_2398
	s_branch .LBB0_2393

.LBB0_2505:
	ds_read_b128 v[98:101], v212
	ds_read_b128 v[102:105], v212 offset:1024
	ds_read_b128 v[138:141], v212 offset:2048
	ds_read_b128 v[142:145], v212 offset:3072
	s_add_i32 s58, s55, 0x80
	s_cmp_eq_u32 s48, s57
	s_cselect_b32 s60, s2, s58
	s_cselect_b32 s58, s3, s56
	s_or_b32 s59, s60, 0x80
	v_add_u32_e32 v162, s55, v207
	s_add_i32 m0, s39, 0xc000
	ds_read_b128 v[146:149], v213
	ds_read_b128 v[150:153], v213 offset:1024
	ds_read_b128 v[154:157], v213 offset:2048
	ds_read_b128 v[158:161], v213 offset:3072
	ds_read_b128 v[170:173], v213 offset:4096
	ds_read_b128 v[174:177], v213 offset:5120
	ds_read_b128 v[178:181], v213 offset:6144
	ds_read_b128 v[182:185], v213 offset:7168
	global_load_lds_dwordx4 v162, s[4:5]
	v_add_u32_e32 v162, s55, v208
	s_add_i32 m0, s39, 0xe000
	s_nop 0
	global_load_lds_dwordx4 v162, s[4:5]
	s_waitcnt lgkmcnt(8)
	s_barrier
	s_waitcnt lgkmcnt(0)


	v_mfma_scale_f32_16x16x128_f8f6f4 v[134:137], v[98:105], v[146:153], v[134:137], v214, v214 op_sel_hi:[0,0,0]
	v_mfma_scale_f32_16x16x128_f8f6f4 v[130:133], v[138:145], v[146:153], v[130:133], v214, v214 op_sel_hi:[0,0,0]
	v_mfma_scale_f32_16x16x128_f8f6f4 v[126:129], v[98:105], v[154:161], v[126:129], v214, v214 op_sel_hi:[0,0,0]
	v_mfma_scale_f32_16x16x128_f8f6f4 v[122:125], v[138:145], v[154:161], v[122:125], v214, v214 op_sel_hi:[0,0,0]
	v_mfma_scale_f32_16x16x128_f8f6f4 v[162:165], v[98:105], v[170:177], v[118:121], v214, v214 op_sel_hi:[0,0,0]
	v_mfma_scale_f32_16x16x128_f8f6f4 v[186:189], v[138:145], v[170:177], v[114:117], v214, v214 op_sel_hi:[0,0,0]
	v_mfma_scale_f32_16x16x128_f8f6f4 v[190:193], v[98:105], v[178:185], v[110:113], v214, v214 op_sel_hi:[0,0,0]
	v_mfma_scale_f32_16x16x128_f8f6f4 v[194:197], v[138:145], v[178:185], v[106:109], v214, v214 op_sel_hi:[0,0,0]

	s_barrier
	s_add_i32 s61, s49, s38
	v_add_u32_e32 v198, s58, v1
	s_mov_b32 m0, s61
	s_nop 1
	ds_read_b128 v[106:109], v215
	ds_read_b128 v[110:113], v215 offset:1024
	ds_read_b128 v[114:117], v215 offset:2048
	ds_read_b128 v[118:121], v215 offset:3072
	global_load_lds_dwordx4 v198, s[6:7]
	v_add_u32_e32 v198, s58, v204
	s_add_i32 m0, s61, 0x2000
	s_nop 0
	global_load_lds_dwordx4 v198, s[6:7]
	s_barrier
	s_waitcnt lgkmcnt(0)


	v_mfma_scale_f32_16x16x128_f8f6f4 v[198:201], v[106:113], v[146:153], v[62:65], v214, v214 op_sel_hi:[0,0,0]
	v_mfma_scale_f32_16x16x128_f8f6f4 v[146:149], v[114:121], v[146:153], v[58:61], v214, v214 op_sel_hi:[0,0,0]
	v_mfma_scale_f32_16x16x128_f8f6f4 v[150:153], v[106:113], v[154:161], v[54:57], v214, v214 op_sel_hi:[0,0,0]
	v_mfma_scale_f32_16x16x128_f8f6f4 v[154:157], v[114:121], v[154:161], v[50:53], v214, v214 op_sel_hi:[0,0,0]
	v_mfma_scale_f32_16x16x128_f8f6f4 v[158:161], v[106:113], v[170:177], v[46:49], v214, v214 op_sel_hi:[0,0,0]
	v_mfma_scale_f32_16x16x128_f8f6f4 v[170:173], v[114:121], v[170:177], v[42:45], v214, v214 op_sel_hi:[0,0,0]
	v_mfma_scale_f32_16x16x128_f8f6f4 v[174:177], v[106:113], v[178:185], v[38:41], v214, v214 op_sel_hi:[0,0,0]
	v_mfma_scale_f32_16x16x128_f8f6f4 v[178:181], v[114:121], v[178:185], v[34:37], v214, v214 op_sel_hi:[0,0,0]

	s_mov_b32 m0, s39
	v_add_u32_e32 v182, s60, v205
	s_barrier
	s_nop 2
	ds_read_b128 v[34:37], v213 offset:16384
	ds_read_b128 v[38:41], v213 offset:17408
	ds_read_b128 v[42:45], v213 offset:18432
	ds_read_b128 v[46:49], v213 offset:19456
	ds_read_b128 v[50:53], v213 offset:20480
	ds_read_b128 v[54:57], v213 offset:21504
	ds_read_b128 v[58:61], v213 offset:22528
	ds_read_b128 v[62:65], v213 offset:23552
	global_load_lds_dwordx4 v182, s[4:5]
	v_add_u32_e32 v182, s60, v206
	s_mov_b32 m0, s40
	s_nop 0
	global_load_lds_dwordx4 v182, s[4:5]
	s_barrier
	s_waitcnt lgkmcnt(0)


	v_mfma_scale_f32_16x16x128_f8f6f4 v[94:97], v[98:105], v[34:41], v[94:97], v214, v214 op_sel_hi:[0,0,0]
	v_mfma_scale_f32_16x16x128_f8f6f4 v[90:93], v[138:145], v[34:41], v[90:93], v214, v214 op_sel_hi:[0,0,0]
	v_mfma_scale_f32_16x16x128_f8f6f4 v[86:89], v[98:105], v[42:49], v[86:89], v214, v214 op_sel_hi:[0,0,0]
	v_mfma_scale_f32_16x16x128_f8f6f4 v[82:85], v[138:145], v[42:49], v[82:85], v214, v214 op_sel_hi:[0,0,0]
	v_mfma_scale_f32_16x16x128_f8f6f4 v[78:81], v[98:105], v[50:57], v[78:81], v214, v214 op_sel_hi:[0,0,0]
	v_mfma_scale_f32_16x16x128_f8f6f4 v[74:77], v[138:145], v[50:57], v[74:77], v214, v214 op_sel_hi:[0,0,0]
	v_mfma_scale_f32_16x16x128_f8f6f4 v[182:185], v[98:105], v[58:65], v[70:73], v214, v214 op_sel_hi:[0,0,0]
	v_mfma_scale_f32_16x16x128_f8f6f4 v[216:219], v[138:145], v[58:65], v[66:69], v214, v214 op_sel_hi:[0,0,0]

	s_barrier
	s_add_i32 s61, s58, 0x40000
	s_add_i32 s62, s50, s38
	s_nop 2
	v_add_u32_e32 v66, s61, v1
	s_mov_b32 m0, s62
	s_nop 0
	global_load_lds_dwordx4 v66, s[6:7]
	v_add_u32_e32 v66, s61, v204
	s_add_i32 m0, s62, 0x2000
	s_nop 0
	global_load_lds_dwordx4 v66, s[6:7]
	s_waitcnt vmcnt(6)
	s_barrier

	v_mfma_scale_f32_16x16x128_f8f6f4 v[220:223], v[106:113], v[34:41], v[30:33], v214, v214 op_sel_hi:[0,0,0]
	v_mfma_scale_f32_16x16x128_f8f6f4 v[224:227], v[114:121], v[34:41], v[26:29], v214, v214 op_sel_hi:[0,0,0]
	v_mfma_scale_f32_16x16x128_f8f6f4 v[228:231], v[106:113], v[42:49], v[22:25], v214, v214 op_sel_hi:[0,0,0]
	v_mfma_scale_f32_16x16x128_f8f6f4 v[232:235], v[114:121], v[42:49], v[18:21], v214, v214 op_sel_hi:[0,0,0]
	v_mfma_scale_f32_16x16x128_f8f6f4 v[236:239], v[106:113], v[50:57], v[14:17], v214, v214 op_sel_hi:[0,0,0]
	v_mfma_scale_f32_16x16x128_f8f6f4 v[240:243], v[114:121], v[50:57], v[10:13], v214, v214 op_sel_hi:[0,0,0]
	v_mfma_scale_f32_16x16x128_f8f6f4 v[244:247], v[106:113], v[58:65], v[6:9], v214, v214 op_sel_hi:[0,0,0]
	v_mfma_scale_f32_16x16x128_f8f6f4 v[248:251], v[114:121], v[58:65], v[2:5], v214, v214 op_sel_hi:[0,0,0]

	s_add_i32 s61, 0, 0x18000
	s_nop 1
	v_add_u32_e32 v14, s61, v211
	s_barrier
	s_nop 0
	ds_read_b128 v[2:5], v14
	ds_read_b128 v[6:9], v14 offset:1024
	ds_read_b128 v[10:13], v14 offset:2048
	ds_read_b128 v[14:17], v14 offset:3072
	s_mov_b32 m0, s42
	v_add_u32_e32 v42, s60, v207
	ds_read_b128 v[18:21], v213 offset:32768
	ds_read_b128 v[22:25], v213 offset:33792
	ds_read_b128 v[26:29], v213 offset:34816
	ds_read_b128 v[30:33], v213 offset:35840
	ds_read_b128 v[34:37], v213 offset:36864
	ds_read_b128 v[38:41], v213 offset:37888
	ds_read_b128 v[66:69], v213 offset:38912
	ds_read_b128 v[70:73], v213 offset:39936
	global_load_lds_dwordx4 v42, s[4:5]
	v_add_u32_e32 v42, s60, v208
	s_mov_b32 m0, s43
	s_nop 0
	global_load_lds_dwordx4 v42, s[4:5]
	s_waitcnt lgkmcnt(8)
	s_barrier
	s_waitcnt lgkmcnt(0)


	v_mfma_scale_f32_16x16x128_f8f6f4 v[134:137], v[2:9], v[18:25], v[134:137], v214, v214 op_sel_hi:[0,0,0]
	v_mfma_scale_f32_16x16x128_f8f6f4 v[130:133], v[10:17], v[18:25], v[130:133], v214, v214 op_sel_hi:[0,0,0]
	v_mfma_scale_f32_16x16x128_f8f6f4 v[126:129], v[2:9], v[26:33], v[126:129], v214, v214 op_sel_hi:[0,0,0]
	v_mfma_scale_f32_16x16x128_f8f6f4 v[122:125], v[10:17], v[26:33], v[122:125], v214, v214 op_sel_hi:[0,0,0]
	v_mfma_scale_f32_16x16x128_f8f6f4 v[118:121], v[2:9], v[34:41], v[162:165], v214, v214 op_sel_hi:[0,0,0]
	v_mfma_scale_f32_16x16x128_f8f6f4 v[114:117], v[10:17], v[34:41], v[186:189], v214, v214 op_sel_hi:[0,0,0]
	v_mfma_scale_f32_16x16x128_f8f6f4 v[110:113], v[2:9], v[66:73], v[190:193], v214, v214 op_sel_hi:[0,0,0]
	v_mfma_scale_f32_16x16x128_f8f6f4 v[106:109], v[10:17], v[66:73], v[194:197], v214, v214 op_sel_hi:[0,0,0]

	s_barrier
	s_add_i32 s60, 0, 0x1c000
	v_add_u32_e32 v42, s60, v211
	s_or_b32 s62, s58, 0x80
	s_add_i32 s61, s61, s38
	ds_read_b128 v[98:101], v42
	ds_read_b128 v[102:105], v42 offset:1024
	ds_read_b128 v[138:141], v42 offset:2048
	ds_read_b128 v[142:145], v42 offset:3072
	v_add_u32_e32 v42, s62, v1
	s_mov_b32 m0, s61
	s_nop 0
	global_load_lds_dwordx4 v42, s[6:7]
	v_add_u32_e32 v42, s62, v204
	s_add_i32 m0, s61, 0x2000
	s_nop 0
	global_load_lds_dwordx4 v42, s[6:7]
	s_barrier
	s_waitcnt lgkmcnt(0)


	v_mfma_scale_f32_16x16x128_f8f6f4 v[62:65], v[98:105], v[18:25], v[198:201], v214, v214 op_sel_hi:[0,0,0]
	v_mfma_scale_f32_16x16x128_f8f6f4 v[58:61], v[138:145], v[18:25], v[146:149], v214, v214 op_sel_hi:[0,0,0]
	v_mfma_scale_f32_16x16x128_f8f6f4 v[54:57], v[98:105], v[26:33], v[150:153], v214, v214 op_sel_hi:[0,0,0]
	v_mfma_scale_f32_16x16x128_f8f6f4 v[50:53], v[138:145], v[26:33], v[154:157], v214, v214 op_sel_hi:[0,0,0]
	v_mfma_scale_f32_16x16x128_f8f6f4 v[46:49], v[98:105], v[34:41], v[158:161], v214, v214 op_sel_hi:[0,0,0]
	v_mfma_scale_f32_16x16x128_f8f6f4 v[42:45], v[138:145], v[34:41], v[170:173], v214, v214 op_sel_hi:[0,0,0]
	v_mfma_scale_f32_16x16x128_f8f6f4 v[38:41], v[98:105], v[66:73], v[174:177], v214, v214 op_sel_hi:[0,0,0]
	v_mfma_scale_f32_16x16x128_f8f6f4 v[34:37], v[138:145], v[66:73], v[178:181], v214, v214 op_sel_hi:[0,0,0]

	s_mov_b32 m0, s44
	v_add_u32_e32 v26, s59, v205
	s_barrier
	ds_read_b128 v[18:21], v213 offset:49152
	ds_read_b128 v[22:25], v213 offset:50176
	ds_read_b128 v[146:149], v213 offset:51200
	ds_read_b128 v[150:153], v213 offset:52224
	ds_read_b128 v[154:157], v213 offset:53248
	ds_read_b128 v[158:161], v213 offset:54272
	ds_read_b128 v[170:173], v213 offset:55296
	ds_read_b128 v[174:177], v213 offset:56320
	global_load_lds_dwordx4 v26, s[4:5]
	v_add_u32_e32 v26, s59, v206
	s_mov_b32 m0, s45
	s_nop 0
	global_load_lds_dwordx4 v26, s[4:5]
	s_barrier
	s_waitcnt lgkmcnt(0)


	v_mfma_scale_f32_16x16x128_f8f6f4 v[94:97], v[2:9], v[18:25], v[94:97], v214, v214 op_sel_hi:[0,0,0]
	v_mfma_scale_f32_16x16x128_f8f6f4 v[90:93], v[10:17], v[18:25], v[90:93], v214, v214 op_sel_hi:[0,0,0]
	v_mfma_scale_f32_16x16x128_f8f6f4 v[86:89], v[2:9], v[146:153], v[86:89], v214, v214 op_sel_hi:[0,0,0]
	v_mfma_scale_f32_16x16x128_f8f6f4 v[82:85], v[10:17], v[146:153], v[82:85], v214, v214 op_sel_hi:[0,0,0]
	v_mfma_scale_f32_16x16x128_f8f6f4 v[78:81], v[2:9], v[154:161], v[78:81], v214, v214 op_sel_hi:[0,0,0]
	v_mfma_scale_f32_16x16x128_f8f6f4 v[74:77], v[10:17], v[154:161], v[74:77], v214, v214 op_sel_hi:[0,0,0]
	v_mfma_scale_f32_16x16x128_f8f6f4 v[70:73], v[2:9], v[170:177], v[182:185], v214, v214 op_sel_hi:[0,0,0]
	v_mfma_scale_f32_16x16x128_f8f6f4 v[66:69], v[10:17], v[170:177], v[216:219], v214, v214 op_sel_hi:[0,0,0]

	s_barrier
	s_add_i32 s58, s58, 0x40080
	s_add_i32 s59, s60, s38
	v_add_u32_e32 v2, s58, v1
	s_mov_b32 m0, s59
	s_nop 0
	global_load_lds_dwordx4 v2, s[6:7]
	v_add_u32_e32 v2, s58, v204
	s_add_i32 m0, s59, 0x2000
	s_nop 0
	global_load_lds_dwordx4 v2, s[6:7]
	s_waitcnt vmcnt(6)
	s_barrier

	v_mfma_scale_f32_16x16x128_f8f6f4 v[30:33], v[98:105], v[18:25], v[220:223], v214, v214 op_sel_hi:[0,0,0]
	v_mfma_scale_f32_16x16x128_f8f6f4 v[26:29], v[138:145], v[18:25], v[224:227], v214, v214 op_sel_hi:[0,0,0]
	v_mfma_scale_f32_16x16x128_f8f6f4 v[22:25], v[98:105], v[146:153], v[228:231], v214, v214 op_sel_hi:[0,0,0]
	v_mfma_scale_f32_16x16x128_f8f6f4 v[18:21], v[138:145], v[146:153], v[232:235], v214, v214 op_sel_hi:[0,0,0]
	v_mfma_scale_f32_16x16x128_f8f6f4 v[14:17], v[98:105], v[154:161], v[236:239], v214, v214 op_sel_hi:[0,0,0]
	v_mfma_scale_f32_16x16x128_f8f6f4 v[10:13], v[138:145], v[154:161], v[240:243], v214, v214 op_sel_hi:[0,0,0]
	v_mfma_scale_f32_16x16x128_f8f6f4 v[6:9], v[98:105], v[170:177], v[244:247], v214, v214 op_sel_hi:[0,0,0]
	v_mfma_scale_f32_16x16x128_f8f6f4 v[2:5], v[138:145], v[170:177], v[248:251], v214, v214 op_sel_hi:[0,0,0]

	s_add_i32 s57, s57, 2
	s_addk_i32 s55, 0x100
	s_addk_i32 s56, 0x100
	s_cmp_ge_i32 s57, s46
	s_barrier
	s_cbranch_scc0 .LBB0_2505
	v_readlane_b32 s57, v254, 22
	s_branch .LBB0_2496
